# speedup vs baseline: 1.1440x; 1.0134x over previous
.Lscan_loop_a_st:
	ds_read_b64 v[128:129], v106 offset:96
	ds_read_b64 v[130:131], v106 offset:104
	ds_read_b64 v[132:133], v106 offset:112
	s_waitcnt vmcnt(8)
	global_load_dwordx4 v[146:149], v[196:197], off
	global_load_dwordx4 v[150:153], v[196:197], off offset:512
	global_load_dwordx4 v[154:157], v[196:197], off offset:1024
	v_lshl_add_u64 v[196:197], v[196:197], 0, s[42:43]
	s_waitcnt lgkmcnt(3)
	v_mfma_f32_16x16x128_f8f6f4 v[134:137], v[122:127], v[2:7], 0 cbsz:2 blgp:2
	v_mfma_f32_16x16x128_f8f6f4 v[138:141], v[122:127], v[14:19], 0 cbsz:2 blgp:2
	v_mfma_f32_16x16x128_f8f6f4 v[142:145], v[122:127], v[26:31], v[188:191] cbsz:2 blgp:2
	v_mfma_f32_16x16x128_f8f6f4 v[204:207], v[122:127], v[38:43], 0 cbsz:2 blgp:2
	v_mfma_f32_16x16x128_f8f6f4 v[208:211], v[122:127], v[50:55], 0 cbsz:2 blgp:2
	v_mfma_f32_16x16x128_f8f6f4 v[212:215], v[122:127], v[62:67], v[188:191] cbsz:2 blgp:2
	s_waitcnt lgkmcnt(0)
	v_mfma_f32_16x16x128_f8f6f4 v[134:137], v[128:133], v[8:13], v[134:137] cbsz:2 blgp:2
	v_mfma_f32_16x16x128_f8f6f4 v[204:207], v[128:133], v[44:49], v[204:207] cbsz:2 blgp:2
	v_mfma_f32_16x16x128_f8f6f4 v[138:141], v[128:133], v[20:25], v[138:141] cbsz:2 blgp:2
	v_mfma_f32_16x16x128_f8f6f4 v[208:211], v[128:133], v[56:61], v[208:211] cbsz:2 blgp:2
	v_mfma_f32_16x16x128_f8f6f4 v[142:145], v[128:133], v[32:37], v[142:145] cbsz:2 blgp:2
	v_mfma_f32_16x16x128_f8f6f4 v[212:215], v[128:133], v[68:73], v[212:215] cbsz:2 blgp:2
	v_cndmask_b32_e64 v158, v134, v204, s[4:5]
	v_fma_mix_f32 v158, v158, v1, v82 op_sel_hi:[0,0,1]
	v_exp_f32_e32 v158, v158
	v_cndmask_b32_e64 v159, v138, v208, s[4:5]
	v_fma_mix_f32 v159, v159, v99, v74 op_sel_hi:[0,0,1]
	v_exp_f32_e32 v159, v159
	v_fma_f32 v158, v158, v186, v186
	v_rcp_f32_e32 v158, v158
	v_add_f32_e32 v159, 1.0, v159
	v_rcp_f32_e32 v159, v159
	v_cndmask_b32_e64 v160, v142, v212, s[4:5]
	v_fma_mix_f32 v161, v158, v160, v78 op_sel_hi:[0,0,1]
	v_exp_f32_e32 v161, v161
	s_add_u32 s48, s48, s40
	v_add_f32_e32 v161, 1.0, v161
	v_rcp_f32_e32 v161, v161
	s_addc_u32 s49, s49, s41
	v_fma_f32 v162, v161, -2.0, 1.0
	v_sub_f32_e32 v163, v176, v162
	v_fma_f32 v176, v159, v163, v162
	v_fma_f32 v164, |v176|, s16, v117
	v_fma_f32 v165, |v176|, s17, v118
	v_fma_f32 v166, |v176|, s18, v119
	v_lshrrev_b32_e32 v167, 26, v176
	v_min3_u32 v164, v164, v165, v166
	v_bfi_b32 v168, 31, v164, v167
	s_nop 1
	v_mul_u32_u24_dpp v170, v168, v180 quad_perm:[1,2,3,3] row_mask:0xf bank_mask:0xf bound_ctrl:1
	v_mad_u32_u24 v171, v168, v181, v170
	ds_write_b8_d16_hi v184, v171 offset:416
	global_store_short_d16_hi v185, v176, s[48:49]
	s_waitcnt lgkmcnt(0)
	s_barrier
	ds_read_b64 v[122:123], v106 offset:416
	ds_read_b64 v[124:125], v106 offset:424
	ds_read_b64 v[126:127], v106 offset:432
	s_barrier
	ds_read_b64 v[128:129], v106 offset:512
	ds_read_b64 v[130:131], v106 offset:520
	ds_read_b64 v[132:133], v106 offset:528
	s_waitcnt lgkmcnt(3)
	v_mfma_f32_16x16x128_f8f6f4 v[134:137], v[122:127], v[2:7], 0 cbsz:2 blgp:2
	v_mfma_f32_16x16x128_f8f6f4 v[138:141], v[122:127], v[14:19], 0 cbsz:2 blgp:2
	v_mfma_f32_16x16x128_f8f6f4 v[142:145], v[122:127], v[26:31], v[188:191] cbsz:2 blgp:2
	v_mfma_f32_16x16x128_f8f6f4 v[204:207], v[122:127], v[38:43], 0 cbsz:2 blgp:2
	v_mfma_f32_16x16x128_f8f6f4 v[208:211], v[122:127], v[50:55], 0 cbsz:2 blgp:2
	v_mfma_f32_16x16x128_f8f6f4 v[212:215], v[122:127], v[62:67], v[188:191] cbsz:2 blgp:2
	s_waitcnt lgkmcnt(0)
	v_mfma_f32_16x16x128_f8f6f4 v[134:137], v[128:133], v[8:13], v[134:137] cbsz:2 blgp:2
	v_mfma_f32_16x16x128_f8f6f4 v[204:207], v[128:133], v[44:49], v[204:207] cbsz:2 blgp:2
	v_mfma_f32_16x16x128_f8f6f4 v[138:141], v[128:133], v[20:25], v[138:141] cbsz:2 blgp:2
	v_mfma_f32_16x16x128_f8f6f4 v[208:211], v[128:133], v[56:61], v[208:211] cbsz:2 blgp:2
	v_mfma_f32_16x16x128_f8f6f4 v[142:145], v[128:133], v[32:37], v[142:145] cbsz:2 blgp:2
	v_mfma_f32_16x16x128_f8f6f4 v[212:215], v[128:133], v[68:73], v[212:215] cbsz:2 blgp:2
	v_cndmask_b32_e64 v158, v134, v204, s[4:5]
	v_fma_mix_f32 v158, v158, v1, v82 op_sel:[0,0,1] op_sel_hi:[0,0,1]
	v_exp_f32_e32 v158, v158
	v_cndmask_b32_e64 v159, v138, v208, s[4:5]
	v_fma_mix_f32 v159, v159, v99, v74 op_sel:[0,0,1] op_sel_hi:[0,0,1]
	v_exp_f32_e32 v159, v159
	v_fma_f32 v158, v158, v186, v186
	v_rcp_f32_e32 v158, v158
	v_add_f32_e32 v159, 1.0, v159
	v_rcp_f32_e32 v159, v159
	v_cndmask_b32_e64 v160, v142, v212, s[4:5]
	v_fma_mix_f32 v161, v158, v160, v78 op_sel:[0,0,1] op_sel_hi:[0,0,1]
	v_exp_f32_e32 v161, v161
	s_add_u32 s48, s48, s40
	v_add_f32_e32 v161, 1.0, v161
	v_rcp_f32_e32 v161, v161
	s_addc_u32 s49, s49, s41
	v_fma_f32 v162, v161, -2.0, 1.0
	v_sub_f32_e32 v163, v176, v162
	v_fma_f32 v176, v159, v163, v162
	v_fma_f32 v164, |v176|, s16, v117
	v_fma_f32 v165, |v176|, s17, v118
	v_fma_f32 v166, |v176|, s18, v119
	v_lshrrev_b32_e32 v167, 26, v176
	v_min3_u32 v164, v164, v165, v166
	v_bfi_b32 v168, 31, v164, v167
	s_nop 1
	v_mul_u32_u24_dpp v170, v168, v180 quad_perm:[1,2,3,3] row_mask:0xf bank_mask:0xf bound_ctrl:1
	v_mad_u32_u24 v171, v168, v181, v170
	ds_write_b8_d16_hi v184, v171
	global_store_short_d16_hi v185, v176, s[48:49]
	s_waitcnt lgkmcnt(0)
	s_barrier
	ds_read_b64 v[122:123], v106 offset:0
	ds_read_b64 v[124:125], v106 offset:8
	ds_read_b64 v[126:127], v106 offset:16
	s_barrier
	ds_read_b64 v[128:129], v106 offset:96
	ds_read_b64 v[130:131], v106 offset:104
	ds_read_b64 v[132:133], v106 offset:112
	s_waitcnt lgkmcnt(3)
	v_mfma_f32_16x16x128_f8f6f4 v[134:137], v[122:127], v[2:7], 0 cbsz:2 blgp:2
	v_mfma_f32_16x16x128_f8f6f4 v[138:141], v[122:127], v[14:19], 0 cbsz:2 blgp:2
	v_mfma_f32_16x16x128_f8f6f4 v[142:145], v[122:127], v[26:31], v[188:191] cbsz:2 blgp:2
	v_mfma_f32_16x16x128_f8f6f4 v[204:207], v[122:127], v[38:43], 0 cbsz:2 blgp:2
	v_mfma_f32_16x16x128_f8f6f4 v[208:211], v[122:127], v[50:55], 0 cbsz:2 blgp:2
	v_mfma_f32_16x16x128_f8f6f4 v[212:215], v[122:127], v[62:67], v[188:191] cbsz:2 blgp:2
	s_waitcnt lgkmcnt(0)
	v_mfma_f32_16x16x128_f8f6f4 v[134:137], v[128:133], v[8:13], v[134:137] cbsz:2 blgp:2
	v_mfma_f32_16x16x128_f8f6f4 v[204:207], v[128:133], v[44:49], v[204:207] cbsz:2 blgp:2
	v_mfma_f32_16x16x128_f8f6f4 v[138:141], v[128:133], v[20:25], v[138:141] cbsz:2 blgp:2
	v_mfma_f32_16x16x128_f8f6f4 v[208:211], v[128:133], v[56:61], v[208:211] cbsz:2 blgp:2
	v_mfma_f32_16x16x128_f8f6f4 v[142:145], v[128:133], v[32:37], v[142:145] cbsz:2 blgp:2
	v_mfma_f32_16x16x128_f8f6f4 v[212:215], v[128:133], v[68:73], v[212:215] cbsz:2 blgp:2
	v_cndmask_b32_e64 v158, v134, v204, s[4:5]
	v_fma_mix_f32 v158, v158, v1, v83 op_sel_hi:[0,0,1]
	v_exp_f32_e32 v158, v158
	v_cndmask_b32_e64 v159, v138, v208, s[4:5]
	v_fma_mix_f32 v159, v159, v99, v75 op_sel_hi:[0,0,1]
	v_exp_f32_e32 v159, v159
	v_fma_f32 v158, v158, v186, v186
	v_rcp_f32_e32 v158, v158
	v_add_f32_e32 v159, 1.0, v159
	v_rcp_f32_e32 v159, v159
	v_cndmask_b32_e64 v160, v142, v212, s[4:5]
	v_fma_mix_f32 v161, v158, v160, v79 op_sel_hi:[0,0,1]
	v_exp_f32_e32 v161, v161
	s_add_u32 s48, s48, s40
	v_add_f32_e32 v161, 1.0, v161
	v_rcp_f32_e32 v161, v161
	s_addc_u32 s49, s49, s41
	v_fma_f32 v162, v161, -2.0, 1.0
	v_sub_f32_e32 v163, v176, v162
	v_fma_f32 v176, v159, v163, v162
	v_fma_f32 v164, |v176|, s16, v117
	v_fma_f32 v165, |v176|, s17, v118
	v_fma_f32 v166, |v176|, s18, v119
	v_lshrrev_b32_e32 v167, 26, v176
	v_min3_u32 v164, v164, v165, v166
	v_bfi_b32 v168, 31, v164, v167
	s_nop 1
	v_mul_u32_u24_dpp v170, v168, v180 quad_perm:[1,2,3,3] row_mask:0xf bank_mask:0xf bound_ctrl:1
	v_mad_u32_u24 v171, v168, v181, v170
	ds_write_b8_d16_hi v184, v171 offset:416
	global_store_short_d16_hi v185, v176, s[48:49]
	s_waitcnt lgkmcnt(0)
	s_barrier
	ds_read_b64 v[122:123], v106 offset:416
	ds_read_b64 v[124:125], v106 offset:424
	ds_read_b64 v[126:127], v106 offset:432
	s_barrier
	ds_read_b64 v[128:129], v106 offset:512
	ds_read_b64 v[130:131], v106 offset:520
	ds_read_b64 v[132:133], v106 offset:528
	s_waitcnt lgkmcnt(3)
	v_mfma_f32_16x16x128_f8f6f4 v[134:137], v[122:127], v[2:7], 0 cbsz:2 blgp:2
	v_mfma_f32_16x16x128_f8f6f4 v[138:141], v[122:127], v[14:19], 0 cbsz:2 blgp:2
	v_mfma_f32_16x16x128_f8f6f4 v[142:145], v[122:127], v[26:31], v[188:191] cbsz:2 blgp:2
	v_mfma_f32_16x16x128_f8f6f4 v[204:207], v[122:127], v[38:43], 0 cbsz:2 blgp:2
	v_mfma_f32_16x16x128_f8f6f4 v[208:211], v[122:127], v[50:55], 0 cbsz:2 blgp:2
	v_mfma_f32_16x16x128_f8f6f4 v[212:215], v[122:127], v[62:67], v[188:191] cbsz:2 blgp:2
	s_waitcnt lgkmcnt(0)
	v_mfma_f32_16x16x128_f8f6f4 v[134:137], v[128:133], v[8:13], v[134:137] cbsz:2 blgp:2
	v_mfma_f32_16x16x128_f8f6f4 v[204:207], v[128:133], v[44:49], v[204:207] cbsz:2 blgp:2
	v_mfma_f32_16x16x128_f8f6f4 v[138:141], v[128:133], v[20:25], v[138:141] cbsz:2 blgp:2
	v_mfma_f32_16x16x128_f8f6f4 v[208:211], v[128:133], v[56:61], v[208:211] cbsz:2 blgp:2
	v_mfma_f32_16x16x128_f8f6f4 v[142:145], v[128:133], v[32:37], v[142:145] cbsz:2 blgp:2
	v_mfma_f32_16x16x128_f8f6f4 v[212:215], v[128:133], v[68:73], v[212:215] cbsz:2 blgp:2
	v_cndmask_b32_e64 v158, v134, v204, s[4:5]
	v_fma_mix_f32 v158, v158, v1, v83 op_sel:[0,0,1] op_sel_hi:[0,0,1]
	v_exp_f32_e32 v158, v158
	v_cndmask_b32_e64 v159, v138, v208, s[4:5]
	v_fma_mix_f32 v159, v159, v99, v75 op_sel:[0,0,1] op_sel_hi:[0,0,1]
	v_exp_f32_e32 v159, v159
	v_fma_f32 v158, v158, v186, v186
	v_rcp_f32_e32 v158, v158
	v_add_f32_e32 v159, 1.0, v159
	v_rcp_f32_e32 v159, v159
	v_cndmask_b32_e64 v160, v142, v212, s[4:5]
	v_fma_mix_f32 v161, v158, v160, v79 op_sel:[0,0,1] op_sel_hi:[0,0,1]
	v_exp_f32_e32 v161, v161
	s_add_u32 s48, s48, s40
	v_add_f32_e32 v161, 1.0, v161
	v_rcp_f32_e32 v161, v161
	s_addc_u32 s49, s49, s41
	v_fma_f32 v162, v161, -2.0, 1.0
	v_sub_f32_e32 v163, v176, v162
	v_fma_f32 v176, v159, v163, v162
	v_fma_f32 v164, |v176|, s16, v117
	v_fma_f32 v165, |v176|, s17, v118
	v_fma_f32 v166, |v176|, s18, v119
	v_lshrrev_b32_e32 v167, 26, v176
	v_min3_u32 v164, v164, v165, v166
	v_bfi_b32 v168, 31, v164, v167
	s_nop 1
	v_mul_u32_u24_dpp v170, v168, v180 quad_perm:[1,2,3,3] row_mask:0xf bank_mask:0xf bound_ctrl:1
	v_mad_u32_u24 v171, v168, v181, v170
	ds_write_b8_d16_hi v184, v171
	global_store_short_d16_hi v185, v176, s[48:49]
	s_waitcnt lgkmcnt(0)
	s_barrier
	ds_read_b64 v[122:123], v106 offset:0
	ds_read_b64 v[124:125], v106 offset:8
	ds_read_b64 v[126:127], v106 offset:16
	s_barrier
	ds_read_b64 v[128:129], v106 offset:96
	ds_read_b64 v[130:131], v106 offset:104
	ds_read_b64 v[132:133], v106 offset:112
	s_waitcnt lgkmcnt(3)
	v_mfma_f32_16x16x128_f8f6f4 v[134:137], v[122:127], v[2:7], 0 cbsz:2 blgp:2
	v_mfma_f32_16x16x128_f8f6f4 v[138:141], v[122:127], v[14:19], 0 cbsz:2 blgp:2
	v_mfma_f32_16x16x128_f8f6f4 v[142:145], v[122:127], v[26:31], v[188:191] cbsz:2 blgp:2
	v_mfma_f32_16x16x128_f8f6f4 v[204:207], v[122:127], v[38:43], 0 cbsz:2 blgp:2
	v_mfma_f32_16x16x128_f8f6f4 v[208:211], v[122:127], v[50:55], 0 cbsz:2 blgp:2
	v_mfma_f32_16x16x128_f8f6f4 v[212:215], v[122:127], v[62:67], v[188:191] cbsz:2 blgp:2
	s_waitcnt lgkmcnt(0)
	v_mfma_f32_16x16x128_f8f6f4 v[134:137], v[128:133], v[8:13], v[134:137] cbsz:2 blgp:2
	v_mfma_f32_16x16x128_f8f6f4 v[204:207], v[128:133], v[44:49], v[204:207] cbsz:2 blgp:2
	v_mfma_f32_16x16x128_f8f6f4 v[138:141], v[128:133], v[20:25], v[138:141] cbsz:2 blgp:2
	v_mfma_f32_16x16x128_f8f6f4 v[208:211], v[128:133], v[56:61], v[208:211] cbsz:2 blgp:2
	v_mfma_f32_16x16x128_f8f6f4 v[142:145], v[128:133], v[32:37], v[142:145] cbsz:2 blgp:2
	v_mfma_f32_16x16x128_f8f6f4 v[212:215], v[128:133], v[68:73], v[212:215] cbsz:2 blgp:2
	v_cndmask_b32_e64 v158, v134, v204, s[4:5]
	v_fma_mix_f32 v158, v158, v1, v84 op_sel_hi:[0,0,1]
	v_exp_f32_e32 v158, v158
	v_cndmask_b32_e64 v159, v138, v208, s[4:5]
	v_fma_mix_f32 v159, v159, v99, v76 op_sel_hi:[0,0,1]
	v_exp_f32_e32 v159, v159
	v_fma_f32 v158, v158, v186, v186
	v_rcp_f32_e32 v158, v158
	v_add_f32_e32 v159, 1.0, v159
	v_rcp_f32_e32 v159, v159
	v_cndmask_b32_e64 v160, v142, v212, s[4:5]
	v_fma_mix_f32 v161, v158, v160, v80 op_sel_hi:[0,0,1]
	v_exp_f32_e32 v161, v161
	s_add_u32 s48, s48, s40
	v_add_f32_e32 v161, 1.0, v161
	v_rcp_f32_e32 v161, v161
	s_addc_u32 s49, s49, s41
	v_fma_f32 v162, v161, -2.0, 1.0
	v_sub_f32_e32 v163, v176, v162
	v_fma_f32 v176, v159, v163, v162
	v_fma_f32 v164, |v176|, s16, v117
	v_fma_f32 v165, |v176|, s17, v118
	v_fma_f32 v166, |v176|, s18, v119
	v_lshrrev_b32_e32 v167, 26, v176
	v_min3_u32 v164, v164, v165, v166
	v_bfi_b32 v168, 31, v164, v167
	s_nop 1
	v_mul_u32_u24_dpp v170, v168, v180 quad_perm:[1,2,3,3] row_mask:0xf bank_mask:0xf bound_ctrl:1
	v_mad_u32_u24 v171, v168, v181, v170
	ds_write_b8_d16_hi v184, v171 offset:416
	global_store_short_d16_hi v185, v176, s[48:49]
	s_waitcnt lgkmcnt(0)
	s_barrier
	ds_read_b64 v[122:123], v106 offset:416
	ds_read_b64 v[124:125], v106 offset:424
	ds_read_b64 v[126:127], v106 offset:432
	s_barrier
	ds_read_b64 v[128:129], v106 offset:512
	ds_read_b64 v[130:131], v106 offset:520
	ds_read_b64 v[132:133], v106 offset:528
	s_waitcnt lgkmcnt(3)
	v_mfma_f32_16x16x128_f8f6f4 v[134:137], v[122:127], v[2:7], 0 cbsz:2 blgp:2
	v_mfma_f32_16x16x128_f8f6f4 v[138:141], v[122:127], v[14:19], 0 cbsz:2 blgp:2
	v_mfma_f32_16x16x128_f8f6f4 v[142:145], v[122:127], v[26:31], v[188:191] cbsz:2 blgp:2
	v_mfma_f32_16x16x128_f8f6f4 v[204:207], v[122:127], v[38:43], 0 cbsz:2 blgp:2
	v_mfma_f32_16x16x128_f8f6f4 v[208:211], v[122:127], v[50:55], 0 cbsz:2 blgp:2
	v_mfma_f32_16x16x128_f8f6f4 v[212:215], v[122:127], v[62:67], v[188:191] cbsz:2 blgp:2
	s_waitcnt lgkmcnt(0)
	v_mfma_f32_16x16x128_f8f6f4 v[134:137], v[128:133], v[8:13], v[134:137] cbsz:2 blgp:2
	v_mfma_f32_16x16x128_f8f6f4 v[204:207], v[128:133], v[44:49], v[204:207] cbsz:2 blgp:2
	v_mfma_f32_16x16x128_f8f6f4 v[138:141], v[128:133], v[20:25], v[138:141] cbsz:2 blgp:2
	v_mfma_f32_16x16x128_f8f6f4 v[208:211], v[128:133], v[56:61], v[208:211] cbsz:2 blgp:2
	v_mfma_f32_16x16x128_f8f6f4 v[142:145], v[128:133], v[32:37], v[142:145] cbsz:2 blgp:2
	v_mfma_f32_16x16x128_f8f6f4 v[212:215], v[128:133], v[68:73], v[212:215] cbsz:2 blgp:2
	v_cndmask_b32_e64 v158, v134, v204, s[4:5]
	v_fma_mix_f32 v158, v158, v1, v84 op_sel:[0,0,1] op_sel_hi:[0,0,1]
	v_exp_f32_e32 v158, v158
	v_cndmask_b32_e64 v159, v138, v208, s[4:5]
	v_fma_mix_f32 v159, v159, v99, v76 op_sel:[0,0,1] op_sel_hi:[0,0,1]
	v_exp_f32_e32 v159, v159
	v_fma_f32 v158, v158, v186, v186
	v_rcp_f32_e32 v158, v158
	v_add_f32_e32 v159, 1.0, v159
	v_rcp_f32_e32 v159, v159
	v_cndmask_b32_e64 v160, v142, v212, s[4:5]
	v_fma_mix_f32 v161, v158, v160, v80 op_sel:[0,0,1] op_sel_hi:[0,0,1]
	v_exp_f32_e32 v161, v161
	s_add_u32 s48, s48, s40
	v_add_f32_e32 v161, 1.0, v161
	v_rcp_f32_e32 v161, v161
	s_addc_u32 s49, s49, s41
	v_fma_f32 v162, v161, -2.0, 1.0
	v_sub_f32_e32 v163, v176, v162
	v_fma_f32 v176, v159, v163, v162
	v_fma_f32 v164, |v176|, s16, v117
	v_fma_f32 v165, |v176|, s17, v118
	v_fma_f32 v166, |v176|, s18, v119
	v_lshrrev_b32_e32 v167, 26, v176
	v_min3_u32 v164, v164, v165, v166
	v_bfi_b32 v168, 31, v164, v167
	s_nop 1
	v_mul_u32_u24_dpp v170, v168, v180 quad_perm:[1,2,3,3] row_mask:0xf bank_mask:0xf bound_ctrl:1
	v_mad_u32_u24 v171, v168, v181, v170
	ds_write_b8_d16_hi v184, v171
	global_store_short_d16_hi v185, v176, s[48:49]
	s_waitcnt lgkmcnt(0)
	s_barrier
	ds_read_b64 v[122:123], v106 offset:0
	ds_read_b64 v[124:125], v106 offset:8
	ds_read_b64 v[126:127], v106 offset:16
	s_barrier
	ds_read_b64 v[128:129], v106 offset:96
	ds_read_b64 v[130:131], v106 offset:104
	ds_read_b64 v[132:133], v106 offset:112
	s_waitcnt lgkmcnt(3)
	v_mfma_f32_16x16x128_f8f6f4 v[134:137], v[122:127], v[2:7], 0 cbsz:2 blgp:2
	v_mfma_f32_16x16x128_f8f6f4 v[138:141], v[122:127], v[14:19], 0 cbsz:2 blgp:2
	v_mfma_f32_16x16x128_f8f6f4 v[142:145], v[122:127], v[26:31], v[188:191] cbsz:2 blgp:2
	v_mfma_f32_16x16x128_f8f6f4 v[204:207], v[122:127], v[38:43], 0 cbsz:2 blgp:2
	v_mfma_f32_16x16x128_f8f6f4 v[208:211], v[122:127], v[50:55], 0 cbsz:2 blgp:2
	v_mfma_f32_16x16x128_f8f6f4 v[212:215], v[122:127], v[62:67], v[188:191] cbsz:2 blgp:2
	s_waitcnt lgkmcnt(0)
	v_mfma_f32_16x16x128_f8f6f4 v[134:137], v[128:133], v[8:13], v[134:137] cbsz:2 blgp:2
	v_mfma_f32_16x16x128_f8f6f4 v[204:207], v[128:133], v[44:49], v[204:207] cbsz:2 blgp:2
	v_mfma_f32_16x16x128_f8f6f4 v[138:141], v[128:133], v[20:25], v[138:141] cbsz:2 blgp:2
	v_mfma_f32_16x16x128_f8f6f4 v[208:211], v[128:133], v[56:61], v[208:211] cbsz:2 blgp:2
	v_mfma_f32_16x16x128_f8f6f4 v[142:145], v[128:133], v[32:37], v[142:145] cbsz:2 blgp:2
	v_mfma_f32_16x16x128_f8f6f4 v[212:215], v[128:133], v[68:73], v[212:215] cbsz:2 blgp:2
	v_cndmask_b32_e64 v158, v134, v204, s[4:5]
	v_fma_mix_f32 v158, v158, v1, v85 op_sel_hi:[0,0,1]
	v_exp_f32_e32 v158, v158
	v_cndmask_b32_e64 v159, v138, v208, s[4:5]
	v_fma_mix_f32 v159, v159, v99, v77 op_sel_hi:[0,0,1]
	v_exp_f32_e32 v159, v159
	v_fma_f32 v158, v158, v186, v186
	v_rcp_f32_e32 v158, v158
	v_add_f32_e32 v159, 1.0, v159
	v_rcp_f32_e32 v159, v159
	v_cndmask_b32_e64 v160, v142, v212, s[4:5]
	v_fma_mix_f32 v161, v158, v160, v81 op_sel_hi:[0,0,1]
	v_exp_f32_e32 v161, v161
	s_add_u32 s48, s48, s40
	v_add_f32_e32 v161, 1.0, v161
	v_rcp_f32_e32 v161, v161
	s_addc_u32 s49, s49, s41
	v_fma_f32 v162, v161, -2.0, 1.0
	v_sub_f32_e32 v163, v176, v162
	v_fma_f32 v176, v159, v163, v162
	v_fma_f32 v164, |v176|, s16, v117
	v_fma_f32 v165, |v176|, s17, v118
	v_fma_f32 v166, |v176|, s18, v119
	v_lshrrev_b32_e32 v167, 26, v176
	v_min3_u32 v164, v164, v165, v166
	v_bfi_b32 v168, 31, v164, v167
	s_nop 1
	v_mul_u32_u24_dpp v170, v168, v180 quad_perm:[1,2,3,3] row_mask:0xf bank_mask:0xf bound_ctrl:1
	v_mad_u32_u24 v171, v168, v181, v170
	ds_write_b8_d16_hi v184, v171 offset:416
	global_store_short_d16_hi v185, v176, s[48:49]
	s_waitcnt lgkmcnt(0)
	s_barrier
	ds_read_b64 v[122:123], v106 offset:416
	ds_read_b64 v[124:125], v106 offset:424
	ds_read_b64 v[126:127], v106 offset:432
	s_barrier
	ds_read_b64 v[128:129], v106 offset:512
	ds_read_b64 v[130:131], v106 offset:520
	ds_read_b64 v[132:133], v106 offset:528
	s_waitcnt lgkmcnt(3)
	v_mfma_f32_16x16x128_f8f6f4 v[134:137], v[122:127], v[2:7], 0 cbsz:2 blgp:2
	v_mfma_f32_16x16x128_f8f6f4 v[138:141], v[122:127], v[14:19], 0 cbsz:2 blgp:2
	v_mfma_f32_16x16x128_f8f6f4 v[142:145], v[122:127], v[26:31], v[188:191] cbsz:2 blgp:2
	v_mfma_f32_16x16x128_f8f6f4 v[204:207], v[122:127], v[38:43], 0 cbsz:2 blgp:2
	v_mfma_f32_16x16x128_f8f6f4 v[208:211], v[122:127], v[50:55], 0 cbsz:2 blgp:2
	v_mfma_f32_16x16x128_f8f6f4 v[212:215], v[122:127], v[62:67], v[188:191] cbsz:2 blgp:2
	s_waitcnt lgkmcnt(0)
	v_mfma_f32_16x16x128_f8f6f4 v[134:137], v[128:133], v[8:13], v[134:137] cbsz:2 blgp:2
	v_mfma_f32_16x16x128_f8f6f4 v[204:207], v[128:133], v[44:49], v[204:207] cbsz:2 blgp:2
	v_mfma_f32_16x16x128_f8f6f4 v[138:141], v[128:133], v[20:25], v[138:141] cbsz:2 blgp:2
	v_mfma_f32_16x16x128_f8f6f4 v[208:211], v[128:133], v[56:61], v[208:211] cbsz:2 blgp:2
	v_mfma_f32_16x16x128_f8f6f4 v[142:145], v[128:133], v[32:37], v[142:145] cbsz:2 blgp:2
	v_mfma_f32_16x16x128_f8f6f4 v[212:215], v[128:133], v[68:73], v[212:215] cbsz:2 blgp:2
	v_cndmask_b32_e64 v158, v134, v204, s[4:5]
	v_fma_mix_f32 v158, v158, v1, v85 op_sel:[0,0,1] op_sel_hi:[0,0,1]
	v_exp_f32_e32 v158, v158
	v_cndmask_b32_e64 v159, v138, v208, s[4:5]
	v_fma_mix_f32 v159, v159, v99, v77 op_sel:[0,0,1] op_sel_hi:[0,0,1]
	v_exp_f32_e32 v159, v159
	v_fma_f32 v158, v158, v186, v186
	v_rcp_f32_e32 v158, v158
	v_add_f32_e32 v159, 1.0, v159
	v_rcp_f32_e32 v159, v159
	v_cndmask_b32_e64 v160, v142, v212, s[4:5]
	v_fma_mix_f32 v161, v158, v160, v81 op_sel:[0,0,1] op_sel_hi:[0,0,1]
	v_exp_f32_e32 v161, v161
	s_add_u32 s48, s48, s40
	v_add_f32_e32 v161, 1.0, v161
	v_rcp_f32_e32 v161, v161
	s_addc_u32 s49, s49, s41
	v_fma_f32 v162, v161, -2.0, 1.0
	v_sub_f32_e32 v163, v176, v162
	v_fma_f32 v176, v159, v163, v162
	v_fma_f32 v164, |v176|, s16, v117
	v_fma_f32 v165, |v176|, s17, v118
	v_fma_f32 v166, |v176|, s18, v119
	v_lshrrev_b32_e32 v167, 26, v176
	v_min3_u32 v164, v164, v165, v166
	v_bfi_b32 v168, 31, v164, v167
	s_nop 1
	v_mul_u32_u24_dpp v170, v168, v180 quad_perm:[1,2,3,3] row_mask:0xf bank_mask:0xf bound_ctrl:1
	v_mad_u32_u24 v171, v168, v181, v170
	ds_write_b8_d16_hi v184, v171
	global_store_short_d16_hi v185, v176, s[48:49]
	s_waitcnt lgkmcnt(0)
	s_barrier
	ds_read_b64 v[122:123], v106 offset:0
	ds_read_b64 v[124:125], v106 offset:8
	ds_read_b64 v[126:127], v106 offset:16
	s_barrier
	ds_read_b64 v[128:129], v106 offset:96
	ds_read_b64 v[130:131], v106 offset:104
	ds_read_b64 v[132:133], v106 offset:112
	s_waitcnt vmcnt(8)
	global_load_dwordx4 v[82:85], v[196:197], off
	global_load_dwordx4 v[74:77], v[196:197], off offset:512
	global_load_dwordx4 v[78:81], v[196:197], off offset:1024
	v_lshl_add_u64 v[196:197], v[196:197], 0, s[42:43]
	s_waitcnt lgkmcnt(3)
	v_mfma_f32_16x16x128_f8f6f4 v[134:137], v[122:127], v[2:7], 0 cbsz:2 blgp:2
	v_mfma_f32_16x16x128_f8f6f4 v[138:141], v[122:127], v[14:19], 0 cbsz:2 blgp:2
	v_mfma_f32_16x16x128_f8f6f4 v[142:145], v[122:127], v[26:31], v[188:191] cbsz:2 blgp:2
	v_mfma_f32_16x16x128_f8f6f4 v[204:207], v[122:127], v[38:43], 0 cbsz:2 blgp:2
	v_mfma_f32_16x16x128_f8f6f4 v[208:211], v[122:127], v[50:55], 0 cbsz:2 blgp:2
	v_mfma_f32_16x16x128_f8f6f4 v[212:215], v[122:127], v[62:67], v[188:191] cbsz:2 blgp:2
	s_waitcnt lgkmcnt(0)
	v_mfma_f32_16x16x128_f8f6f4 v[134:137], v[128:133], v[8:13], v[134:137] cbsz:2 blgp:2
	v_mfma_f32_16x16x128_f8f6f4 v[204:207], v[128:133], v[44:49], v[204:207] cbsz:2 blgp:2
	v_mfma_f32_16x16x128_f8f6f4 v[138:141], v[128:133], v[20:25], v[138:141] cbsz:2 blgp:2
	v_mfma_f32_16x16x128_f8f6f4 v[208:211], v[128:133], v[56:61], v[208:211] cbsz:2 blgp:2
	v_mfma_f32_16x16x128_f8f6f4 v[142:145], v[128:133], v[32:37], v[142:145] cbsz:2 blgp:2
	v_mfma_f32_16x16x128_f8f6f4 v[212:215], v[128:133], v[68:73], v[212:215] cbsz:2 blgp:2
	v_cndmask_b32_e64 v158, v134, v204, s[4:5]
	v_fma_mix_f32 v158, v158, v1, v146 op_sel_hi:[0,0,1]
	v_exp_f32_e32 v158, v158
	v_cndmask_b32_e64 v159, v138, v208, s[4:5]
	v_fma_mix_f32 v159, v159, v99, v150 op_sel_hi:[0,0,1]
	v_exp_f32_e32 v159, v159
	v_fma_f32 v158, v158, v186, v186
	v_rcp_f32_e32 v158, v158
	v_add_f32_e32 v159, 1.0, v159
	v_rcp_f32_e32 v159, v159
	v_cndmask_b32_e64 v160, v142, v212, s[4:5]
	v_fma_mix_f32 v161, v158, v160, v154 op_sel_hi:[0,0,1]
	v_exp_f32_e32 v161, v161
	s_add_u32 s48, s48, s40
	v_add_f32_e32 v161, 1.0, v161
	v_rcp_f32_e32 v161, v161
	s_addc_u32 s49, s49, s41
	v_fma_f32 v162, v161, -2.0, 1.0
	v_sub_f32_e32 v163, v176, v162
	v_fma_f32 v176, v159, v163, v162
	v_fma_f32 v164, |v176|, s16, v117
	v_fma_f32 v165, |v176|, s17, v118
	v_fma_f32 v166, |v176|, s18, v119
	v_lshrrev_b32_e32 v167, 26, v176
	v_min3_u32 v164, v164, v165, v166
	v_bfi_b32 v168, 31, v164, v167
	s_nop 1
	v_mul_u32_u24_dpp v170, v168, v180 quad_perm:[1,2,3,3] row_mask:0xf bank_mask:0xf bound_ctrl:1
	v_mad_u32_u24 v171, v168, v181, v170
	ds_write_b8_d16_hi v184, v171 offset:416
	global_store_short_d16_hi v185, v176, s[48:49]
	s_waitcnt lgkmcnt(0)
	s_barrier
	ds_read_b64 v[122:123], v106 offset:416
	ds_read_b64 v[124:125], v106 offset:424
	ds_read_b64 v[126:127], v106 offset:432
	s_barrier
	ds_read_b64 v[128:129], v106 offset:512
	ds_read_b64 v[130:131], v106 offset:520
	ds_read_b64 v[132:133], v106 offset:528
	s_waitcnt lgkmcnt(3)
	v_mfma_f32_16x16x128_f8f6f4 v[134:137], v[122:127], v[2:7], 0 cbsz:2 blgp:2
	v_mfma_f32_16x16x128_f8f6f4 v[138:141], v[122:127], v[14:19], 0 cbsz:2 blgp:2
	v_mfma_f32_16x16x128_f8f6f4 v[142:145], v[122:127], v[26:31], v[188:191] cbsz:2 blgp:2
	v_mfma_f32_16x16x128_f8f6f4 v[204:207], v[122:127], v[38:43], 0 cbsz:2 blgp:2
	v_mfma_f32_16x16x128_f8f6f4 v[208:211], v[122:127], v[50:55], 0 cbsz:2 blgp:2
	v_mfma_f32_16x16x128_f8f6f4 v[212:215], v[122:127], v[62:67], v[188:191] cbsz:2 blgp:2
	s_waitcnt lgkmcnt(0)
	v_mfma_f32_16x16x128_f8f6f4 v[134:137], v[128:133], v[8:13], v[134:137] cbsz:2 blgp:2
	v_mfma_f32_16x16x128_f8f6f4 v[204:207], v[128:133], v[44:49], v[204:207] cbsz:2 blgp:2
	v_mfma_f32_16x16x128_f8f6f4 v[138:141], v[128:133], v[20:25], v[138:141] cbsz:2 blgp:2
	v_mfma_f32_16x16x128_f8f6f4 v[208:211], v[128:133], v[56:61], v[208:211] cbsz:2 blgp:2
	v_mfma_f32_16x16x128_f8f6f4 v[142:145], v[128:133], v[32:37], v[142:145] cbsz:2 blgp:2
	v_mfma_f32_16x16x128_f8f6f4 v[212:215], v[128:133], v[68:73], v[212:215] cbsz:2 blgp:2
	v_cndmask_b32_e64 v158, v134, v204, s[4:5]
	v_fma_mix_f32 v158, v158, v1, v146 op_sel:[0,0,1] op_sel_hi:[0,0,1]
	v_exp_f32_e32 v158, v158
	v_cndmask_b32_e64 v159, v138, v208, s[4:5]
	v_fma_mix_f32 v159, v159, v99, v150 op_sel:[0,0,1] op_sel_hi:[0,0,1]
	v_exp_f32_e32 v159, v159
	v_fma_f32 v158, v158, v186, v186
	v_rcp_f32_e32 v158, v158
	v_add_f32_e32 v159, 1.0, v159
	v_rcp_f32_e32 v159, v159
	v_cndmask_b32_e64 v160, v142, v212, s[4:5]
	v_fma_mix_f32 v161, v158, v160, v154 op_sel:[0,0,1] op_sel_hi:[0,0,1]
	v_exp_f32_e32 v161, v161
	s_add_u32 s48, s48, s40
	v_add_f32_e32 v161, 1.0, v161
	v_rcp_f32_e32 v161, v161
	s_addc_u32 s49, s49, s41
	v_fma_f32 v162, v161, -2.0, 1.0
	v_sub_f32_e32 v163, v176, v162
	v_fma_f32 v176, v159, v163, v162
	v_fma_f32 v164, |v176|, s16, v117
	v_fma_f32 v165, |v176|, s17, v118
	v_fma_f32 v166, |v176|, s18, v119
	v_lshrrev_b32_e32 v167, 26, v176
	v_min3_u32 v164, v164, v165, v166
	v_bfi_b32 v168, 31, v164, v167
	s_nop 1
	v_mul_u32_u24_dpp v170, v168, v180 quad_perm:[1,2,3,3] row_mask:0xf bank_mask:0xf bound_ctrl:1
	v_mad_u32_u24 v171, v168, v181, v170
	ds_write_b8_d16_hi v184, v171
	global_store_short_d16_hi v185, v176, s[48:49]
	s_waitcnt lgkmcnt(0)
	s_barrier
	ds_read_b64 v[122:123], v106 offset:0
	ds_read_b64 v[124:125], v106 offset:8
	ds_read_b64 v[126:127], v106 offset:16
	s_barrier
	ds_read_b64 v[128:129], v106 offset:96
	ds_read_b64 v[130:131], v106 offset:104
	ds_read_b64 v[132:133], v106 offset:112
	s_waitcnt lgkmcnt(3)
	v_mfma_f32_16x16x128_f8f6f4 v[134:137], v[122:127], v[2:7], 0 cbsz:2 blgp:2
	v_mfma_f32_16x16x128_f8f6f4 v[138:141], v[122:127], v[14:19], 0 cbsz:2 blgp:2
	v_mfma_f32_16x16x128_f8f6f4 v[142:145], v[122:127], v[26:31], v[188:191] cbsz:2 blgp:2
	v_mfma_f32_16x16x128_f8f6f4 v[204:207], v[122:127], v[38:43], 0 cbsz:2 blgp:2
	v_mfma_f32_16x16x128_f8f6f4 v[208:211], v[122:127], v[50:55], 0 cbsz:2 blgp:2
	v_mfma_f32_16x16x128_f8f6f4 v[212:215], v[122:127], v[62:67], v[188:191] cbsz:2 blgp:2
	s_waitcnt lgkmcnt(0)
	v_mfma_f32_16x16x128_f8f6f4 v[134:137], v[128:133], v[8:13], v[134:137] cbsz:2 blgp:2
	v_mfma_f32_16x16x128_f8f6f4 v[204:207], v[128:133], v[44:49], v[204:207] cbsz:2 blgp:2
	v_mfma_f32_16x16x128_f8f6f4 v[138:141], v[128:133], v[20:25], v[138:141] cbsz:2 blgp:2
	v_mfma_f32_16x16x128_f8f6f4 v[208:211], v[128:133], v[56:61], v[208:211] cbsz:2 blgp:2
	v_mfma_f32_16x16x128_f8f6f4 v[142:145], v[128:133], v[32:37], v[142:145] cbsz:2 blgp:2
	v_mfma_f32_16x16x128_f8f6f4 v[212:215], v[128:133], v[68:73], v[212:215] cbsz:2 blgp:2
	v_cndmask_b32_e64 v158, v134, v204, s[4:5]
	v_fma_mix_f32 v158, v158, v1, v147 op_sel_hi:[0,0,1]
	v_exp_f32_e32 v158, v158
	v_cndmask_b32_e64 v159, v138, v208, s[4:5]
	v_fma_mix_f32 v159, v159, v99, v151 op_sel_hi:[0,0,1]
	v_exp_f32_e32 v159, v159
	v_fma_f32 v158, v158, v186, v186
	v_rcp_f32_e32 v158, v158
	v_add_f32_e32 v159, 1.0, v159
	v_rcp_f32_e32 v159, v159
	v_cndmask_b32_e64 v160, v142, v212, s[4:5]
	v_fma_mix_f32 v161, v158, v160, v155 op_sel_hi:[0,0,1]
	v_exp_f32_e32 v161, v161
	s_add_u32 s48, s48, s40
	v_add_f32_e32 v161, 1.0, v161
	v_rcp_f32_e32 v161, v161
	s_addc_u32 s49, s49, s41
	v_fma_f32 v162, v161, -2.0, 1.0
	v_sub_f32_e32 v163, v176, v162
	v_fma_f32 v176, v159, v163, v162
	v_fma_f32 v164, |v176|, s16, v117
	v_fma_f32 v165, |v176|, s17, v118
	v_fma_f32 v166, |v176|, s18, v119
	v_lshrrev_b32_e32 v167, 26, v176
	v_min3_u32 v164, v164, v165, v166
	v_bfi_b32 v168, 31, v164, v167
	s_nop 1
	v_mul_u32_u24_dpp v170, v168, v180 quad_perm:[1,2,3,3] row_mask:0xf bank_mask:0xf bound_ctrl:1
	v_mad_u32_u24 v171, v168, v181, v170
	ds_write_b8_d16_hi v184, v171 offset:416
	global_store_short_d16_hi v185, v176, s[48:49]
	s_waitcnt lgkmcnt(0)
	s_barrier
	ds_read_b64 v[122:123], v106 offset:416
	ds_read_b64 v[124:125], v106 offset:424
	ds_read_b64 v[126:127], v106 offset:432
	s_barrier
	ds_read_b64 v[128:129], v106 offset:512
	ds_read_b64 v[130:131], v106 offset:520
	ds_read_b64 v[132:133], v106 offset:528
	s_waitcnt lgkmcnt(3)
	v_mfma_f32_16x16x128_f8f6f4 v[134:137], v[122:127], v[2:7], 0 cbsz:2 blgp:2
	v_mfma_f32_16x16x128_f8f6f4 v[138:141], v[122:127], v[14:19], 0 cbsz:2 blgp:2
	v_mfma_f32_16x16x128_f8f6f4 v[142:145], v[122:127], v[26:31], v[188:191] cbsz:2 blgp:2
	v_mfma_f32_16x16x128_f8f6f4 v[204:207], v[122:127], v[38:43], 0 cbsz:2 blgp:2
	v_mfma_f32_16x16x128_f8f6f4 v[208:211], v[122:127], v[50:55], 0 cbsz:2 blgp:2
	v_mfma_f32_16x16x128_f8f6f4 v[212:215], v[122:127], v[62:67], v[188:191] cbsz:2 blgp:2
	s_waitcnt lgkmcnt(0)
	v_mfma_f32_16x16x128_f8f6f4 v[134:137], v[128:133], v[8:13], v[134:137] cbsz:2 blgp:2
	v_mfma_f32_16x16x128_f8f6f4 v[204:207], v[128:133], v[44:49], v[204:207] cbsz:2 blgp:2
	v_mfma_f32_16x16x128_f8f6f4 v[138:141], v[128:133], v[20:25], v[138:141] cbsz:2 blgp:2
	v_mfma_f32_16x16x128_f8f6f4 v[208:211], v[128:133], v[56:61], v[208:211] cbsz:2 blgp:2
	v_mfma_f32_16x16x128_f8f6f4 v[142:145], v[128:133], v[32:37], v[142:145] cbsz:2 blgp:2
	v_mfma_f32_16x16x128_f8f6f4 v[212:215], v[128:133], v[68:73], v[212:215] cbsz:2 blgp:2
	v_cndmask_b32_e64 v158, v134, v204, s[4:5]
	v_fma_mix_f32 v158, v158, v1, v147 op_sel:[0,0,1] op_sel_hi:[0,0,1]
	v_exp_f32_e32 v158, v158
	v_cndmask_b32_e64 v159, v138, v208, s[4:5]
	v_fma_mix_f32 v159, v159, v99, v151 op_sel:[0,0,1] op_sel_hi:[0,0,1]
	v_exp_f32_e32 v159, v159
	v_fma_f32 v158, v158, v186, v186
	v_rcp_f32_e32 v158, v158
	v_add_f32_e32 v159, 1.0, v159
	v_rcp_f32_e32 v159, v159
	v_cndmask_b32_e64 v160, v142, v212, s[4:5]
	v_fma_mix_f32 v161, v158, v160, v155 op_sel:[0,0,1] op_sel_hi:[0,0,1]
	v_exp_f32_e32 v161, v161
	s_add_u32 s48, s48, s40
	v_add_f32_e32 v161, 1.0, v161
	v_rcp_f32_e32 v161, v161
	s_addc_u32 s49, s49, s41
	v_fma_f32 v162, v161, -2.0, 1.0
	v_sub_f32_e32 v163, v176, v162
	v_fma_f32 v176, v159, v163, v162
	v_fma_f32 v164, |v176|, s16, v117
	v_fma_f32 v165, |v176|, s17, v118
	v_fma_f32 v166, |v176|, s18, v119
	v_lshrrev_b32_e32 v167, 26, v176
	v_min3_u32 v164, v164, v165, v166
	v_bfi_b32 v168, 31, v164, v167
	s_nop 1
	v_mul_u32_u24_dpp v170, v168, v180 quad_perm:[1,2,3,3] row_mask:0xf bank_mask:0xf bound_ctrl:1
	v_mad_u32_u24 v171, v168, v181, v170
	ds_write_b8_d16_hi v184, v171
	global_store_short_d16_hi v185, v176, s[48:49]
	s_waitcnt lgkmcnt(0)
	s_barrier
	ds_read_b64 v[122:123], v106 offset:0
	ds_read_b64 v[124:125], v106 offset:8
	ds_read_b64 v[126:127], v106 offset:16
	s_barrier
	ds_read_b64 v[128:129], v106 offset:96
	ds_read_b64 v[130:131], v106 offset:104
	ds_read_b64 v[132:133], v106 offset:112
	s_waitcnt lgkmcnt(3)
	v_mfma_f32_16x16x128_f8f6f4 v[134:137], v[122:127], v[2:7], 0 cbsz:2 blgp:2
	v_mfma_f32_16x16x128_f8f6f4 v[138:141], v[122:127], v[14:19], 0 cbsz:2 blgp:2
	v_mfma_f32_16x16x128_f8f6f4 v[142:145], v[122:127], v[26:31], v[188:191] cbsz:2 blgp:2
	v_mfma_f32_16x16x128_f8f6f4 v[204:207], v[122:127], v[38:43], 0 cbsz:2 blgp:2
	v_mfma_f32_16x16x128_f8f6f4 v[208:211], v[122:127], v[50:55], 0 cbsz:2 blgp:2
	v_mfma_f32_16x16x128_f8f6f4 v[212:215], v[122:127], v[62:67], v[188:191] cbsz:2 blgp:2
	s_waitcnt lgkmcnt(0)
	v_mfma_f32_16x16x128_f8f6f4 v[134:137], v[128:133], v[8:13], v[134:137] cbsz:2 blgp:2
	v_mfma_f32_16x16x128_f8f6f4 v[204:207], v[128:133], v[44:49], v[204:207] cbsz:2 blgp:2
	v_mfma_f32_16x16x128_f8f6f4 v[138:141], v[128:133], v[20:25], v[138:141] cbsz:2 blgp:2
	v_mfma_f32_16x16x128_f8f6f4 v[208:211], v[128:133], v[56:61], v[208:211] cbsz:2 blgp:2
	v_mfma_f32_16x16x128_f8f6f4 v[142:145], v[128:133], v[32:37], v[142:145] cbsz:2 blgp:2
	v_mfma_f32_16x16x128_f8f6f4 v[212:215], v[128:133], v[68:73], v[212:215] cbsz:2 blgp:2
	v_cndmask_b32_e64 v158, v134, v204, s[4:5]
	v_fma_mix_f32 v158, v158, v1, v148 op_sel_hi:[0,0,1]
	v_exp_f32_e32 v158, v158
	v_cndmask_b32_e64 v159, v138, v208, s[4:5]
	v_fma_mix_f32 v159, v159, v99, v152 op_sel_hi:[0,0,1]
	v_exp_f32_e32 v159, v159
	v_fma_f32 v158, v158, v186, v186
	v_rcp_f32_e32 v158, v158
	v_add_f32_e32 v159, 1.0, v159
	v_rcp_f32_e32 v159, v159
	v_cndmask_b32_e64 v160, v142, v212, s[4:5]
	v_fma_mix_f32 v161, v158, v160, v156 op_sel_hi:[0,0,1]
	v_exp_f32_e32 v161, v161
	s_add_u32 s48, s48, s40
	v_add_f32_e32 v161, 1.0, v161
	v_rcp_f32_e32 v161, v161
	s_addc_u32 s49, s49, s41
	v_fma_f32 v162, v161, -2.0, 1.0
	v_sub_f32_e32 v163, v176, v162
	v_fma_f32 v176, v159, v163, v162
	v_fma_f32 v164, |v176|, s16, v117
	v_fma_f32 v165, |v176|, s17, v118
	v_fma_f32 v166, |v176|, s18, v119
	v_lshrrev_b32_e32 v167, 26, v176
	v_min3_u32 v164, v164, v165, v166
	v_bfi_b32 v168, 31, v164, v167
	s_nop 1
	v_mul_u32_u24_dpp v170, v168, v180 quad_perm:[1,2,3,3] row_mask:0xf bank_mask:0xf bound_ctrl:1
	v_mad_u32_u24 v171, v168, v181, v170
	ds_write_b8_d16_hi v184, v171 offset:416
	global_store_short_d16_hi v185, v176, s[48:49]
	s_waitcnt lgkmcnt(0)
	s_barrier
	ds_read_b64 v[122:123], v106 offset:416
	ds_read_b64 v[124:125], v106 offset:424
	ds_read_b64 v[126:127], v106 offset:432
	s_barrier
	ds_read_b64 v[128:129], v106 offset:512
	ds_read_b64 v[130:131], v106 offset:520
	ds_read_b64 v[132:133], v106 offset:528
	s_waitcnt lgkmcnt(3)
	v_mfma_f32_16x16x128_f8f6f4 v[134:137], v[122:127], v[2:7], 0 cbsz:2 blgp:2
	v_mfma_f32_16x16x128_f8f6f4 v[138:141], v[122:127], v[14:19], 0 cbsz:2 blgp:2
	v_mfma_f32_16x16x128_f8f6f4 v[142:145], v[122:127], v[26:31], v[188:191] cbsz:2 blgp:2
	v_mfma_f32_16x16x128_f8f6f4 v[204:207], v[122:127], v[38:43], 0 cbsz:2 blgp:2
	v_mfma_f32_16x16x128_f8f6f4 v[208:211], v[122:127], v[50:55], 0 cbsz:2 blgp:2
	v_mfma_f32_16x16x128_f8f6f4 v[212:215], v[122:127], v[62:67], v[188:191] cbsz:2 blgp:2
	s_waitcnt lgkmcnt(0)
	v_mfma_f32_16x16x128_f8f6f4 v[134:137], v[128:133], v[8:13], v[134:137] cbsz:2 blgp:2
	v_mfma_f32_16x16x128_f8f6f4 v[204:207], v[128:133], v[44:49], v[204:207] cbsz:2 blgp:2
	v_mfma_f32_16x16x128_f8f6f4 v[138:141], v[128:133], v[20:25], v[138:141] cbsz:2 blgp:2
	v_mfma_f32_16x16x128_f8f6f4 v[208:211], v[128:133], v[56:61], v[208:211] cbsz:2 blgp:2
	v_mfma_f32_16x16x128_f8f6f4 v[142:145], v[128:133], v[32:37], v[142:145] cbsz:2 blgp:2
	v_mfma_f32_16x16x128_f8f6f4 v[212:215], v[128:133], v[68:73], v[212:215] cbsz:2 blgp:2
	v_cndmask_b32_e64 v158, v134, v204, s[4:5]
	v_fma_mix_f32 v158, v158, v1, v148 op_sel:[0,0,1] op_sel_hi:[0,0,1]
	v_exp_f32_e32 v158, v158
	v_cndmask_b32_e64 v159, v138, v208, s[4:5]
	v_fma_mix_f32 v159, v159, v99, v152 op_sel:[0,0,1] op_sel_hi:[0,0,1]
	v_exp_f32_e32 v159, v159
	v_fma_f32 v158, v158, v186, v186
	v_rcp_f32_e32 v158, v158
	v_add_f32_e32 v159, 1.0, v159
	v_rcp_f32_e32 v159, v159
	v_cndmask_b32_e64 v160, v142, v212, s[4:5]
	v_fma_mix_f32 v161, v158, v160, v156 op_sel:[0,0,1] op_sel_hi:[0,0,1]
	v_exp_f32_e32 v161, v161
	s_add_u32 s48, s48, s40
	v_add_f32_e32 v161, 1.0, v161
	v_rcp_f32_e32 v161, v161
	s_addc_u32 s49, s49, s41
	v_fma_f32 v162, v161, -2.0, 1.0
	v_sub_f32_e32 v163, v176, v162
	v_fma_f32 v176, v159, v163, v162
	v_fma_f32 v164, |v176|, s16, v117
	v_fma_f32 v165, |v176|, s17, v118
	v_fma_f32 v166, |v176|, s18, v119
	v_lshrrev_b32_e32 v167, 26, v176
	v_min3_u32 v164, v164, v165, v166
	v_bfi_b32 v168, 31, v164, v167
	s_nop 1
	v_mul_u32_u24_dpp v170, v168, v180 quad_perm:[1,2,3,3] row_mask:0xf bank_mask:0xf bound_ctrl:1
	v_mad_u32_u24 v171, v168, v181, v170
	ds_write_b8_d16_hi v184, v171
	global_store_short_d16_hi v185, v176, s[48:49]
	s_waitcnt lgkmcnt(0)
	s_barrier
	ds_read_b64 v[122:123], v106 offset:0
	ds_read_b64 v[124:125], v106 offset:8
	ds_read_b64 v[126:127], v106 offset:16
	s_barrier
	ds_read_b64 v[128:129], v106 offset:96
	ds_read_b64 v[130:131], v106 offset:104
	ds_read_b64 v[132:133], v106 offset:112
	s_waitcnt lgkmcnt(3)
	v_mfma_f32_16x16x128_f8f6f4 v[134:137], v[122:127], v[2:7], 0 cbsz:2 blgp:2
	v_mfma_f32_16x16x128_f8f6f4 v[138:141], v[122:127], v[14:19], 0 cbsz:2 blgp:2
	v_mfma_f32_16x16x128_f8f6f4 v[142:145], v[122:127], v[26:31], v[188:191] cbsz:2 blgp:2
	v_mfma_f32_16x16x128_f8f6f4 v[204:207], v[122:127], v[38:43], 0 cbsz:2 blgp:2
	v_mfma_f32_16x16x128_f8f6f4 v[208:211], v[122:127], v[50:55], 0 cbsz:2 blgp:2
	v_mfma_f32_16x16x128_f8f6f4 v[212:215], v[122:127], v[62:67], v[188:191] cbsz:2 blgp:2
	s_waitcnt lgkmcnt(0)
	v_mfma_f32_16x16x128_f8f6f4 v[134:137], v[128:133], v[8:13], v[134:137] cbsz:2 blgp:2
	v_mfma_f32_16x16x128_f8f6f4 v[204:207], v[128:133], v[44:49], v[204:207] cbsz:2 blgp:2
	v_mfma_f32_16x16x128_f8f6f4 v[138:141], v[128:133], v[20:25], v[138:141] cbsz:2 blgp:2
	v_mfma_f32_16x16x128_f8f6f4 v[208:211], v[128:133], v[56:61], v[208:211] cbsz:2 blgp:2
	v_mfma_f32_16x16x128_f8f6f4 v[142:145], v[128:133], v[32:37], v[142:145] cbsz:2 blgp:2
	v_mfma_f32_16x16x128_f8f6f4 v[212:215], v[128:133], v[68:73], v[212:215] cbsz:2 blgp:2
	v_cndmask_b32_e64 v158, v134, v204, s[4:5]
	v_fma_mix_f32 v158, v158, v1, v149 op_sel_hi:[0,0,1]
	v_exp_f32_e32 v158, v158
	v_cndmask_b32_e64 v159, v138, v208, s[4:5]
	v_fma_mix_f32 v159, v159, v99, v153 op_sel_hi:[0,0,1]
	v_exp_f32_e32 v159, v159
	v_fma_f32 v158, v158, v186, v186
	v_rcp_f32_e32 v158, v158
	v_add_f32_e32 v159, 1.0, v159
	v_rcp_f32_e32 v159, v159
	v_cndmask_b32_e64 v160, v142, v212, s[4:5]
	v_fma_mix_f32 v161, v158, v160, v157 op_sel_hi:[0,0,1]
	v_exp_f32_e32 v161, v161
	s_add_u32 s48, s48, s40
	v_add_f32_e32 v161, 1.0, v161
	v_rcp_f32_e32 v161, v161
	s_addc_u32 s49, s49, s41
	v_fma_f32 v162, v161, -2.0, 1.0
	v_sub_f32_e32 v163, v176, v162
	v_fma_f32 v176, v159, v163, v162
	v_fma_f32 v164, |v176|, s16, v117
	v_fma_f32 v165, |v176|, s17, v118
	v_fma_f32 v166, |v176|, s18, v119
	v_lshrrev_b32_e32 v167, 26, v176
	v_min3_u32 v164, v164, v165, v166
	v_bfi_b32 v168, 31, v164, v167
	s_nop 1
	v_mul_u32_u24_dpp v170, v168, v180 quad_perm:[1,2,3,3] row_mask:0xf bank_mask:0xf bound_ctrl:1
	v_mad_u32_u24 v171, v168, v181, v170
	ds_write_b8_d16_hi v184, v171 offset:416
	global_store_short_d16_hi v185, v176, s[48:49]
	s_waitcnt lgkmcnt(0)
	s_barrier
	ds_read_b64 v[122:123], v106 offset:416
	ds_read_b64 v[124:125], v106 offset:424
	ds_read_b64 v[126:127], v106 offset:432
	s_barrier
	ds_read_b64 v[128:129], v106 offset:512
	ds_read_b64 v[130:131], v106 offset:520
	ds_read_b64 v[132:133], v106 offset:528
	s_add_i32 s44, s44, 16
	s_waitcnt lgkmcnt(3)
	v_mfma_f32_16x16x128_f8f6f4 v[134:137], v[122:127], v[2:7], 0 cbsz:2 blgp:2
	v_mfma_f32_16x16x128_f8f6f4 v[138:141], v[122:127], v[14:19], 0 cbsz:2 blgp:2
	v_mfma_f32_16x16x128_f8f6f4 v[142:145], v[122:127], v[26:31], v[188:191] cbsz:2 blgp:2
	v_mfma_f32_16x16x128_f8f6f4 v[204:207], v[122:127], v[38:43], 0 cbsz:2 blgp:2
	v_mfma_f32_16x16x128_f8f6f4 v[208:211], v[122:127], v[50:55], 0 cbsz:2 blgp:2
	v_mfma_f32_16x16x128_f8f6f4 v[212:215], v[122:127], v[62:67], v[188:191] cbsz:2 blgp:2
	s_waitcnt lgkmcnt(0)
	v_mfma_f32_16x16x128_f8f6f4 v[134:137], v[128:133], v[8:13], v[134:137] cbsz:2 blgp:2
	v_mfma_f32_16x16x128_f8f6f4 v[204:207], v[128:133], v[44:49], v[204:207] cbsz:2 blgp:2
	v_mfma_f32_16x16x128_f8f6f4 v[138:141], v[128:133], v[20:25], v[138:141] cbsz:2 blgp:2
	v_mfma_f32_16x16x128_f8f6f4 v[208:211], v[128:133], v[56:61], v[208:211] cbsz:2 blgp:2
	v_mfma_f32_16x16x128_f8f6f4 v[142:145], v[128:133], v[32:37], v[142:145] cbsz:2 blgp:2
	v_mfma_f32_16x16x128_f8f6f4 v[212:215], v[128:133], v[68:73], v[212:215] cbsz:2 blgp:2
	v_cndmask_b32_e64 v158, v134, v204, s[4:5]
	v_fma_mix_f32 v158, v158, v1, v149 op_sel:[0,0,1] op_sel_hi:[0,0,1]
	v_exp_f32_e32 v158, v158
	v_cndmask_b32_e64 v159, v138, v208, s[4:5]
	v_fma_mix_f32 v159, v159, v99, v153 op_sel:[0,0,1] op_sel_hi:[0,0,1]
	v_exp_f32_e32 v159, v159
	v_fma_f32 v158, v158, v186, v186
	v_rcp_f32_e32 v158, v158
	v_add_f32_e32 v159, 1.0, v159
	v_rcp_f32_e32 v159, v159
	v_cndmask_b32_e64 v160, v142, v212, s[4:5]
	v_fma_mix_f32 v161, v158, v160, v157 op_sel:[0,0,1] op_sel_hi:[0,0,1]
	v_exp_f32_e32 v161, v161
	s_add_u32 s48, s48, s40
	v_add_f32_e32 v161, 1.0, v161
	v_rcp_f32_e32 v161, v161
	s_addc_u32 s49, s49, s41
	v_fma_f32 v162, v161, -2.0, 1.0
	v_sub_f32_e32 v163, v176, v162
	v_fma_f32 v176, v159, v163, v162
	v_fma_f32 v164, |v176|, s16, v117
	v_fma_f32 v165, |v176|, s17, v118
	v_fma_f32 v166, |v176|, s18, v119
	v_lshrrev_b32_e32 v167, 26, v176
	v_min3_u32 v164, v164, v165, v166
	v_bfi_b32 v168, 31, v164, v167
	s_nop 1
	v_mul_u32_u24_dpp v170, v168, v180 quad_perm:[1,2,3,3] row_mask:0xf bank_mask:0xf bound_ctrl:1
	v_mad_u32_u24 v171, v168, v181, v170
	ds_write_b8_d16_hi v184, v171
	global_store_short_d16_hi v185, v176, s[48:49]
	s_waitcnt lgkmcnt(0)
	s_barrier
	ds_read_b64 v[122:123], v106 offset:0
	ds_read_b64 v[124:125], v106 offset:8
	ds_read_b64 v[126:127], v106 offset:16
	s_cmp_lt_i32 s44, s45
	s_barrier
	s_cbranch_scc1 .Lscan_loop_a_st
	s_branch .Lscan_exit_st
.Lscan_loop_b_st:
	ds_read_b64 v[122:123], v106 offset:0
	ds_read_b64 v[124:125], v106 offset:8
	ds_read_b64 v[126:127], v106 offset:16
	ds_read_b64 v[128:129], v106 offset:96
	ds_read_b64 v[130:131], v106 offset:104
	ds_read_b64 v[132:133], v106 offset:112
	s_waitcnt vmcnt(8)
	global_load_dwordx4 v[146:149], v[196:197], off
	global_load_dwordx4 v[150:153], v[196:197], off offset:512
	global_load_dwordx4 v[154:157], v[196:197], off offset:1024
	v_lshl_add_u64 v[196:197], v[196:197], 0, s[42:43]
	s_waitcnt lgkmcnt(3)
	v_mfma_f32_16x16x128_f8f6f4 v[134:137], v[122:127], v[2:7], 0 cbsz:2 blgp:2
	v_mfma_f32_16x16x128_f8f6f4 v[138:141], v[122:127], v[14:19], 0 cbsz:2 blgp:2
	v_mfma_f32_16x16x128_f8f6f4 v[142:145], v[122:127], v[26:31], v[188:191] cbsz:2 blgp:2
	v_mfma_f32_16x16x128_f8f6f4 v[204:207], v[122:127], v[38:43], 0 cbsz:2 blgp:2
	v_mfma_f32_16x16x128_f8f6f4 v[208:211], v[122:127], v[50:55], 0 cbsz:2 blgp:2
	v_mfma_f32_16x16x128_f8f6f4 v[212:215], v[122:127], v[62:67], v[188:191] cbsz:2 blgp:2
	s_waitcnt lgkmcnt(0)
	v_mfma_f32_16x16x128_f8f6f4 v[134:137], v[128:133], v[8:13], v[134:137] cbsz:2 blgp:2
	v_mfma_f32_16x16x128_f8f6f4 v[204:207], v[128:133], v[44:49], v[204:207] cbsz:2 blgp:2
	v_mfma_f32_16x16x128_f8f6f4 v[138:141], v[128:133], v[20:25], v[138:141] cbsz:2 blgp:2
	v_mfma_f32_16x16x128_f8f6f4 v[208:211], v[128:133], v[56:61], v[208:211] cbsz:2 blgp:2
	v_mfma_f32_16x16x128_f8f6f4 v[142:145], v[128:133], v[32:37], v[142:145] cbsz:2 blgp:2
	v_mfma_f32_16x16x128_f8f6f4 v[212:215], v[128:133], v[68:73], v[212:215] cbsz:2 blgp:2
	v_cndmask_b32_e64 v158, v134, v204, s[4:5]
	v_fma_mix_f32 v158, v158, v1, v82 op_sel_hi:[0,0,1]
	v_exp_f32_e32 v158, v158
	v_cndmask_b32_e64 v159, v138, v208, s[4:5]
	v_fma_mix_f32 v159, v159, v99, v74 op_sel_hi:[0,0,1]
	v_exp_f32_e32 v159, v159
	v_fma_f32 v158, v158, v186, v186
	v_rcp_f32_e32 v158, v158
	v_add_f32_e32 v159, 1.0, v159
	v_rcp_f32_e32 v159, v159
	v_cndmask_b32_e64 v160, v142, v212, s[4:5]
	v_fma_mix_f32 v161, v158, v160, v78 op_sel_hi:[0,0,1]
	v_exp_f32_e32 v161, v161
	s_add_u32 s48, s48, s40
	v_add_f32_e32 v161, 1.0, v161
	v_rcp_f32_e32 v161, v161
	s_addc_u32 s49, s49, s41
	v_fma_f32 v162, v161, -2.0, 1.0
	v_sub_f32_e32 v163, v176, v162
	v_fma_f32 v176, v159, v163, v162
	v_fma_f32 v164, |v176|, s16, v117
	v_fma_f32 v165, |v176|, s17, v118
	v_fma_f32 v166, |v176|, s18, v119
	v_lshrrev_b32_e32 v167, 26, v176
	v_min3_u32 v164, v164, v165, v166
	v_bfi_b32 v168, 31, v164, v167
	s_nop 1
	v_mul_u32_u24_dpp v170, v168, v180 quad_perm:[1,2,3,3] row_mask:0xf bank_mask:0xf bound_ctrl:1
	v_mad_u32_u24 v171, v168, v181, v170
	ds_write_b8_d16_hi v184, v171 offset:416
	s_barrier
	global_store_short_d16_hi v185, v176, s[48:49]
	s_waitcnt lgkmcnt(0)
	s_barrier
	ds_read_b64 v[122:123], v106 offset:416
	ds_read_b64 v[124:125], v106 offset:424
	ds_read_b64 v[126:127], v106 offset:432
	ds_read_b64 v[128:129], v106 offset:512
	ds_read_b64 v[130:131], v106 offset:520
	ds_read_b64 v[132:133], v106 offset:528
	s_waitcnt lgkmcnt(3)
	v_mfma_f32_16x16x128_f8f6f4 v[134:137], v[122:127], v[2:7], 0 cbsz:2 blgp:2
	v_mfma_f32_16x16x128_f8f6f4 v[138:141], v[122:127], v[14:19], 0 cbsz:2 blgp:2
	v_mfma_f32_16x16x128_f8f6f4 v[142:145], v[122:127], v[26:31], v[188:191] cbsz:2 blgp:2
	v_mfma_f32_16x16x128_f8f6f4 v[204:207], v[122:127], v[38:43], 0 cbsz:2 blgp:2
	v_mfma_f32_16x16x128_f8f6f4 v[208:211], v[122:127], v[50:55], 0 cbsz:2 blgp:2
	v_mfma_f32_16x16x128_f8f6f4 v[212:215], v[122:127], v[62:67], v[188:191] cbsz:2 blgp:2
	s_waitcnt lgkmcnt(0)
	v_mfma_f32_16x16x128_f8f6f4 v[134:137], v[128:133], v[8:13], v[134:137] cbsz:2 blgp:2
	v_mfma_f32_16x16x128_f8f6f4 v[204:207], v[128:133], v[44:49], v[204:207] cbsz:2 blgp:2
	v_mfma_f32_16x16x128_f8f6f4 v[138:141], v[128:133], v[20:25], v[138:141] cbsz:2 blgp:2
	v_mfma_f32_16x16x128_f8f6f4 v[208:211], v[128:133], v[56:61], v[208:211] cbsz:2 blgp:2
	v_mfma_f32_16x16x128_f8f6f4 v[142:145], v[128:133], v[32:37], v[142:145] cbsz:2 blgp:2
	v_mfma_f32_16x16x128_f8f6f4 v[212:215], v[128:133], v[68:73], v[212:215] cbsz:2 blgp:2
	v_cndmask_b32_e64 v158, v134, v204, s[4:5]
	v_fma_mix_f32 v158, v158, v1, v82 op_sel:[0,0,1] op_sel_hi:[0,0,1]
	v_exp_f32_e32 v158, v158
	v_cndmask_b32_e64 v159, v138, v208, s[4:5]
	v_fma_mix_f32 v159, v159, v99, v74 op_sel:[0,0,1] op_sel_hi:[0,0,1]
	v_exp_f32_e32 v159, v159
	v_fma_f32 v158, v158, v186, v186
	v_rcp_f32_e32 v158, v158
	v_add_f32_e32 v159, 1.0, v159
	v_rcp_f32_e32 v159, v159
	v_cndmask_b32_e64 v160, v142, v212, s[4:5]
	v_fma_mix_f32 v161, v158, v160, v78 op_sel:[0,0,1] op_sel_hi:[0,0,1]
	v_exp_f32_e32 v161, v161
	s_add_u32 s48, s48, s40
	v_add_f32_e32 v161, 1.0, v161
	v_rcp_f32_e32 v161, v161
	s_addc_u32 s49, s49, s41
	v_fma_f32 v162, v161, -2.0, 1.0
	v_sub_f32_e32 v163, v176, v162
	v_fma_f32 v176, v159, v163, v162
	v_fma_f32 v164, |v176|, s16, v117
	v_fma_f32 v165, |v176|, s17, v118
	v_fma_f32 v166, |v176|, s18, v119
	v_lshrrev_b32_e32 v167, 26, v176
	v_min3_u32 v164, v164, v165, v166
	v_bfi_b32 v168, 31, v164, v167
	s_nop 1
	v_mul_u32_u24_dpp v170, v168, v180 quad_perm:[1,2,3,3] row_mask:0xf bank_mask:0xf bound_ctrl:1
	v_mad_u32_u24 v171, v168, v181, v170
	ds_write_b8_d16_hi v184, v171
	s_barrier
	global_store_short_d16_hi v185, v176, s[48:49]
	s_waitcnt lgkmcnt(0)
	s_barrier
	ds_read_b64 v[122:123], v106 offset:0
	ds_read_b64 v[124:125], v106 offset:8
	ds_read_b64 v[126:127], v106 offset:16
	ds_read_b64 v[128:129], v106 offset:96
	ds_read_b64 v[130:131], v106 offset:104
	ds_read_b64 v[132:133], v106 offset:112
	s_waitcnt lgkmcnt(3)
	v_mfma_f32_16x16x128_f8f6f4 v[134:137], v[122:127], v[2:7], 0 cbsz:2 blgp:2
	v_mfma_f32_16x16x128_f8f6f4 v[138:141], v[122:127], v[14:19], 0 cbsz:2 blgp:2
	v_mfma_f32_16x16x128_f8f6f4 v[142:145], v[122:127], v[26:31], v[188:191] cbsz:2 blgp:2
	v_mfma_f32_16x16x128_f8f6f4 v[204:207], v[122:127], v[38:43], 0 cbsz:2 blgp:2
	v_mfma_f32_16x16x128_f8f6f4 v[208:211], v[122:127], v[50:55], 0 cbsz:2 blgp:2
	v_mfma_f32_16x16x128_f8f6f4 v[212:215], v[122:127], v[62:67], v[188:191] cbsz:2 blgp:2
	s_waitcnt lgkmcnt(0)
	v_mfma_f32_16x16x128_f8f6f4 v[134:137], v[128:133], v[8:13], v[134:137] cbsz:2 blgp:2
	v_mfma_f32_16x16x128_f8f6f4 v[204:207], v[128:133], v[44:49], v[204:207] cbsz:2 blgp:2
	v_mfma_f32_16x16x128_f8f6f4 v[138:141], v[128:133], v[20:25], v[138:141] cbsz:2 blgp:2
	v_mfma_f32_16x16x128_f8f6f4 v[208:211], v[128:133], v[56:61], v[208:211] cbsz:2 blgp:2
	v_mfma_f32_16x16x128_f8f6f4 v[142:145], v[128:133], v[32:37], v[142:145] cbsz:2 blgp:2
	v_mfma_f32_16x16x128_f8f6f4 v[212:215], v[128:133], v[68:73], v[212:215] cbsz:2 blgp:2
	v_cndmask_b32_e64 v158, v134, v204, s[4:5]
	v_fma_mix_f32 v158, v158, v1, v83 op_sel_hi:[0,0,1]
	v_exp_f32_e32 v158, v158
	v_cndmask_b32_e64 v159, v138, v208, s[4:5]
	v_fma_mix_f32 v159, v159, v99, v75 op_sel_hi:[0,0,1]
	v_exp_f32_e32 v159, v159
	v_fma_f32 v158, v158, v186, v186
	v_rcp_f32_e32 v158, v158
	v_add_f32_e32 v159, 1.0, v159
	v_rcp_f32_e32 v159, v159
	v_cndmask_b32_e64 v160, v142, v212, s[4:5]
	v_fma_mix_f32 v161, v158, v160, v79 op_sel_hi:[0,0,1]
	v_exp_f32_e32 v161, v161
	s_add_u32 s48, s48, s40
	v_add_f32_e32 v161, 1.0, v161
	v_rcp_f32_e32 v161, v161
	s_addc_u32 s49, s49, s41
	v_fma_f32 v162, v161, -2.0, 1.0
	v_sub_f32_e32 v163, v176, v162
	v_fma_f32 v176, v159, v163, v162
	v_fma_f32 v164, |v176|, s16, v117
	v_fma_f32 v165, |v176|, s17, v118
	v_fma_f32 v166, |v176|, s18, v119
	v_lshrrev_b32_e32 v167, 26, v176
	v_min3_u32 v164, v164, v165, v166
	v_bfi_b32 v168, 31, v164, v167
	s_nop 1
	v_mul_u32_u24_dpp v170, v168, v180 quad_perm:[1,2,3,3] row_mask:0xf bank_mask:0xf bound_ctrl:1
	v_mad_u32_u24 v171, v168, v181, v170
	ds_write_b8_d16_hi v184, v171 offset:416
	s_barrier
	global_store_short_d16_hi v185, v176, s[48:49]
	s_waitcnt lgkmcnt(0)
	s_barrier
	ds_read_b64 v[122:123], v106 offset:416
	ds_read_b64 v[124:125], v106 offset:424
	ds_read_b64 v[126:127], v106 offset:432
	ds_read_b64 v[128:129], v106 offset:512
	ds_read_b64 v[130:131], v106 offset:520
	ds_read_b64 v[132:133], v106 offset:528
	s_waitcnt lgkmcnt(3)
	v_mfma_f32_16x16x128_f8f6f4 v[134:137], v[122:127], v[2:7], 0 cbsz:2 blgp:2
	v_mfma_f32_16x16x128_f8f6f4 v[138:141], v[122:127], v[14:19], 0 cbsz:2 blgp:2
	v_mfma_f32_16x16x128_f8f6f4 v[142:145], v[122:127], v[26:31], v[188:191] cbsz:2 blgp:2
	v_mfma_f32_16x16x128_f8f6f4 v[204:207], v[122:127], v[38:43], 0 cbsz:2 blgp:2
	v_mfma_f32_16x16x128_f8f6f4 v[208:211], v[122:127], v[50:55], 0 cbsz:2 blgp:2
	v_mfma_f32_16x16x128_f8f6f4 v[212:215], v[122:127], v[62:67], v[188:191] cbsz:2 blgp:2
	s_waitcnt lgkmcnt(0)
	v_mfma_f32_16x16x128_f8f6f4 v[134:137], v[128:133], v[8:13], v[134:137] cbsz:2 blgp:2
	v_mfma_f32_16x16x128_f8f6f4 v[204:207], v[128:133], v[44:49], v[204:207] cbsz:2 blgp:2
	v_mfma_f32_16x16x128_f8f6f4 v[138:141], v[128:133], v[20:25], v[138:141] cbsz:2 blgp:2
	v_mfma_f32_16x16x128_f8f6f4 v[208:211], v[128:133], v[56:61], v[208:211] cbsz:2 blgp:2
	v_mfma_f32_16x16x128_f8f6f4 v[142:145], v[128:133], v[32:37], v[142:145] cbsz:2 blgp:2
	v_mfma_f32_16x16x128_f8f6f4 v[212:215], v[128:133], v[68:73], v[212:215] cbsz:2 blgp:2
	v_cndmask_b32_e64 v158, v134, v204, s[4:5]
	v_fma_mix_f32 v158, v158, v1, v83 op_sel:[0,0,1] op_sel_hi:[0,0,1]
	v_exp_f32_e32 v158, v158
	v_cndmask_b32_e64 v159, v138, v208, s[4:5]
	v_fma_mix_f32 v159, v159, v99, v75 op_sel:[0,0,1] op_sel_hi:[0,0,1]
	v_exp_f32_e32 v159, v159
	v_fma_f32 v158, v158, v186, v186
	v_rcp_f32_e32 v158, v158
	v_add_f32_e32 v159, 1.0, v159
	v_rcp_f32_e32 v159, v159
	v_cndmask_b32_e64 v160, v142, v212, s[4:5]
	v_fma_mix_f32 v161, v158, v160, v79 op_sel:[0,0,1] op_sel_hi:[0,0,1]
	v_exp_f32_e32 v161, v161
	s_add_u32 s48, s48, s40
	v_add_f32_e32 v161, 1.0, v161
	v_rcp_f32_e32 v161, v161
	s_addc_u32 s49, s49, s41
	v_fma_f32 v162, v161, -2.0, 1.0
	v_sub_f32_e32 v163, v176, v162
	v_fma_f32 v176, v159, v163, v162
	v_fma_f32 v164, |v176|, s16, v117
	v_fma_f32 v165, |v176|, s17, v118
	v_fma_f32 v166, |v176|, s18, v119
	v_lshrrev_b32_e32 v167, 26, v176
	v_min3_u32 v164, v164, v165, v166
	v_bfi_b32 v168, 31, v164, v167
	s_nop 1
	v_mul_u32_u24_dpp v170, v168, v180 quad_perm:[1,2,3,3] row_mask:0xf bank_mask:0xf bound_ctrl:1
	v_mad_u32_u24 v171, v168, v181, v170
	ds_write_b8_d16_hi v184, v171
	s_barrier
	global_store_short_d16_hi v185, v176, s[48:49]
	s_waitcnt lgkmcnt(0)
	s_barrier
	ds_read_b64 v[122:123], v106 offset:0
	ds_read_b64 v[124:125], v106 offset:8
	ds_read_b64 v[126:127], v106 offset:16
	ds_read_b64 v[128:129], v106 offset:96
	ds_read_b64 v[130:131], v106 offset:104
	ds_read_b64 v[132:133], v106 offset:112
	s_waitcnt lgkmcnt(3)
	v_mfma_f32_16x16x128_f8f6f4 v[134:137], v[122:127], v[2:7], 0 cbsz:2 blgp:2
	v_mfma_f32_16x16x128_f8f6f4 v[138:141], v[122:127], v[14:19], 0 cbsz:2 blgp:2
	v_mfma_f32_16x16x128_f8f6f4 v[142:145], v[122:127], v[26:31], v[188:191] cbsz:2 blgp:2
	v_mfma_f32_16x16x128_f8f6f4 v[204:207], v[122:127], v[38:43], 0 cbsz:2 blgp:2
	v_mfma_f32_16x16x128_f8f6f4 v[208:211], v[122:127], v[50:55], 0 cbsz:2 blgp:2
	v_mfma_f32_16x16x128_f8f6f4 v[212:215], v[122:127], v[62:67], v[188:191] cbsz:2 blgp:2
	s_waitcnt lgkmcnt(0)
	v_mfma_f32_16x16x128_f8f6f4 v[134:137], v[128:133], v[8:13], v[134:137] cbsz:2 blgp:2
	v_mfma_f32_16x16x128_f8f6f4 v[204:207], v[128:133], v[44:49], v[204:207] cbsz:2 blgp:2
	v_mfma_f32_16x16x128_f8f6f4 v[138:141], v[128:133], v[20:25], v[138:141] cbsz:2 blgp:2
	v_mfma_f32_16x16x128_f8f6f4 v[208:211], v[128:133], v[56:61], v[208:211] cbsz:2 blgp:2
	v_mfma_f32_16x16x128_f8f6f4 v[142:145], v[128:133], v[32:37], v[142:145] cbsz:2 blgp:2
	v_mfma_f32_16x16x128_f8f6f4 v[212:215], v[128:133], v[68:73], v[212:215] cbsz:2 blgp:2
	v_cndmask_b32_e64 v158, v134, v204, s[4:5]
	v_fma_mix_f32 v158, v158, v1, v84 op_sel_hi:[0,0,1]
	v_exp_f32_e32 v158, v158
	v_cndmask_b32_e64 v159, v138, v208, s[4:5]
	v_fma_mix_f32 v159, v159, v99, v76 op_sel_hi:[0,0,1]
	v_exp_f32_e32 v159, v159
	v_fma_f32 v158, v158, v186, v186
	v_rcp_f32_e32 v158, v158
	v_add_f32_e32 v159, 1.0, v159
	v_rcp_f32_e32 v159, v159
	v_cndmask_b32_e64 v160, v142, v212, s[4:5]
	v_fma_mix_f32 v161, v158, v160, v80 op_sel_hi:[0,0,1]
	v_exp_f32_e32 v161, v161
	s_add_u32 s48, s48, s40
	v_add_f32_e32 v161, 1.0, v161
	v_rcp_f32_e32 v161, v161
	s_addc_u32 s49, s49, s41
	v_fma_f32 v162, v161, -2.0, 1.0
	v_sub_f32_e32 v163, v176, v162
	v_fma_f32 v176, v159, v163, v162
	v_fma_f32 v164, |v176|, s16, v117
	v_fma_f32 v165, |v176|, s17, v118
	v_fma_f32 v166, |v176|, s18, v119
	v_lshrrev_b32_e32 v167, 26, v176
	v_min3_u32 v164, v164, v165, v166
	v_bfi_b32 v168, 31, v164, v167
	s_nop 1
	v_mul_u32_u24_dpp v170, v168, v180 quad_perm:[1,2,3,3] row_mask:0xf bank_mask:0xf bound_ctrl:1
	v_mad_u32_u24 v171, v168, v181, v170
	ds_write_b8_d16_hi v184, v171 offset:416
	s_barrier
	global_store_short_d16_hi v185, v176, s[48:49]
	s_waitcnt lgkmcnt(0)
	s_barrier
	ds_read_b64 v[122:123], v106 offset:416
	ds_read_b64 v[124:125], v106 offset:424
	ds_read_b64 v[126:127], v106 offset:432
	ds_read_b64 v[128:129], v106 offset:512
	ds_read_b64 v[130:131], v106 offset:520
	ds_read_b64 v[132:133], v106 offset:528
	s_waitcnt lgkmcnt(3)
	v_mfma_f32_16x16x128_f8f6f4 v[134:137], v[122:127], v[2:7], 0 cbsz:2 blgp:2
	v_mfma_f32_16x16x128_f8f6f4 v[138:141], v[122:127], v[14:19], 0 cbsz:2 blgp:2
	v_mfma_f32_16x16x128_f8f6f4 v[142:145], v[122:127], v[26:31], v[188:191] cbsz:2 blgp:2
	v_mfma_f32_16x16x128_f8f6f4 v[204:207], v[122:127], v[38:43], 0 cbsz:2 blgp:2
	v_mfma_f32_16x16x128_f8f6f4 v[208:211], v[122:127], v[50:55], 0 cbsz:2 blgp:2
	v_mfma_f32_16x16x128_f8f6f4 v[212:215], v[122:127], v[62:67], v[188:191] cbsz:2 blgp:2
	s_waitcnt lgkmcnt(0)
	v_mfma_f32_16x16x128_f8f6f4 v[134:137], v[128:133], v[8:13], v[134:137] cbsz:2 blgp:2
	v_mfma_f32_16x16x128_f8f6f4 v[204:207], v[128:133], v[44:49], v[204:207] cbsz:2 blgp:2
	v_mfma_f32_16x16x128_f8f6f4 v[138:141], v[128:133], v[20:25], v[138:141] cbsz:2 blgp:2
	v_mfma_f32_16x16x128_f8f6f4 v[208:211], v[128:133], v[56:61], v[208:211] cbsz:2 blgp:2
	v_mfma_f32_16x16x128_f8f6f4 v[142:145], v[128:133], v[32:37], v[142:145] cbsz:2 blgp:2
	v_mfma_f32_16x16x128_f8f6f4 v[212:215], v[128:133], v[68:73], v[212:215] cbsz:2 blgp:2
	v_cndmask_b32_e64 v158, v134, v204, s[4:5]
	v_fma_mix_f32 v158, v158, v1, v84 op_sel:[0,0,1] op_sel_hi:[0,0,1]
	v_exp_f32_e32 v158, v158
	v_cndmask_b32_e64 v159, v138, v208, s[4:5]
	v_fma_mix_f32 v159, v159, v99, v76 op_sel:[0,0,1] op_sel_hi:[0,0,1]
	v_exp_f32_e32 v159, v159
	v_fma_f32 v158, v158, v186, v186
	v_rcp_f32_e32 v158, v158
	v_add_f32_e32 v159, 1.0, v159
	v_rcp_f32_e32 v159, v159
	v_cndmask_b32_e64 v160, v142, v212, s[4:5]
	v_fma_mix_f32 v161, v158, v160, v80 op_sel:[0,0,1] op_sel_hi:[0,0,1]
	v_exp_f32_e32 v161, v161
	s_add_u32 s48, s48, s40
	v_add_f32_e32 v161, 1.0, v161
	v_rcp_f32_e32 v161, v161
	s_addc_u32 s49, s49, s41
	v_fma_f32 v162, v161, -2.0, 1.0
	v_sub_f32_e32 v163, v176, v162
	v_fma_f32 v176, v159, v163, v162
	v_fma_f32 v164, |v176|, s16, v117
	v_fma_f32 v165, |v176|, s17, v118
	v_fma_f32 v166, |v176|, s18, v119
	v_lshrrev_b32_e32 v167, 26, v176
	v_min3_u32 v164, v164, v165, v166
	v_bfi_b32 v168, 31, v164, v167
	s_nop 1
	v_mul_u32_u24_dpp v170, v168, v180 quad_perm:[1,2,3,3] row_mask:0xf bank_mask:0xf bound_ctrl:1
	v_mad_u32_u24 v171, v168, v181, v170
	ds_write_b8_d16_hi v184, v171
	s_barrier
	global_store_short_d16_hi v185, v176, s[48:49]
	s_waitcnt lgkmcnt(0)
	s_barrier
	ds_read_b64 v[122:123], v106 offset:0
	ds_read_b64 v[124:125], v106 offset:8
	ds_read_b64 v[126:127], v106 offset:16
	ds_read_b64 v[128:129], v106 offset:96
	ds_read_b64 v[130:131], v106 offset:104
	ds_read_b64 v[132:133], v106 offset:112
	s_waitcnt lgkmcnt(3)
	v_mfma_f32_16x16x128_f8f6f4 v[134:137], v[122:127], v[2:7], 0 cbsz:2 blgp:2
	v_mfma_f32_16x16x128_f8f6f4 v[138:141], v[122:127], v[14:19], 0 cbsz:2 blgp:2
	v_mfma_f32_16x16x128_f8f6f4 v[142:145], v[122:127], v[26:31], v[188:191] cbsz:2 blgp:2
	v_mfma_f32_16x16x128_f8f6f4 v[204:207], v[122:127], v[38:43], 0 cbsz:2 blgp:2
	v_mfma_f32_16x16x128_f8f6f4 v[208:211], v[122:127], v[50:55], 0 cbsz:2 blgp:2
	v_mfma_f32_16x16x128_f8f6f4 v[212:215], v[122:127], v[62:67], v[188:191] cbsz:2 blgp:2
	s_waitcnt lgkmcnt(0)
	v_mfma_f32_16x16x128_f8f6f4 v[134:137], v[128:133], v[8:13], v[134:137] cbsz:2 blgp:2
	v_mfma_f32_16x16x128_f8f6f4 v[204:207], v[128:133], v[44:49], v[204:207] cbsz:2 blgp:2
	v_mfma_f32_16x16x128_f8f6f4 v[138:141], v[128:133], v[20:25], v[138:141] cbsz:2 blgp:2
	v_mfma_f32_16x16x128_f8f6f4 v[208:211], v[128:133], v[56:61], v[208:211] cbsz:2 blgp:2
	v_mfma_f32_16x16x128_f8f6f4 v[142:145], v[128:133], v[32:37], v[142:145] cbsz:2 blgp:2
	v_mfma_f32_16x16x128_f8f6f4 v[212:215], v[128:133], v[68:73], v[212:215] cbsz:2 blgp:2
	v_cndmask_b32_e64 v158, v134, v204, s[4:5]
	v_fma_mix_f32 v158, v158, v1, v85 op_sel_hi:[0,0,1]
	v_exp_f32_e32 v158, v158
	v_cndmask_b32_e64 v159, v138, v208, s[4:5]
	v_fma_mix_f32 v159, v159, v99, v77 op_sel_hi:[0,0,1]
	v_exp_f32_e32 v159, v159
	v_fma_f32 v158, v158, v186, v186
	v_rcp_f32_e32 v158, v158
	v_add_f32_e32 v159, 1.0, v159
	v_rcp_f32_e32 v159, v159
	v_cndmask_b32_e64 v160, v142, v212, s[4:5]
	v_fma_mix_f32 v161, v158, v160, v81 op_sel_hi:[0,0,1]
	v_exp_f32_e32 v161, v161
	s_add_u32 s48, s48, s40
	v_add_f32_e32 v161, 1.0, v161
	v_rcp_f32_e32 v161, v161
	s_addc_u32 s49, s49, s41
	v_fma_f32 v162, v161, -2.0, 1.0
	v_sub_f32_e32 v163, v176, v162
	v_fma_f32 v176, v159, v163, v162
	v_fma_f32 v164, |v176|, s16, v117
	v_fma_f32 v165, |v176|, s17, v118
	v_fma_f32 v166, |v176|, s18, v119
	v_lshrrev_b32_e32 v167, 26, v176
	v_min3_u32 v164, v164, v165, v166
	v_bfi_b32 v168, 31, v164, v167
	s_nop 1
	v_mul_u32_u24_dpp v170, v168, v180 quad_perm:[1,2,3,3] row_mask:0xf bank_mask:0xf bound_ctrl:1
	v_mad_u32_u24 v171, v168, v181, v170
	ds_write_b8_d16_hi v184, v171 offset:416
	s_barrier
	global_store_short_d16_hi v185, v176, s[48:49]
	s_waitcnt lgkmcnt(0)
	s_barrier
	ds_read_b64 v[122:123], v106 offset:416
	ds_read_b64 v[124:125], v106 offset:424
	ds_read_b64 v[126:127], v106 offset:432
	ds_read_b64 v[128:129], v106 offset:512
	ds_read_b64 v[130:131], v106 offset:520
	ds_read_b64 v[132:133], v106 offset:528
	s_waitcnt lgkmcnt(3)
	v_mfma_f32_16x16x128_f8f6f4 v[134:137], v[122:127], v[2:7], 0 cbsz:2 blgp:2
	v_mfma_f32_16x16x128_f8f6f4 v[138:141], v[122:127], v[14:19], 0 cbsz:2 blgp:2
	v_mfma_f32_16x16x128_f8f6f4 v[142:145], v[122:127], v[26:31], v[188:191] cbsz:2 blgp:2
	v_mfma_f32_16x16x128_f8f6f4 v[204:207], v[122:127], v[38:43], 0 cbsz:2 blgp:2
	v_mfma_f32_16x16x128_f8f6f4 v[208:211], v[122:127], v[50:55], 0 cbsz:2 blgp:2
	v_mfma_f32_16x16x128_f8f6f4 v[212:215], v[122:127], v[62:67], v[188:191] cbsz:2 blgp:2
	s_waitcnt lgkmcnt(0)
	v_mfma_f32_16x16x128_f8f6f4 v[134:137], v[128:133], v[8:13], v[134:137] cbsz:2 blgp:2
	v_mfma_f32_16x16x128_f8f6f4 v[204:207], v[128:133], v[44:49], v[204:207] cbsz:2 blgp:2
	v_mfma_f32_16x16x128_f8f6f4 v[138:141], v[128:133], v[20:25], v[138:141] cbsz:2 blgp:2
	v_mfma_f32_16x16x128_f8f6f4 v[208:211], v[128:133], v[56:61], v[208:211] cbsz:2 blgp:2
	v_mfma_f32_16x16x128_f8f6f4 v[142:145], v[128:133], v[32:37], v[142:145] cbsz:2 blgp:2
	v_mfma_f32_16x16x128_f8f6f4 v[212:215], v[128:133], v[68:73], v[212:215] cbsz:2 blgp:2
	v_cndmask_b32_e64 v158, v134, v204, s[4:5]
	v_fma_mix_f32 v158, v158, v1, v85 op_sel:[0,0,1] op_sel_hi:[0,0,1]
	v_exp_f32_e32 v158, v158
	v_cndmask_b32_e64 v159, v138, v208, s[4:5]
	v_fma_mix_f32 v159, v159, v99, v77 op_sel:[0,0,1] op_sel_hi:[0,0,1]
	v_exp_f32_e32 v159, v159
	v_fma_f32 v158, v158, v186, v186
	v_rcp_f32_e32 v158, v158
	v_add_f32_e32 v159, 1.0, v159
	v_rcp_f32_e32 v159, v159
	v_cndmask_b32_e64 v160, v142, v212, s[4:5]
	v_fma_mix_f32 v161, v158, v160, v81 op_sel:[0,0,1] op_sel_hi:[0,0,1]
	v_exp_f32_e32 v161, v161
	s_add_u32 s48, s48, s40
	v_add_f32_e32 v161, 1.0, v161
	v_rcp_f32_e32 v161, v161
	s_addc_u32 s49, s49, s41
	v_fma_f32 v162, v161, -2.0, 1.0
	v_sub_f32_e32 v163, v176, v162
	v_fma_f32 v176, v159, v163, v162
	v_fma_f32 v164, |v176|, s16, v117
	v_fma_f32 v165, |v176|, s17, v118
	v_fma_f32 v166, |v176|, s18, v119
	v_lshrrev_b32_e32 v167, 26, v176
	v_min3_u32 v164, v164, v165, v166
	v_bfi_b32 v168, 31, v164, v167
	s_nop 1
	v_mul_u32_u24_dpp v170, v168, v180 quad_perm:[1,2,3,3] row_mask:0xf bank_mask:0xf bound_ctrl:1
	v_mad_u32_u24 v171, v168, v181, v170
	ds_write_b8_d16_hi v184, v171
	s_barrier
	global_store_short_d16_hi v185, v176, s[48:49]
	s_waitcnt lgkmcnt(0)
	s_barrier
	ds_read_b64 v[122:123], v106 offset:0
	ds_read_b64 v[124:125], v106 offset:8
	ds_read_b64 v[126:127], v106 offset:16
	ds_read_b64 v[128:129], v106 offset:96
	ds_read_b64 v[130:131], v106 offset:104
	ds_read_b64 v[132:133], v106 offset:112
	s_waitcnt vmcnt(8)
	global_load_dwordx4 v[82:85], v[196:197], off
	global_load_dwordx4 v[74:77], v[196:197], off offset:512
	global_load_dwordx4 v[78:81], v[196:197], off offset:1024
	v_lshl_add_u64 v[196:197], v[196:197], 0, s[42:43]
	s_waitcnt lgkmcnt(3)
	v_mfma_f32_16x16x128_f8f6f4 v[134:137], v[122:127], v[2:7], 0 cbsz:2 blgp:2
	v_mfma_f32_16x16x128_f8f6f4 v[138:141], v[122:127], v[14:19], 0 cbsz:2 blgp:2
	v_mfma_f32_16x16x128_f8f6f4 v[142:145], v[122:127], v[26:31], v[188:191] cbsz:2 blgp:2
	v_mfma_f32_16x16x128_f8f6f4 v[204:207], v[122:127], v[38:43], 0 cbsz:2 blgp:2
	v_mfma_f32_16x16x128_f8f6f4 v[208:211], v[122:127], v[50:55], 0 cbsz:2 blgp:2
	v_mfma_f32_16x16x128_f8f6f4 v[212:215], v[122:127], v[62:67], v[188:191] cbsz:2 blgp:2
	s_waitcnt lgkmcnt(0)
	v_mfma_f32_16x16x128_f8f6f4 v[134:137], v[128:133], v[8:13], v[134:137] cbsz:2 blgp:2
	v_mfma_f32_16x16x128_f8f6f4 v[204:207], v[128:133], v[44:49], v[204:207] cbsz:2 blgp:2
	v_mfma_f32_16x16x128_f8f6f4 v[138:141], v[128:133], v[20:25], v[138:141] cbsz:2 blgp:2
	v_mfma_f32_16x16x128_f8f6f4 v[208:211], v[128:133], v[56:61], v[208:211] cbsz:2 blgp:2
	v_mfma_f32_16x16x128_f8f6f4 v[142:145], v[128:133], v[32:37], v[142:145] cbsz:2 blgp:2
	v_mfma_f32_16x16x128_f8f6f4 v[212:215], v[128:133], v[68:73], v[212:215] cbsz:2 blgp:2
	v_cndmask_b32_e64 v158, v134, v204, s[4:5]
	v_fma_mix_f32 v158, v158, v1, v146 op_sel_hi:[0,0,1]
	v_exp_f32_e32 v158, v158
	v_cndmask_b32_e64 v159, v138, v208, s[4:5]
	v_fma_mix_f32 v159, v159, v99, v150 op_sel_hi:[0,0,1]
	v_exp_f32_e32 v159, v159
	v_fma_f32 v158, v158, v186, v186
	v_rcp_f32_e32 v158, v158
	v_add_f32_e32 v159, 1.0, v159
	v_rcp_f32_e32 v159, v159
	v_cndmask_b32_e64 v160, v142, v212, s[4:5]
	v_fma_mix_f32 v161, v158, v160, v154 op_sel_hi:[0,0,1]
	v_exp_f32_e32 v161, v161
	s_add_u32 s48, s48, s40
	v_add_f32_e32 v161, 1.0, v161
	v_rcp_f32_e32 v161, v161
	s_addc_u32 s49, s49, s41
	v_fma_f32 v162, v161, -2.0, 1.0
	v_sub_f32_e32 v163, v176, v162
	v_fma_f32 v176, v159, v163, v162
	v_fma_f32 v164, |v176|, s16, v117
	v_fma_f32 v165, |v176|, s17, v118
	v_fma_f32 v166, |v176|, s18, v119
	v_lshrrev_b32_e32 v167, 26, v176
	v_min3_u32 v164, v164, v165, v166
	v_bfi_b32 v168, 31, v164, v167
	s_nop 1
	v_mul_u32_u24_dpp v170, v168, v180 quad_perm:[1,2,3,3] row_mask:0xf bank_mask:0xf bound_ctrl:1
	v_mad_u32_u24 v171, v168, v181, v170
	ds_write_b8_d16_hi v184, v171 offset:416
	s_barrier
	global_store_short_d16_hi v185, v176, s[48:49]
	s_waitcnt lgkmcnt(0)
	s_barrier
	ds_read_b64 v[122:123], v106 offset:416
	ds_read_b64 v[124:125], v106 offset:424
	ds_read_b64 v[126:127], v106 offset:432
	ds_read_b64 v[128:129], v106 offset:512
	ds_read_b64 v[130:131], v106 offset:520
	ds_read_b64 v[132:133], v106 offset:528
	s_waitcnt lgkmcnt(3)
	v_mfma_f32_16x16x128_f8f6f4 v[134:137], v[122:127], v[2:7], 0 cbsz:2 blgp:2
	v_mfma_f32_16x16x128_f8f6f4 v[138:141], v[122:127], v[14:19], 0 cbsz:2 blgp:2
	v_mfma_f32_16x16x128_f8f6f4 v[142:145], v[122:127], v[26:31], v[188:191] cbsz:2 blgp:2
	v_mfma_f32_16x16x128_f8f6f4 v[204:207], v[122:127], v[38:43], 0 cbsz:2 blgp:2
	v_mfma_f32_16x16x128_f8f6f4 v[208:211], v[122:127], v[50:55], 0 cbsz:2 blgp:2
	v_mfma_f32_16x16x128_f8f6f4 v[212:215], v[122:127], v[62:67], v[188:191] cbsz:2 blgp:2
	s_waitcnt lgkmcnt(0)
	v_mfma_f32_16x16x128_f8f6f4 v[134:137], v[128:133], v[8:13], v[134:137] cbsz:2 blgp:2
	v_mfma_f32_16x16x128_f8f6f4 v[204:207], v[128:133], v[44:49], v[204:207] cbsz:2 blgp:2
	v_mfma_f32_16x16x128_f8f6f4 v[138:141], v[128:133], v[20:25], v[138:141] cbsz:2 blgp:2
	v_mfma_f32_16x16x128_f8f6f4 v[208:211], v[128:133], v[56:61], v[208:211] cbsz:2 blgp:2
	v_mfma_f32_16x16x128_f8f6f4 v[142:145], v[128:133], v[32:37], v[142:145] cbsz:2 blgp:2
	v_mfma_f32_16x16x128_f8f6f4 v[212:215], v[128:133], v[68:73], v[212:215] cbsz:2 blgp:2
	v_cndmask_b32_e64 v158, v134, v204, s[4:5]
	v_fma_mix_f32 v158, v158, v1, v146 op_sel:[0,0,1] op_sel_hi:[0,0,1]
	v_exp_f32_e32 v158, v158
	v_cndmask_b32_e64 v159, v138, v208, s[4:5]
	v_fma_mix_f32 v159, v159, v99, v150 op_sel:[0,0,1] op_sel_hi:[0,0,1]
	v_exp_f32_e32 v159, v159
	v_fma_f32 v158, v158, v186, v186
	v_rcp_f32_e32 v158, v158
	v_add_f32_e32 v159, 1.0, v159
	v_rcp_f32_e32 v159, v159
	v_cndmask_b32_e64 v160, v142, v212, s[4:5]
	v_fma_mix_f32 v161, v158, v160, v154 op_sel:[0,0,1] op_sel_hi:[0,0,1]
	v_exp_f32_e32 v161, v161
	s_add_u32 s48, s48, s40
	v_add_f32_e32 v161, 1.0, v161
	v_rcp_f32_e32 v161, v161
	s_addc_u32 s49, s49, s41
	v_fma_f32 v162, v161, -2.0, 1.0
	v_sub_f32_e32 v163, v176, v162
	v_fma_f32 v176, v159, v163, v162
	v_fma_f32 v164, |v176|, s16, v117
	v_fma_f32 v165, |v176|, s17, v118
	v_fma_f32 v166, |v176|, s18, v119
	v_lshrrev_b32_e32 v167, 26, v176
	v_min3_u32 v164, v164, v165, v166
	v_bfi_b32 v168, 31, v164, v167
	s_nop 1
	v_mul_u32_u24_dpp v170, v168, v180 quad_perm:[1,2,3,3] row_mask:0xf bank_mask:0xf bound_ctrl:1
	v_mad_u32_u24 v171, v168, v181, v170
	ds_write_b8_d16_hi v184, v171
	s_barrier
	global_store_short_d16_hi v185, v176, s[48:49]
	s_waitcnt lgkmcnt(0)
	s_barrier
	ds_read_b64 v[122:123], v106 offset:0
	ds_read_b64 v[124:125], v106 offset:8
	ds_read_b64 v[126:127], v106 offset:16
	ds_read_b64 v[128:129], v106 offset:96
	ds_read_b64 v[130:131], v106 offset:104
	ds_read_b64 v[132:133], v106 offset:112
	s_waitcnt lgkmcnt(3)
	v_mfma_f32_16x16x128_f8f6f4 v[134:137], v[122:127], v[2:7], 0 cbsz:2 blgp:2
	v_mfma_f32_16x16x128_f8f6f4 v[138:141], v[122:127], v[14:19], 0 cbsz:2 blgp:2
	v_mfma_f32_16x16x128_f8f6f4 v[142:145], v[122:127], v[26:31], v[188:191] cbsz:2 blgp:2
	v_mfma_f32_16x16x128_f8f6f4 v[204:207], v[122:127], v[38:43], 0 cbsz:2 blgp:2
	v_mfma_f32_16x16x128_f8f6f4 v[208:211], v[122:127], v[50:55], 0 cbsz:2 blgp:2
	v_mfma_f32_16x16x128_f8f6f4 v[212:215], v[122:127], v[62:67], v[188:191] cbsz:2 blgp:2
	s_waitcnt lgkmcnt(0)
	v_mfma_f32_16x16x128_f8f6f4 v[134:137], v[128:133], v[8:13], v[134:137] cbsz:2 blgp:2
	v_mfma_f32_16x16x128_f8f6f4 v[204:207], v[128:133], v[44:49], v[204:207] cbsz:2 blgp:2
	v_mfma_f32_16x16x128_f8f6f4 v[138:141], v[128:133], v[20:25], v[138:141] cbsz:2 blgp:2
	v_mfma_f32_16x16x128_f8f6f4 v[208:211], v[128:133], v[56:61], v[208:211] cbsz:2 blgp:2
	v_mfma_f32_16x16x128_f8f6f4 v[142:145], v[128:133], v[32:37], v[142:145] cbsz:2 blgp:2
	v_mfma_f32_16x16x128_f8f6f4 v[212:215], v[128:133], v[68:73], v[212:215] cbsz:2 blgp:2
	v_cndmask_b32_e64 v158, v134, v204, s[4:5]
	v_fma_mix_f32 v158, v158, v1, v147 op_sel_hi:[0,0,1]
	v_exp_f32_e32 v158, v158
	v_cndmask_b32_e64 v159, v138, v208, s[4:5]
	v_fma_mix_f32 v159, v159, v99, v151 op_sel_hi:[0,0,1]
	v_exp_f32_e32 v159, v159
	v_fma_f32 v158, v158, v186, v186
	v_rcp_f32_e32 v158, v158
	v_add_f32_e32 v159, 1.0, v159
	v_rcp_f32_e32 v159, v159
	v_cndmask_b32_e64 v160, v142, v212, s[4:5]
	v_fma_mix_f32 v161, v158, v160, v155 op_sel_hi:[0,0,1]
	v_exp_f32_e32 v161, v161
	s_add_u32 s48, s48, s40
	v_add_f32_e32 v161, 1.0, v161
	v_rcp_f32_e32 v161, v161
	s_addc_u32 s49, s49, s41
	v_fma_f32 v162, v161, -2.0, 1.0
	v_sub_f32_e32 v163, v176, v162
	v_fma_f32 v176, v159, v163, v162
	v_fma_f32 v164, |v176|, s16, v117
	v_fma_f32 v165, |v176|, s17, v118
	v_fma_f32 v166, |v176|, s18, v119
	v_lshrrev_b32_e32 v167, 26, v176
	v_min3_u32 v164, v164, v165, v166
	v_bfi_b32 v168, 31, v164, v167
	s_nop 1
	v_mul_u32_u24_dpp v170, v168, v180 quad_perm:[1,2,3,3] row_mask:0xf bank_mask:0xf bound_ctrl:1
	v_mad_u32_u24 v171, v168, v181, v170
	ds_write_b8_d16_hi v184, v171 offset:416
	s_barrier
	global_store_short_d16_hi v185, v176, s[48:49]
	s_waitcnt lgkmcnt(0)
	s_barrier
	ds_read_b64 v[122:123], v106 offset:416
	ds_read_b64 v[124:125], v106 offset:424
	ds_read_b64 v[126:127], v106 offset:432
	ds_read_b64 v[128:129], v106 offset:512
	ds_read_b64 v[130:131], v106 offset:520
	ds_read_b64 v[132:133], v106 offset:528
	s_waitcnt lgkmcnt(3)
	v_mfma_f32_16x16x128_f8f6f4 v[134:137], v[122:127], v[2:7], 0 cbsz:2 blgp:2
	v_mfma_f32_16x16x128_f8f6f4 v[138:141], v[122:127], v[14:19], 0 cbsz:2 blgp:2
	v_mfma_f32_16x16x128_f8f6f4 v[142:145], v[122:127], v[26:31], v[188:191] cbsz:2 blgp:2
	v_mfma_f32_16x16x128_f8f6f4 v[204:207], v[122:127], v[38:43], 0 cbsz:2 blgp:2
	v_mfma_f32_16x16x128_f8f6f4 v[208:211], v[122:127], v[50:55], 0 cbsz:2 blgp:2
	v_mfma_f32_16x16x128_f8f6f4 v[212:215], v[122:127], v[62:67], v[188:191] cbsz:2 blgp:2
	s_waitcnt lgkmcnt(0)
	v_mfma_f32_16x16x128_f8f6f4 v[134:137], v[128:133], v[8:13], v[134:137] cbsz:2 blgp:2
	v_mfma_f32_16x16x128_f8f6f4 v[204:207], v[128:133], v[44:49], v[204:207] cbsz:2 blgp:2
	v_mfma_f32_16x16x128_f8f6f4 v[138:141], v[128:133], v[20:25], v[138:141] cbsz:2 blgp:2
	v_mfma_f32_16x16x128_f8f6f4 v[208:211], v[128:133], v[56:61], v[208:211] cbsz:2 blgp:2
	v_mfma_f32_16x16x128_f8f6f4 v[142:145], v[128:133], v[32:37], v[142:145] cbsz:2 blgp:2
	v_mfma_f32_16x16x128_f8f6f4 v[212:215], v[128:133], v[68:73], v[212:215] cbsz:2 blgp:2
	v_cndmask_b32_e64 v158, v134, v204, s[4:5]
	v_fma_mix_f32 v158, v158, v1, v147 op_sel:[0,0,1] op_sel_hi:[0,0,1]
	v_exp_f32_e32 v158, v158
	v_cndmask_b32_e64 v159, v138, v208, s[4:5]
	v_fma_mix_f32 v159, v159, v99, v151 op_sel:[0,0,1] op_sel_hi:[0,0,1]
	v_exp_f32_e32 v159, v159
	v_fma_f32 v158, v158, v186, v186
	v_rcp_f32_e32 v158, v158
	v_add_f32_e32 v159, 1.0, v159
	v_rcp_f32_e32 v159, v159
	v_cndmask_b32_e64 v160, v142, v212, s[4:5]
	v_fma_mix_f32 v161, v158, v160, v155 op_sel:[0,0,1] op_sel_hi:[0,0,1]
	v_exp_f32_e32 v161, v161
	s_add_u32 s48, s48, s40
	v_add_f32_e32 v161, 1.0, v161
	v_rcp_f32_e32 v161, v161
	s_addc_u32 s49, s49, s41
	v_fma_f32 v162, v161, -2.0, 1.0
	v_sub_f32_e32 v163, v176, v162
	v_fma_f32 v176, v159, v163, v162
	v_fma_f32 v164, |v176|, s16, v117
	v_fma_f32 v165, |v176|, s17, v118
	v_fma_f32 v166, |v176|, s18, v119
	v_lshrrev_b32_e32 v167, 26, v176
	v_min3_u32 v164, v164, v165, v166
	v_bfi_b32 v168, 31, v164, v167
	s_nop 1
	v_mul_u32_u24_dpp v170, v168, v180 quad_perm:[1,2,3,3] row_mask:0xf bank_mask:0xf bound_ctrl:1
	v_mad_u32_u24 v171, v168, v181, v170
	ds_write_b8_d16_hi v184, v171
	s_barrier
	global_store_short_d16_hi v185, v176, s[48:49]
	s_waitcnt lgkmcnt(0)
	s_barrier
	ds_read_b64 v[122:123], v106 offset:0
	ds_read_b64 v[124:125], v106 offset:8
	ds_read_b64 v[126:127], v106 offset:16
	ds_read_b64 v[128:129], v106 offset:96
	ds_read_b64 v[130:131], v106 offset:104
	ds_read_b64 v[132:133], v106 offset:112
	s_waitcnt lgkmcnt(3)
	v_mfma_f32_16x16x128_f8f6f4 v[134:137], v[122:127], v[2:7], 0 cbsz:2 blgp:2
	v_mfma_f32_16x16x128_f8f6f4 v[138:141], v[122:127], v[14:19], 0 cbsz:2 blgp:2
	v_mfma_f32_16x16x128_f8f6f4 v[142:145], v[122:127], v[26:31], v[188:191] cbsz:2 blgp:2
	v_mfma_f32_16x16x128_f8f6f4 v[204:207], v[122:127], v[38:43], 0 cbsz:2 blgp:2
	v_mfma_f32_16x16x128_f8f6f4 v[208:211], v[122:127], v[50:55], 0 cbsz:2 blgp:2
	v_mfma_f32_16x16x128_f8f6f4 v[212:215], v[122:127], v[62:67], v[188:191] cbsz:2 blgp:2
	s_waitcnt lgkmcnt(0)
	v_mfma_f32_16x16x128_f8f6f4 v[134:137], v[128:133], v[8:13], v[134:137] cbsz:2 blgp:2
	v_mfma_f32_16x16x128_f8f6f4 v[204:207], v[128:133], v[44:49], v[204:207] cbsz:2 blgp:2
	v_mfma_f32_16x16x128_f8f6f4 v[138:141], v[128:133], v[20:25], v[138:141] cbsz:2 blgp:2
	v_mfma_f32_16x16x128_f8f6f4 v[208:211], v[128:133], v[56:61], v[208:211] cbsz:2 blgp:2
	v_mfma_f32_16x16x128_f8f6f4 v[142:145], v[128:133], v[32:37], v[142:145] cbsz:2 blgp:2
	v_mfma_f32_16x16x128_f8f6f4 v[212:215], v[128:133], v[68:73], v[212:215] cbsz:2 blgp:2
	v_cndmask_b32_e64 v158, v134, v204, s[4:5]
	v_fma_mix_f32 v158, v158, v1, v148 op_sel_hi:[0,0,1]
	v_exp_f32_e32 v158, v158
	v_cndmask_b32_e64 v159, v138, v208, s[4:5]
	v_fma_mix_f32 v159, v159, v99, v152 op_sel_hi:[0,0,1]
	v_exp_f32_e32 v159, v159
	v_fma_f32 v158, v158, v186, v186
	v_rcp_f32_e32 v158, v158
	v_add_f32_e32 v159, 1.0, v159
	v_rcp_f32_e32 v159, v159
	v_cndmask_b32_e64 v160, v142, v212, s[4:5]
	v_fma_mix_f32 v161, v158, v160, v156 op_sel_hi:[0,0,1]
	v_exp_f32_e32 v161, v161
	s_add_u32 s48, s48, s40
	v_add_f32_e32 v161, 1.0, v161
	v_rcp_f32_e32 v161, v161
	s_addc_u32 s49, s49, s41
	v_fma_f32 v162, v161, -2.0, 1.0
	v_sub_f32_e32 v163, v176, v162
	v_fma_f32 v176, v159, v163, v162
	v_fma_f32 v164, |v176|, s16, v117
	v_fma_f32 v165, |v176|, s17, v118
	v_fma_f32 v166, |v176|, s18, v119
	v_lshrrev_b32_e32 v167, 26, v176
	v_min3_u32 v164, v164, v165, v166
	v_bfi_b32 v168, 31, v164, v167
	s_nop 1
	v_mul_u32_u24_dpp v170, v168, v180 quad_perm:[1,2,3,3] row_mask:0xf bank_mask:0xf bound_ctrl:1
	v_mad_u32_u24 v171, v168, v181, v170
	ds_write_b8_d16_hi v184, v171 offset:416
	s_barrier
	global_store_short_d16_hi v185, v176, s[48:49]
	s_waitcnt lgkmcnt(0)
	s_barrier
	ds_read_b64 v[122:123], v106 offset:416
	ds_read_b64 v[124:125], v106 offset:424
	ds_read_b64 v[126:127], v106 offset:432
	ds_read_b64 v[128:129], v106 offset:512
	ds_read_b64 v[130:131], v106 offset:520
	ds_read_b64 v[132:133], v106 offset:528
	s_waitcnt lgkmcnt(3)
	v_mfma_f32_16x16x128_f8f6f4 v[134:137], v[122:127], v[2:7], 0 cbsz:2 blgp:2
	v_mfma_f32_16x16x128_f8f6f4 v[138:141], v[122:127], v[14:19], 0 cbsz:2 blgp:2
	v_mfma_f32_16x16x128_f8f6f4 v[142:145], v[122:127], v[26:31], v[188:191] cbsz:2 blgp:2
	v_mfma_f32_16x16x128_f8f6f4 v[204:207], v[122:127], v[38:43], 0 cbsz:2 blgp:2
	v_mfma_f32_16x16x128_f8f6f4 v[208:211], v[122:127], v[50:55], 0 cbsz:2 blgp:2
	v_mfma_f32_16x16x128_f8f6f4 v[212:215], v[122:127], v[62:67], v[188:191] cbsz:2 blgp:2
	s_waitcnt lgkmcnt(0)
	v_mfma_f32_16x16x128_f8f6f4 v[134:137], v[128:133], v[8:13], v[134:137] cbsz:2 blgp:2
	v_mfma_f32_16x16x128_f8f6f4 v[204:207], v[128:133], v[44:49], v[204:207] cbsz:2 blgp:2
	v_mfma_f32_16x16x128_f8f6f4 v[138:141], v[128:133], v[20:25], v[138:141] cbsz:2 blgp:2
	v_mfma_f32_16x16x128_f8f6f4 v[208:211], v[128:133], v[56:61], v[208:211] cbsz:2 blgp:2
	v_mfma_f32_16x16x128_f8f6f4 v[142:145], v[128:133], v[32:37], v[142:145] cbsz:2 blgp:2
	v_mfma_f32_16x16x128_f8f6f4 v[212:215], v[128:133], v[68:73], v[212:215] cbsz:2 blgp:2
	v_cndmask_b32_e64 v158, v134, v204, s[4:5]
	v_fma_mix_f32 v158, v158, v1, v148 op_sel:[0,0,1] op_sel_hi:[0,0,1]
	v_exp_f32_e32 v158, v158
	v_cndmask_b32_e64 v159, v138, v208, s[4:5]
	v_fma_mix_f32 v159, v159, v99, v152 op_sel:[0,0,1] op_sel_hi:[0,0,1]
	v_exp_f32_e32 v159, v159
	v_fma_f32 v158, v158, v186, v186
	v_rcp_f32_e32 v158, v158
	v_add_f32_e32 v159, 1.0, v159
	v_rcp_f32_e32 v159, v159
	v_cndmask_b32_e64 v160, v142, v212, s[4:5]
	v_fma_mix_f32 v161, v158, v160, v156 op_sel:[0,0,1] op_sel_hi:[0,0,1]
	v_exp_f32_e32 v161, v161
	s_add_u32 s48, s48, s40
	v_add_f32_e32 v161, 1.0, v161
	v_rcp_f32_e32 v161, v161
	s_addc_u32 s49, s49, s41
	v_fma_f32 v162, v161, -2.0, 1.0
	v_sub_f32_e32 v163, v176, v162
	v_fma_f32 v176, v159, v163, v162
	v_fma_f32 v164, |v176|, s16, v117
	v_fma_f32 v165, |v176|, s17, v118
	v_fma_f32 v166, |v176|, s18, v119
	v_lshrrev_b32_e32 v167, 26, v176
	v_min3_u32 v164, v164, v165, v166
	v_bfi_b32 v168, 31, v164, v167
	s_nop 1
	v_mul_u32_u24_dpp v170, v168, v180 quad_perm:[1,2,3,3] row_mask:0xf bank_mask:0xf bound_ctrl:1
	v_mad_u32_u24 v171, v168, v181, v170
	ds_write_b8_d16_hi v184, v171
	s_barrier
	global_store_short_d16_hi v185, v176, s[48:49]
	s_waitcnt lgkmcnt(0)
	s_barrier
	ds_read_b64 v[122:123], v106 offset:0
	ds_read_b64 v[124:125], v106 offset:8
	ds_read_b64 v[126:127], v106 offset:16
	ds_read_b64 v[128:129], v106 offset:96
	ds_read_b64 v[130:131], v106 offset:104
	ds_read_b64 v[132:133], v106 offset:112
	s_waitcnt lgkmcnt(3)
	v_mfma_f32_16x16x128_f8f6f4 v[134:137], v[122:127], v[2:7], 0 cbsz:2 blgp:2
	v_mfma_f32_16x16x128_f8f6f4 v[138:141], v[122:127], v[14:19], 0 cbsz:2 blgp:2
	v_mfma_f32_16x16x128_f8f6f4 v[142:145], v[122:127], v[26:31], v[188:191] cbsz:2 blgp:2
	v_mfma_f32_16x16x128_f8f6f4 v[204:207], v[122:127], v[38:43], 0 cbsz:2 blgp:2
	v_mfma_f32_16x16x128_f8f6f4 v[208:211], v[122:127], v[50:55], 0 cbsz:2 blgp:2
	v_mfma_f32_16x16x128_f8f6f4 v[212:215], v[122:127], v[62:67], v[188:191] cbsz:2 blgp:2
	s_waitcnt lgkmcnt(0)
	v_mfma_f32_16x16x128_f8f6f4 v[134:137], v[128:133], v[8:13], v[134:137] cbsz:2 blgp:2
	v_mfma_f32_16x16x128_f8f6f4 v[204:207], v[128:133], v[44:49], v[204:207] cbsz:2 blgp:2
	v_mfma_f32_16x16x128_f8f6f4 v[138:141], v[128:133], v[20:25], v[138:141] cbsz:2 blgp:2
	v_mfma_f32_16x16x128_f8f6f4 v[208:211], v[128:133], v[56:61], v[208:211] cbsz:2 blgp:2
	v_mfma_f32_16x16x128_f8f6f4 v[142:145], v[128:133], v[32:37], v[142:145] cbsz:2 blgp:2
	v_mfma_f32_16x16x128_f8f6f4 v[212:215], v[128:133], v[68:73], v[212:215] cbsz:2 blgp:2
	v_cndmask_b32_e64 v158, v134, v204, s[4:5]
	v_fma_mix_f32 v158, v158, v1, v149 op_sel_hi:[0,0,1]
	v_exp_f32_e32 v158, v158
	v_cndmask_b32_e64 v159, v138, v208, s[4:5]
	v_fma_mix_f32 v159, v159, v99, v153 op_sel_hi:[0,0,1]
	v_exp_f32_e32 v159, v159
	v_fma_f32 v158, v158, v186, v186
	v_rcp_f32_e32 v158, v158
	v_add_f32_e32 v159, 1.0, v159
	v_rcp_f32_e32 v159, v159
	v_cndmask_b32_e64 v160, v142, v212, s[4:5]
	v_fma_mix_f32 v161, v158, v160, v157 op_sel_hi:[0,0,1]
	v_exp_f32_e32 v161, v161
	s_add_u32 s48, s48, s40
	v_add_f32_e32 v161, 1.0, v161
	v_rcp_f32_e32 v161, v161
	s_addc_u32 s49, s49, s41
	v_fma_f32 v162, v161, -2.0, 1.0
	v_sub_f32_e32 v163, v176, v162
	v_fma_f32 v176, v159, v163, v162
	v_fma_f32 v164, |v176|, s16, v117
	v_fma_f32 v165, |v176|, s17, v118
	v_fma_f32 v166, |v176|, s18, v119
	v_lshrrev_b32_e32 v167, 26, v176
	v_min3_u32 v164, v164, v165, v166
	v_bfi_b32 v168, 31, v164, v167
	s_nop 1
	v_mul_u32_u24_dpp v170, v168, v180 quad_perm:[1,2,3,3] row_mask:0xf bank_mask:0xf bound_ctrl:1
	v_mad_u32_u24 v171, v168, v181, v170
	ds_write_b8_d16_hi v184, v171 offset:416
	s_barrier
	global_store_short_d16_hi v185, v176, s[48:49]
	s_waitcnt lgkmcnt(0)
	s_barrier
	ds_read_b64 v[122:123], v106 offset:416
	ds_read_b64 v[124:125], v106 offset:424
	ds_read_b64 v[126:127], v106 offset:432
	ds_read_b64 v[128:129], v106 offset:512
	ds_read_b64 v[130:131], v106 offset:520
	ds_read_b64 v[132:133], v106 offset:528
	s_add_i32 s44, s44, 16
	s_waitcnt lgkmcnt(3)
	v_mfma_f32_16x16x128_f8f6f4 v[134:137], v[122:127], v[2:7], 0 cbsz:2 blgp:2
	v_mfma_f32_16x16x128_f8f6f4 v[138:141], v[122:127], v[14:19], 0 cbsz:2 blgp:2
	v_mfma_f32_16x16x128_f8f6f4 v[142:145], v[122:127], v[26:31], v[188:191] cbsz:2 blgp:2
	v_mfma_f32_16x16x128_f8f6f4 v[204:207], v[122:127], v[38:43], 0 cbsz:2 blgp:2
	v_mfma_f32_16x16x128_f8f6f4 v[208:211], v[122:127], v[50:55], 0 cbsz:2 blgp:2
	v_mfma_f32_16x16x128_f8f6f4 v[212:215], v[122:127], v[62:67], v[188:191] cbsz:2 blgp:2
	s_waitcnt lgkmcnt(0)
	v_mfma_f32_16x16x128_f8f6f4 v[134:137], v[128:133], v[8:13], v[134:137] cbsz:2 blgp:2
	v_mfma_f32_16x16x128_f8f6f4 v[204:207], v[128:133], v[44:49], v[204:207] cbsz:2 blgp:2
	v_mfma_f32_16x16x128_f8f6f4 v[138:141], v[128:133], v[20:25], v[138:141] cbsz:2 blgp:2
	v_mfma_f32_16x16x128_f8f6f4 v[208:211], v[128:133], v[56:61], v[208:211] cbsz:2 blgp:2
	v_mfma_f32_16x16x128_f8f6f4 v[142:145], v[128:133], v[32:37], v[142:145] cbsz:2 blgp:2
	v_mfma_f32_16x16x128_f8f6f4 v[212:215], v[128:133], v[68:73], v[212:215] cbsz:2 blgp:2
	v_cndmask_b32_e64 v158, v134, v204, s[4:5]
	v_fma_mix_f32 v158, v158, v1, v149 op_sel:[0,0,1] op_sel_hi:[0,0,1]
	v_exp_f32_e32 v158, v158
	v_cndmask_b32_e64 v159, v138, v208, s[4:5]
	v_fma_mix_f32 v159, v159, v99, v153 op_sel:[0,0,1] op_sel_hi:[0,0,1]
	v_exp_f32_e32 v159, v159
	v_fma_f32 v158, v158, v186, v186
	v_rcp_f32_e32 v158, v158
	v_add_f32_e32 v159, 1.0, v159
	v_rcp_f32_e32 v159, v159
	v_cndmask_b32_e64 v160, v142, v212, s[4:5]
	v_fma_mix_f32 v161, v158, v160, v157 op_sel:[0,0,1] op_sel_hi:[0,0,1]
	v_exp_f32_e32 v161, v161
	s_add_u32 s48, s48, s40
	v_add_f32_e32 v161, 1.0, v161
	v_rcp_f32_e32 v161, v161
	s_addc_u32 s49, s49, s41
	v_fma_f32 v162, v161, -2.0, 1.0
	v_sub_f32_e32 v163, v176, v162
	v_fma_f32 v176, v159, v163, v162
	v_fma_f32 v164, |v176|, s16, v117
	v_fma_f32 v165, |v176|, s17, v118
	v_fma_f32 v166, |v176|, s18, v119
	v_lshrrev_b32_e32 v167, 26, v176
	v_min3_u32 v164, v164, v165, v166
	v_bfi_b32 v168, 31, v164, v167
	s_nop 1
	v_mul_u32_u24_dpp v170, v168, v180 quad_perm:[1,2,3,3] row_mask:0xf bank_mask:0xf bound_ctrl:1
	v_mad_u32_u24 v171, v168, v181, v170
	ds_write_b8_d16_hi v184, v171
	s_barrier
	global_store_short_d16_hi v185, v176, s[48:49]
	s_cmp_lt_i32 s44, s45
	s_waitcnt lgkmcnt(0)
	s_barrier
	s_cbranch_scc1 .Lscan_loop_b_st

.Lscan_loop_a_f2:
	ds_read_b64 v[128:129], v105 offset:96
	ds_read_b64 v[130:131], v105 offset:104
	ds_read_b64 v[132:133], v105 offset:112
	s_waitcnt vmcnt(8)
	global_load_dwordx4 v[146:149], v[196:197], off
	global_load_dwordx4 v[150:153], v[196:197], off offset:512
	global_load_dwordx4 v[154:157], v[196:197], off offset:1024
	v_lshl_add_u64 v[196:197], v[196:197], 0, s[42:43]
	s_waitcnt lgkmcnt(3)
	v_mfma_f32_16x16x128_f8f6f4 v[134:137], v[122:127], v[2:7], 0 cbsz:2 blgp:2
	v_mfma_f32_16x16x128_f8f6f4 v[138:141], v[122:127], v[14:19], 0 cbsz:2 blgp:2
	v_mfma_f32_16x16x128_f8f6f4 v[142:145], v[122:127], v[26:31], v[188:191] cbsz:2 blgp:2
	v_mfma_f32_16x16x128_f8f6f4 v[204:207], v[122:127], v[38:43], 0 cbsz:2 blgp:2
	v_mfma_f32_16x16x128_f8f6f4 v[208:211], v[122:127], v[50:55], 0 cbsz:2 blgp:2
	v_mfma_f32_16x16x128_f8f6f4 v[212:215], v[122:127], v[62:67], v[188:191] cbsz:2 blgp:2
	s_waitcnt lgkmcnt(0)
	v_mfma_f32_16x16x128_f8f6f4 v[134:137], v[128:133], v[8:13], v[134:137] cbsz:2 blgp:2
	v_mfma_f32_16x16x128_f8f6f4 v[204:207], v[128:133], v[44:49], v[204:207] cbsz:2 blgp:2
	v_mfma_f32_16x16x128_f8f6f4 v[138:141], v[128:133], v[20:25], v[138:141] cbsz:2 blgp:2
	v_mfma_f32_16x16x128_f8f6f4 v[208:211], v[128:133], v[56:61], v[208:211] cbsz:2 blgp:2
	v_mfma_f32_16x16x128_f8f6f4 v[142:145], v[128:133], v[32:37], v[142:145] cbsz:2 blgp:2
	v_mfma_f32_16x16x128_f8f6f4 v[212:215], v[128:133], v[68:73], v[212:215] cbsz:2 blgp:2
	v_cndmask_b32_e64 v158, v134, v204, s[0:1]
	v_fma_mix_f32 v158, v158, v100, v82 op_sel_hi:[0,0,1]
	v_exp_f32_e32 v158, v158
	v_cndmask_b32_e64 v159, v138, v208, s[0:1]
	v_fma_mix_f32 v159, v159, v101, v74 op_sel_hi:[0,0,1]
	v_exp_f32_e32 v159, v159
	v_fma_f32 v158, v158, v186, v186
	v_rcp_f32_e32 v158, v158
	v_add_f32_e32 v159, 1.0, v159
	v_rcp_f32_e32 v159, v159
	v_cndmask_b32_e64 v160, v142, v212, s[0:1]
	v_fma_mix_f32 v161, v158, v160, v78 op_sel_hi:[0,0,1]
	v_exp_f32_e32 v161, v161
	s_add_u32 s48, s48, s40
	v_add_f32_e32 v161, 1.0, v161
	v_rcp_f32_e32 v161, v161
	s_addc_u32 s49, s49, s41
	v_fma_f32 v162, v161, -2.0, 1.0
	v_sub_f32_e32 v163, v176, v162
	v_fma_f32 v176, v159, v163, v162
	v_fma_f32 v164, |v176|, s17, v113
	v_fma_f32 v165, |v176|, s18, v114
	v_fma_f32 v166, |v176|, s19, v115
	v_lshrrev_b32_e32 v167, 26, v176
	v_min3_u32 v164, v164, v165, v166
	v_bfi_b32 v168, 31, v164, v167
	s_nop 1
	v_mul_u32_u24_dpp v170, v168, v180 quad_perm:[1,2,3,3] row_mask:0xf bank_mask:0xf bound_ctrl:1
	v_mad_u32_u24 v171, v168, v181, v170
	ds_write_b8_d16_hi v184, v171 offset:416
	global_store_short_d16_hi v185, v176, s[48:49]
	s_waitcnt lgkmcnt(0)
	s_barrier
	ds_read_b64 v[122:123], v105 offset:416
	ds_read_b64 v[124:125], v105 offset:424
	ds_read_b64 v[126:127], v105 offset:432
	s_barrier
	ds_read_b64 v[128:129], v105 offset:512
	ds_read_b64 v[130:131], v105 offset:520
	ds_read_b64 v[132:133], v105 offset:528
	s_waitcnt lgkmcnt(3)
	v_mfma_f32_16x16x128_f8f6f4 v[134:137], v[122:127], v[2:7], 0 cbsz:2 blgp:2
	v_mfma_f32_16x16x128_f8f6f4 v[138:141], v[122:127], v[14:19], 0 cbsz:2 blgp:2
	v_mfma_f32_16x16x128_f8f6f4 v[142:145], v[122:127], v[26:31], v[188:191] cbsz:2 blgp:2
	v_mfma_f32_16x16x128_f8f6f4 v[204:207], v[122:127], v[38:43], 0 cbsz:2 blgp:2
	v_mfma_f32_16x16x128_f8f6f4 v[208:211], v[122:127], v[50:55], 0 cbsz:2 blgp:2
	v_mfma_f32_16x16x128_f8f6f4 v[212:215], v[122:127], v[62:67], v[188:191] cbsz:2 blgp:2
	s_waitcnt lgkmcnt(0)
	v_mfma_f32_16x16x128_f8f6f4 v[134:137], v[128:133], v[8:13], v[134:137] cbsz:2 blgp:2
	v_mfma_f32_16x16x128_f8f6f4 v[204:207], v[128:133], v[44:49], v[204:207] cbsz:2 blgp:2
	v_mfma_f32_16x16x128_f8f6f4 v[138:141], v[128:133], v[20:25], v[138:141] cbsz:2 blgp:2
	v_mfma_f32_16x16x128_f8f6f4 v[208:211], v[128:133], v[56:61], v[208:211] cbsz:2 blgp:2
	v_mfma_f32_16x16x128_f8f6f4 v[142:145], v[128:133], v[32:37], v[142:145] cbsz:2 blgp:2
	v_mfma_f32_16x16x128_f8f6f4 v[212:215], v[128:133], v[68:73], v[212:215] cbsz:2 blgp:2
	v_cndmask_b32_e64 v158, v134, v204, s[0:1]
	v_fma_mix_f32 v158, v158, v100, v82 op_sel:[0,0,1] op_sel_hi:[0,0,1]
	v_exp_f32_e32 v158, v158
	v_cndmask_b32_e64 v159, v138, v208, s[0:1]
	v_fma_mix_f32 v159, v159, v101, v74 op_sel:[0,0,1] op_sel_hi:[0,0,1]
	v_exp_f32_e32 v159, v159
	v_fma_f32 v158, v158, v186, v186
	v_rcp_f32_e32 v158, v158
	v_add_f32_e32 v159, 1.0, v159
	v_rcp_f32_e32 v159, v159
	v_cndmask_b32_e64 v160, v142, v212, s[0:1]
	v_fma_mix_f32 v161, v158, v160, v78 op_sel:[0,0,1] op_sel_hi:[0,0,1]
	v_exp_f32_e32 v161, v161
	s_add_u32 s48, s48, s40
	v_add_f32_e32 v161, 1.0, v161
	v_rcp_f32_e32 v161, v161
	s_addc_u32 s49, s49, s41
	v_fma_f32 v162, v161, -2.0, 1.0
	v_sub_f32_e32 v163, v176, v162
	v_fma_f32 v176, v159, v163, v162
	v_fma_f32 v164, |v176|, s17, v113
	v_fma_f32 v165, |v176|, s18, v114
	v_fma_f32 v166, |v176|, s19, v115
	v_lshrrev_b32_e32 v167, 26, v176
	v_min3_u32 v164, v164, v165, v166
	v_bfi_b32 v168, 31, v164, v167
	s_nop 1
	v_mul_u32_u24_dpp v170, v168, v180 quad_perm:[1,2,3,3] row_mask:0xf bank_mask:0xf bound_ctrl:1
	v_mad_u32_u24 v171, v168, v181, v170
	ds_write_b8_d16_hi v184, v171
	global_store_short_d16_hi v185, v176, s[48:49]
	s_waitcnt lgkmcnt(0)
	s_barrier
	ds_read_b64 v[122:123], v105 offset:0
	ds_read_b64 v[124:125], v105 offset:8
	ds_read_b64 v[126:127], v105 offset:16
	s_barrier
	ds_read_b64 v[128:129], v105 offset:96
	ds_read_b64 v[130:131], v105 offset:104
	ds_read_b64 v[132:133], v105 offset:112
	s_waitcnt lgkmcnt(3)
	v_mfma_f32_16x16x128_f8f6f4 v[134:137], v[122:127], v[2:7], 0 cbsz:2 blgp:2
	v_mfma_f32_16x16x128_f8f6f4 v[138:141], v[122:127], v[14:19], 0 cbsz:2 blgp:2
	v_mfma_f32_16x16x128_f8f6f4 v[142:145], v[122:127], v[26:31], v[188:191] cbsz:2 blgp:2
	v_mfma_f32_16x16x128_f8f6f4 v[204:207], v[122:127], v[38:43], 0 cbsz:2 blgp:2
	v_mfma_f32_16x16x128_f8f6f4 v[208:211], v[122:127], v[50:55], 0 cbsz:2 blgp:2
	v_mfma_f32_16x16x128_f8f6f4 v[212:215], v[122:127], v[62:67], v[188:191] cbsz:2 blgp:2
	s_waitcnt lgkmcnt(0)
	v_mfma_f32_16x16x128_f8f6f4 v[134:137], v[128:133], v[8:13], v[134:137] cbsz:2 blgp:2
	v_mfma_f32_16x16x128_f8f6f4 v[204:207], v[128:133], v[44:49], v[204:207] cbsz:2 blgp:2
	v_mfma_f32_16x16x128_f8f6f4 v[138:141], v[128:133], v[20:25], v[138:141] cbsz:2 blgp:2
	v_mfma_f32_16x16x128_f8f6f4 v[208:211], v[128:133], v[56:61], v[208:211] cbsz:2 blgp:2
	v_mfma_f32_16x16x128_f8f6f4 v[142:145], v[128:133], v[32:37], v[142:145] cbsz:2 blgp:2
	v_mfma_f32_16x16x128_f8f6f4 v[212:215], v[128:133], v[68:73], v[212:215] cbsz:2 blgp:2
	v_cndmask_b32_e64 v158, v134, v204, s[0:1]
	v_fma_mix_f32 v158, v158, v100, v83 op_sel_hi:[0,0,1]
	v_exp_f32_e32 v158, v158
	v_cndmask_b32_e64 v159, v138, v208, s[0:1]
	v_fma_mix_f32 v159, v159, v101, v75 op_sel_hi:[0,0,1]
	v_exp_f32_e32 v159, v159
	v_fma_f32 v158, v158, v186, v186
	v_rcp_f32_e32 v158, v158
	v_add_f32_e32 v159, 1.0, v159
	v_rcp_f32_e32 v159, v159
	v_cndmask_b32_e64 v160, v142, v212, s[0:1]
	v_fma_mix_f32 v161, v158, v160, v79 op_sel_hi:[0,0,1]
	v_exp_f32_e32 v161, v161
	s_add_u32 s48, s48, s40
	v_add_f32_e32 v161, 1.0, v161
	v_rcp_f32_e32 v161, v161
	s_addc_u32 s49, s49, s41
	v_fma_f32 v162, v161, -2.0, 1.0
	v_sub_f32_e32 v163, v176, v162
	v_fma_f32 v176, v159, v163, v162
	v_fma_f32 v164, |v176|, s17, v113
	v_fma_f32 v165, |v176|, s18, v114
	v_fma_f32 v166, |v176|, s19, v115
	v_lshrrev_b32_e32 v167, 26, v176
	v_min3_u32 v164, v164, v165, v166
	v_bfi_b32 v168, 31, v164, v167
	s_nop 1
	v_mul_u32_u24_dpp v170, v168, v180 quad_perm:[1,2,3,3] row_mask:0xf bank_mask:0xf bound_ctrl:1
	v_mad_u32_u24 v171, v168, v181, v170
	ds_write_b8_d16_hi v184, v171 offset:416
	global_store_short_d16_hi v185, v176, s[48:49]
	s_waitcnt lgkmcnt(0)
	s_barrier
	ds_read_b64 v[122:123], v105 offset:416
	ds_read_b64 v[124:125], v105 offset:424
	ds_read_b64 v[126:127], v105 offset:432
	s_barrier
	ds_read_b64 v[128:129], v105 offset:512
	ds_read_b64 v[130:131], v105 offset:520
	ds_read_b64 v[132:133], v105 offset:528
	s_waitcnt lgkmcnt(3)
	v_mfma_f32_16x16x128_f8f6f4 v[134:137], v[122:127], v[2:7], 0 cbsz:2 blgp:2
	v_mfma_f32_16x16x128_f8f6f4 v[138:141], v[122:127], v[14:19], 0 cbsz:2 blgp:2
	v_mfma_f32_16x16x128_f8f6f4 v[142:145], v[122:127], v[26:31], v[188:191] cbsz:2 blgp:2
	v_mfma_f32_16x16x128_f8f6f4 v[204:207], v[122:127], v[38:43], 0 cbsz:2 blgp:2
	v_mfma_f32_16x16x128_f8f6f4 v[208:211], v[122:127], v[50:55], 0 cbsz:2 blgp:2
	v_mfma_f32_16x16x128_f8f6f4 v[212:215], v[122:127], v[62:67], v[188:191] cbsz:2 blgp:2
	s_waitcnt lgkmcnt(0)
	v_mfma_f32_16x16x128_f8f6f4 v[134:137], v[128:133], v[8:13], v[134:137] cbsz:2 blgp:2
	v_mfma_f32_16x16x128_f8f6f4 v[204:207], v[128:133], v[44:49], v[204:207] cbsz:2 blgp:2
	v_mfma_f32_16x16x128_f8f6f4 v[138:141], v[128:133], v[20:25], v[138:141] cbsz:2 blgp:2
	v_mfma_f32_16x16x128_f8f6f4 v[208:211], v[128:133], v[56:61], v[208:211] cbsz:2 blgp:2
	v_mfma_f32_16x16x128_f8f6f4 v[142:145], v[128:133], v[32:37], v[142:145] cbsz:2 blgp:2
	v_mfma_f32_16x16x128_f8f6f4 v[212:215], v[128:133], v[68:73], v[212:215] cbsz:2 blgp:2
	v_cndmask_b32_e64 v158, v134, v204, s[0:1]
	v_fma_mix_f32 v158, v158, v100, v83 op_sel:[0,0,1] op_sel_hi:[0,0,1]
	v_exp_f32_e32 v158, v158
	v_cndmask_b32_e64 v159, v138, v208, s[0:1]
	v_fma_mix_f32 v159, v159, v101, v75 op_sel:[0,0,1] op_sel_hi:[0,0,1]
	v_exp_f32_e32 v159, v159
	v_fma_f32 v158, v158, v186, v186
	v_rcp_f32_e32 v158, v158
	v_add_f32_e32 v159, 1.0, v159
	v_rcp_f32_e32 v159, v159
	v_cndmask_b32_e64 v160, v142, v212, s[0:1]
	v_fma_mix_f32 v161, v158, v160, v79 op_sel:[0,0,1] op_sel_hi:[0,0,1]
	v_exp_f32_e32 v161, v161
	s_add_u32 s48, s48, s40
	v_add_f32_e32 v161, 1.0, v161
	v_rcp_f32_e32 v161, v161
	s_addc_u32 s49, s49, s41
	v_fma_f32 v162, v161, -2.0, 1.0
	v_sub_f32_e32 v163, v176, v162
	v_fma_f32 v176, v159, v163, v162
	v_fma_f32 v164, |v176|, s17, v113
	v_fma_f32 v165, |v176|, s18, v114
	v_fma_f32 v166, |v176|, s19, v115
	v_lshrrev_b32_e32 v167, 26, v176
	v_min3_u32 v164, v164, v165, v166
	v_bfi_b32 v168, 31, v164, v167
	s_nop 1
	v_mul_u32_u24_dpp v170, v168, v180 quad_perm:[1,2,3,3] row_mask:0xf bank_mask:0xf bound_ctrl:1
	v_mad_u32_u24 v171, v168, v181, v170
	ds_write_b8_d16_hi v184, v171
	global_store_short_d16_hi v185, v176, s[48:49]
	s_waitcnt lgkmcnt(0)
	s_barrier
	ds_read_b64 v[122:123], v105 offset:0
	ds_read_b64 v[124:125], v105 offset:8
	ds_read_b64 v[126:127], v105 offset:16
	s_barrier
	ds_read_b64 v[128:129], v105 offset:96
	ds_read_b64 v[130:131], v105 offset:104
	ds_read_b64 v[132:133], v105 offset:112
	s_waitcnt lgkmcnt(3)
	v_mfma_f32_16x16x128_f8f6f4 v[134:137], v[122:127], v[2:7], 0 cbsz:2 blgp:2
	v_mfma_f32_16x16x128_f8f6f4 v[138:141], v[122:127], v[14:19], 0 cbsz:2 blgp:2
	v_mfma_f32_16x16x128_f8f6f4 v[142:145], v[122:127], v[26:31], v[188:191] cbsz:2 blgp:2
	v_mfma_f32_16x16x128_f8f6f4 v[204:207], v[122:127], v[38:43], 0 cbsz:2 blgp:2
	v_mfma_f32_16x16x128_f8f6f4 v[208:211], v[122:127], v[50:55], 0 cbsz:2 blgp:2
	v_mfma_f32_16x16x128_f8f6f4 v[212:215], v[122:127], v[62:67], v[188:191] cbsz:2 blgp:2
	s_waitcnt lgkmcnt(0)
	v_mfma_f32_16x16x128_f8f6f4 v[134:137], v[128:133], v[8:13], v[134:137] cbsz:2 blgp:2
	v_mfma_f32_16x16x128_f8f6f4 v[204:207], v[128:133], v[44:49], v[204:207] cbsz:2 blgp:2
	v_mfma_f32_16x16x128_f8f6f4 v[138:141], v[128:133], v[20:25], v[138:141] cbsz:2 blgp:2
	v_mfma_f32_16x16x128_f8f6f4 v[208:211], v[128:133], v[56:61], v[208:211] cbsz:2 blgp:2
	v_mfma_f32_16x16x128_f8f6f4 v[142:145], v[128:133], v[32:37], v[142:145] cbsz:2 blgp:2
	v_mfma_f32_16x16x128_f8f6f4 v[212:215], v[128:133], v[68:73], v[212:215] cbsz:2 blgp:2
	v_cndmask_b32_e64 v158, v134, v204, s[0:1]
	v_fma_mix_f32 v158, v158, v100, v84 op_sel_hi:[0,0,1]
	v_exp_f32_e32 v158, v158
	v_cndmask_b32_e64 v159, v138, v208, s[0:1]
	v_fma_mix_f32 v159, v159, v101, v76 op_sel_hi:[0,0,1]
	v_exp_f32_e32 v159, v159
	v_fma_f32 v158, v158, v186, v186
	v_rcp_f32_e32 v158, v158
	v_add_f32_e32 v159, 1.0, v159
	v_rcp_f32_e32 v159, v159
	v_cndmask_b32_e64 v160, v142, v212, s[0:1]
	v_fma_mix_f32 v161, v158, v160, v80 op_sel_hi:[0,0,1]
	v_exp_f32_e32 v161, v161
	s_add_u32 s48, s48, s40
	v_add_f32_e32 v161, 1.0, v161
	v_rcp_f32_e32 v161, v161
	s_addc_u32 s49, s49, s41
	v_fma_f32 v162, v161, -2.0, 1.0
	v_sub_f32_e32 v163, v176, v162
	v_fma_f32 v176, v159, v163, v162
	v_fma_f32 v164, |v176|, s17, v113
	v_fma_f32 v165, |v176|, s18, v114
	v_fma_f32 v166, |v176|, s19, v115
	v_lshrrev_b32_e32 v167, 26, v176
	v_min3_u32 v164, v164, v165, v166
	v_bfi_b32 v168, 31, v164, v167
	s_nop 1
	v_mul_u32_u24_dpp v170, v168, v180 quad_perm:[1,2,3,3] row_mask:0xf bank_mask:0xf bound_ctrl:1
	v_mad_u32_u24 v171, v168, v181, v170
	ds_write_b8_d16_hi v184, v171 offset:416
	global_store_short_d16_hi v185, v176, s[48:49]
	s_waitcnt lgkmcnt(0)
	s_barrier
	ds_read_b64 v[122:123], v105 offset:416
	ds_read_b64 v[124:125], v105 offset:424
	ds_read_b64 v[126:127], v105 offset:432
	s_barrier
	ds_read_b64 v[128:129], v105 offset:512
	ds_read_b64 v[130:131], v105 offset:520
	ds_read_b64 v[132:133], v105 offset:528
	s_waitcnt lgkmcnt(3)
	v_mfma_f32_16x16x128_f8f6f4 v[134:137], v[122:127], v[2:7], 0 cbsz:2 blgp:2
	v_mfma_f32_16x16x128_f8f6f4 v[138:141], v[122:127], v[14:19], 0 cbsz:2 blgp:2
	v_mfma_f32_16x16x128_f8f6f4 v[142:145], v[122:127], v[26:31], v[188:191] cbsz:2 blgp:2
	v_mfma_f32_16x16x128_f8f6f4 v[204:207], v[122:127], v[38:43], 0 cbsz:2 blgp:2
	v_mfma_f32_16x16x128_f8f6f4 v[208:211], v[122:127], v[50:55], 0 cbsz:2 blgp:2
	v_mfma_f32_16x16x128_f8f6f4 v[212:215], v[122:127], v[62:67], v[188:191] cbsz:2 blgp:2
	s_waitcnt lgkmcnt(0)
	v_mfma_f32_16x16x128_f8f6f4 v[134:137], v[128:133], v[8:13], v[134:137] cbsz:2 blgp:2
	v_mfma_f32_16x16x128_f8f6f4 v[204:207], v[128:133], v[44:49], v[204:207] cbsz:2 blgp:2
	v_mfma_f32_16x16x128_f8f6f4 v[138:141], v[128:133], v[20:25], v[138:141] cbsz:2 blgp:2
	v_mfma_f32_16x16x128_f8f6f4 v[208:211], v[128:133], v[56:61], v[208:211] cbsz:2 blgp:2
	v_mfma_f32_16x16x128_f8f6f4 v[142:145], v[128:133], v[32:37], v[142:145] cbsz:2 blgp:2
	v_mfma_f32_16x16x128_f8f6f4 v[212:215], v[128:133], v[68:73], v[212:215] cbsz:2 blgp:2
	v_cndmask_b32_e64 v158, v134, v204, s[0:1]
	v_fma_mix_f32 v158, v158, v100, v84 op_sel:[0,0,1] op_sel_hi:[0,0,1]
	v_exp_f32_e32 v158, v158
	v_cndmask_b32_e64 v159, v138, v208, s[0:1]
	v_fma_mix_f32 v159, v159, v101, v76 op_sel:[0,0,1] op_sel_hi:[0,0,1]
	v_exp_f32_e32 v159, v159
	v_fma_f32 v158, v158, v186, v186
	v_rcp_f32_e32 v158, v158
	v_add_f32_e32 v159, 1.0, v159
	v_rcp_f32_e32 v159, v159
	v_cndmask_b32_e64 v160, v142, v212, s[0:1]
	v_fma_mix_f32 v161, v158, v160, v80 op_sel:[0,0,1] op_sel_hi:[0,0,1]
	v_exp_f32_e32 v161, v161
	s_add_u32 s48, s48, s40
	v_add_f32_e32 v161, 1.0, v161
	v_rcp_f32_e32 v161, v161
	s_addc_u32 s49, s49, s41
	v_fma_f32 v162, v161, -2.0, 1.0
	v_sub_f32_e32 v163, v176, v162
	v_fma_f32 v176, v159, v163, v162
	v_fma_f32 v164, |v176|, s17, v113
	v_fma_f32 v165, |v176|, s18, v114
	v_fma_f32 v166, |v176|, s19, v115
	v_lshrrev_b32_e32 v167, 26, v176
	v_min3_u32 v164, v164, v165, v166
	v_bfi_b32 v168, 31, v164, v167
	s_nop 1
	v_mul_u32_u24_dpp v170, v168, v180 quad_perm:[1,2,3,3] row_mask:0xf bank_mask:0xf bound_ctrl:1
	v_mad_u32_u24 v171, v168, v181, v170
	ds_write_b8_d16_hi v184, v171
	global_store_short_d16_hi v185, v176, s[48:49]
	s_waitcnt lgkmcnt(0)
	s_barrier
	ds_read_b64 v[122:123], v105 offset:0
	ds_read_b64 v[124:125], v105 offset:8
	ds_read_b64 v[126:127], v105 offset:16
	s_barrier
	ds_read_b64 v[128:129], v105 offset:96
	ds_read_b64 v[130:131], v105 offset:104
	ds_read_b64 v[132:133], v105 offset:112
	s_waitcnt lgkmcnt(3)
	v_mfma_f32_16x16x128_f8f6f4 v[134:137], v[122:127], v[2:7], 0 cbsz:2 blgp:2
	v_mfma_f32_16x16x128_f8f6f4 v[138:141], v[122:127], v[14:19], 0 cbsz:2 blgp:2
	v_mfma_f32_16x16x128_f8f6f4 v[142:145], v[122:127], v[26:31], v[188:191] cbsz:2 blgp:2
	v_mfma_f32_16x16x128_f8f6f4 v[204:207], v[122:127], v[38:43], 0 cbsz:2 blgp:2
	v_mfma_f32_16x16x128_f8f6f4 v[208:211], v[122:127], v[50:55], 0 cbsz:2 blgp:2
	v_mfma_f32_16x16x128_f8f6f4 v[212:215], v[122:127], v[62:67], v[188:191] cbsz:2 blgp:2
	s_waitcnt lgkmcnt(0)
	v_mfma_f32_16x16x128_f8f6f4 v[134:137], v[128:133], v[8:13], v[134:137] cbsz:2 blgp:2
	v_mfma_f32_16x16x128_f8f6f4 v[204:207], v[128:133], v[44:49], v[204:207] cbsz:2 blgp:2
	v_mfma_f32_16x16x128_f8f6f4 v[138:141], v[128:133], v[20:25], v[138:141] cbsz:2 blgp:2
	v_mfma_f32_16x16x128_f8f6f4 v[208:211], v[128:133], v[56:61], v[208:211] cbsz:2 blgp:2
	v_mfma_f32_16x16x128_f8f6f4 v[142:145], v[128:133], v[32:37], v[142:145] cbsz:2 blgp:2
	v_mfma_f32_16x16x128_f8f6f4 v[212:215], v[128:133], v[68:73], v[212:215] cbsz:2 blgp:2
	v_cndmask_b32_e64 v158, v134, v204, s[0:1]
	v_fma_mix_f32 v158, v158, v100, v85 op_sel_hi:[0,0,1]
	v_exp_f32_e32 v158, v158
	v_cndmask_b32_e64 v159, v138, v208, s[0:1]
	v_fma_mix_f32 v159, v159, v101, v77 op_sel_hi:[0,0,1]
	v_exp_f32_e32 v159, v159
	v_fma_f32 v158, v158, v186, v186
	v_rcp_f32_e32 v158, v158
	v_add_f32_e32 v159, 1.0, v159
	v_rcp_f32_e32 v159, v159
	v_cndmask_b32_e64 v160, v142, v212, s[0:1]
	v_fma_mix_f32 v161, v158, v160, v81 op_sel_hi:[0,0,1]
	v_exp_f32_e32 v161, v161
	s_add_u32 s48, s48, s40
	v_add_f32_e32 v161, 1.0, v161
	v_rcp_f32_e32 v161, v161
	s_addc_u32 s49, s49, s41
	v_fma_f32 v162, v161, -2.0, 1.0
	v_sub_f32_e32 v163, v176, v162
	v_fma_f32 v176, v159, v163, v162
	v_fma_f32 v164, |v176|, s17, v113
	v_fma_f32 v165, |v176|, s18, v114
	v_fma_f32 v166, |v176|, s19, v115
	v_lshrrev_b32_e32 v167, 26, v176
	v_min3_u32 v164, v164, v165, v166
	v_bfi_b32 v168, 31, v164, v167
	s_nop 1
	v_mul_u32_u24_dpp v170, v168, v180 quad_perm:[1,2,3,3] row_mask:0xf bank_mask:0xf bound_ctrl:1
	v_mad_u32_u24 v171, v168, v181, v170
	ds_write_b8_d16_hi v184, v171 offset:416
	global_store_short_d16_hi v185, v176, s[48:49]
	s_waitcnt lgkmcnt(0)
	s_barrier
	ds_read_b64 v[122:123], v105 offset:416
	ds_read_b64 v[124:125], v105 offset:424
	ds_read_b64 v[126:127], v105 offset:432
	s_barrier
	ds_read_b64 v[128:129], v105 offset:512
	ds_read_b64 v[130:131], v105 offset:520
	ds_read_b64 v[132:133], v105 offset:528
	s_waitcnt lgkmcnt(3)
	v_mfma_f32_16x16x128_f8f6f4 v[134:137], v[122:127], v[2:7], 0 cbsz:2 blgp:2
	v_mfma_f32_16x16x128_f8f6f4 v[138:141], v[122:127], v[14:19], 0 cbsz:2 blgp:2
	v_mfma_f32_16x16x128_f8f6f4 v[142:145], v[122:127], v[26:31], v[188:191] cbsz:2 blgp:2
	v_mfma_f32_16x16x128_f8f6f4 v[204:207], v[122:127], v[38:43], 0 cbsz:2 blgp:2
	v_mfma_f32_16x16x128_f8f6f4 v[208:211], v[122:127], v[50:55], 0 cbsz:2 blgp:2
	v_mfma_f32_16x16x128_f8f6f4 v[212:215], v[122:127], v[62:67], v[188:191] cbsz:2 blgp:2
	s_waitcnt lgkmcnt(0)
	v_mfma_f32_16x16x128_f8f6f4 v[134:137], v[128:133], v[8:13], v[134:137] cbsz:2 blgp:2
	v_mfma_f32_16x16x128_f8f6f4 v[204:207], v[128:133], v[44:49], v[204:207] cbsz:2 blgp:2
	v_mfma_f32_16x16x128_f8f6f4 v[138:141], v[128:133], v[20:25], v[138:141] cbsz:2 blgp:2
	v_mfma_f32_16x16x128_f8f6f4 v[208:211], v[128:133], v[56:61], v[208:211] cbsz:2 blgp:2
	v_mfma_f32_16x16x128_f8f6f4 v[142:145], v[128:133], v[32:37], v[142:145] cbsz:2 blgp:2
	v_mfma_f32_16x16x128_f8f6f4 v[212:215], v[128:133], v[68:73], v[212:215] cbsz:2 blgp:2
	v_cndmask_b32_e64 v158, v134, v204, s[0:1]
	v_fma_mix_f32 v158, v158, v100, v85 op_sel:[0,0,1] op_sel_hi:[0,0,1]
	v_exp_f32_e32 v158, v158
	v_cndmask_b32_e64 v159, v138, v208, s[0:1]
	v_fma_mix_f32 v159, v159, v101, v77 op_sel:[0,0,1] op_sel_hi:[0,0,1]
	v_exp_f32_e32 v159, v159
	v_fma_f32 v158, v158, v186, v186
	v_rcp_f32_e32 v158, v158
	v_add_f32_e32 v159, 1.0, v159
	v_rcp_f32_e32 v159, v159
	v_cndmask_b32_e64 v160, v142, v212, s[0:1]
	v_fma_mix_f32 v161, v158, v160, v81 op_sel:[0,0,1] op_sel_hi:[0,0,1]
	v_exp_f32_e32 v161, v161
	s_add_u32 s48, s48, s40
	v_add_f32_e32 v161, 1.0, v161
	v_rcp_f32_e32 v161, v161
	s_addc_u32 s49, s49, s41
	v_fma_f32 v162, v161, -2.0, 1.0
	v_sub_f32_e32 v163, v176, v162
	v_fma_f32 v176, v159, v163, v162
	v_fma_f32 v164, |v176|, s17, v113
	v_fma_f32 v165, |v176|, s18, v114
	v_fma_f32 v166, |v176|, s19, v115
	v_lshrrev_b32_e32 v167, 26, v176
	v_min3_u32 v164, v164, v165, v166
	v_bfi_b32 v168, 31, v164, v167
	s_nop 1
	v_mul_u32_u24_dpp v170, v168, v180 quad_perm:[1,2,3,3] row_mask:0xf bank_mask:0xf bound_ctrl:1
	v_mad_u32_u24 v171, v168, v181, v170
	ds_write_b8_d16_hi v184, v171
	global_store_short_d16_hi v185, v176, s[48:49]
	s_waitcnt lgkmcnt(0)
	s_barrier
	ds_read_b64 v[122:123], v105 offset:0
	ds_read_b64 v[124:125], v105 offset:8
	ds_read_b64 v[126:127], v105 offset:16
	s_barrier
	ds_read_b64 v[128:129], v105 offset:96
	ds_read_b64 v[130:131], v105 offset:104
	ds_read_b64 v[132:133], v105 offset:112
	s_waitcnt vmcnt(8)
	global_load_dwordx4 v[82:85], v[196:197], off
	global_load_dwordx4 v[74:77], v[196:197], off offset:512
	global_load_dwordx4 v[78:81], v[196:197], off offset:1024
	v_lshl_add_u64 v[196:197], v[196:197], 0, s[42:43]
	s_waitcnt lgkmcnt(3)
	v_mfma_f32_16x16x128_f8f6f4 v[134:137], v[122:127], v[2:7], 0 cbsz:2 blgp:2
	v_mfma_f32_16x16x128_f8f6f4 v[138:141], v[122:127], v[14:19], 0 cbsz:2 blgp:2
	v_mfma_f32_16x16x128_f8f6f4 v[142:145], v[122:127], v[26:31], v[188:191] cbsz:2 blgp:2
	v_mfma_f32_16x16x128_f8f6f4 v[204:207], v[122:127], v[38:43], 0 cbsz:2 blgp:2
	v_mfma_f32_16x16x128_f8f6f4 v[208:211], v[122:127], v[50:55], 0 cbsz:2 blgp:2
	v_mfma_f32_16x16x128_f8f6f4 v[212:215], v[122:127], v[62:67], v[188:191] cbsz:2 blgp:2
	s_waitcnt lgkmcnt(0)
	v_mfma_f32_16x16x128_f8f6f4 v[134:137], v[128:133], v[8:13], v[134:137] cbsz:2 blgp:2
	v_mfma_f32_16x16x128_f8f6f4 v[204:207], v[128:133], v[44:49], v[204:207] cbsz:2 blgp:2
	v_mfma_f32_16x16x128_f8f6f4 v[138:141], v[128:133], v[20:25], v[138:141] cbsz:2 blgp:2
	v_mfma_f32_16x16x128_f8f6f4 v[208:211], v[128:133], v[56:61], v[208:211] cbsz:2 blgp:2
	v_mfma_f32_16x16x128_f8f6f4 v[142:145], v[128:133], v[32:37], v[142:145] cbsz:2 blgp:2
	v_mfma_f32_16x16x128_f8f6f4 v[212:215], v[128:133], v[68:73], v[212:215] cbsz:2 blgp:2
	v_cndmask_b32_e64 v158, v134, v204, s[0:1]
	v_fma_mix_f32 v158, v158, v100, v146 op_sel_hi:[0,0,1]
	v_exp_f32_e32 v158, v158
	v_cndmask_b32_e64 v159, v138, v208, s[0:1]
	v_fma_mix_f32 v159, v159, v101, v150 op_sel_hi:[0,0,1]
	v_exp_f32_e32 v159, v159
	v_fma_f32 v158, v158, v186, v186
	v_rcp_f32_e32 v158, v158
	v_add_f32_e32 v159, 1.0, v159
	v_rcp_f32_e32 v159, v159
	v_cndmask_b32_e64 v160, v142, v212, s[0:1]
	v_fma_mix_f32 v161, v158, v160, v154 op_sel_hi:[0,0,1]
	v_exp_f32_e32 v161, v161
	s_add_u32 s48, s48, s40
	v_add_f32_e32 v161, 1.0, v161
	v_rcp_f32_e32 v161, v161
	s_addc_u32 s49, s49, s41
	v_fma_f32 v162, v161, -2.0, 1.0
	v_sub_f32_e32 v163, v176, v162
	v_fma_f32 v176, v159, v163, v162
	v_fma_f32 v164, |v176|, s17, v113
	v_fma_f32 v165, |v176|, s18, v114
	v_fma_f32 v166, |v176|, s19, v115
	v_lshrrev_b32_e32 v167, 26, v176
	v_min3_u32 v164, v164, v165, v166
	v_bfi_b32 v168, 31, v164, v167
	s_nop 1
	v_mul_u32_u24_dpp v170, v168, v180 quad_perm:[1,2,3,3] row_mask:0xf bank_mask:0xf bound_ctrl:1
	v_mad_u32_u24 v171, v168, v181, v170
	ds_write_b8_d16_hi v184, v171 offset:416
	global_store_short_d16_hi v185, v176, s[48:49]
	s_waitcnt lgkmcnt(0)
	s_barrier
	ds_read_b64 v[122:123], v105 offset:416
	ds_read_b64 v[124:125], v105 offset:424
	ds_read_b64 v[126:127], v105 offset:432
	s_barrier
	ds_read_b64 v[128:129], v105 offset:512
	ds_read_b64 v[130:131], v105 offset:520
	ds_read_b64 v[132:133], v105 offset:528
	s_waitcnt lgkmcnt(3)
	v_mfma_f32_16x16x128_f8f6f4 v[134:137], v[122:127], v[2:7], 0 cbsz:2 blgp:2
	v_mfma_f32_16x16x128_f8f6f4 v[138:141], v[122:127], v[14:19], 0 cbsz:2 blgp:2
	v_mfma_f32_16x16x128_f8f6f4 v[142:145], v[122:127], v[26:31], v[188:191] cbsz:2 blgp:2
	v_mfma_f32_16x16x128_f8f6f4 v[204:207], v[122:127], v[38:43], 0 cbsz:2 blgp:2
	v_mfma_f32_16x16x128_f8f6f4 v[208:211], v[122:127], v[50:55], 0 cbsz:2 blgp:2
	v_mfma_f32_16x16x128_f8f6f4 v[212:215], v[122:127], v[62:67], v[188:191] cbsz:2 blgp:2
	s_waitcnt lgkmcnt(0)
	v_mfma_f32_16x16x128_f8f6f4 v[134:137], v[128:133], v[8:13], v[134:137] cbsz:2 blgp:2
	v_mfma_f32_16x16x128_f8f6f4 v[204:207], v[128:133], v[44:49], v[204:207] cbsz:2 blgp:2
	v_mfma_f32_16x16x128_f8f6f4 v[138:141], v[128:133], v[20:25], v[138:141] cbsz:2 blgp:2
	v_mfma_f32_16x16x128_f8f6f4 v[208:211], v[128:133], v[56:61], v[208:211] cbsz:2 blgp:2
	v_mfma_f32_16x16x128_f8f6f4 v[142:145], v[128:133], v[32:37], v[142:145] cbsz:2 blgp:2
	v_mfma_f32_16x16x128_f8f6f4 v[212:215], v[128:133], v[68:73], v[212:215] cbsz:2 blgp:2
	v_cndmask_b32_e64 v158, v134, v204, s[0:1]
	v_fma_mix_f32 v158, v158, v100, v146 op_sel:[0,0,1] op_sel_hi:[0,0,1]
	v_exp_f32_e32 v158, v158
	v_cndmask_b32_e64 v159, v138, v208, s[0:1]
	v_fma_mix_f32 v159, v159, v101, v150 op_sel:[0,0,1] op_sel_hi:[0,0,1]
	v_exp_f32_e32 v159, v159
	v_fma_f32 v158, v158, v186, v186
	v_rcp_f32_e32 v158, v158
	v_add_f32_e32 v159, 1.0, v159
	v_rcp_f32_e32 v159, v159
	v_cndmask_b32_e64 v160, v142, v212, s[0:1]
	v_fma_mix_f32 v161, v158, v160, v154 op_sel:[0,0,1] op_sel_hi:[0,0,1]
	v_exp_f32_e32 v161, v161
	s_add_u32 s48, s48, s40
	v_add_f32_e32 v161, 1.0, v161
	v_rcp_f32_e32 v161, v161
	s_addc_u32 s49, s49, s41
	v_fma_f32 v162, v161, -2.0, 1.0
	v_sub_f32_e32 v163, v176, v162
	v_fma_f32 v176, v159, v163, v162
	v_fma_f32 v164, |v176|, s17, v113
	v_fma_f32 v165, |v176|, s18, v114
	v_fma_f32 v166, |v176|, s19, v115
	v_lshrrev_b32_e32 v167, 26, v176
	v_min3_u32 v164, v164, v165, v166
	v_bfi_b32 v168, 31, v164, v167
	s_nop 1
	v_mul_u32_u24_dpp v170, v168, v180 quad_perm:[1,2,3,3] row_mask:0xf bank_mask:0xf bound_ctrl:1
	v_mad_u32_u24 v171, v168, v181, v170
	ds_write_b8_d16_hi v184, v171
	global_store_short_d16_hi v185, v176, s[48:49]
	s_waitcnt lgkmcnt(0)
	s_barrier
	ds_read_b64 v[122:123], v105 offset:0
	ds_read_b64 v[124:125], v105 offset:8
	ds_read_b64 v[126:127], v105 offset:16
	s_barrier
	ds_read_b64 v[128:129], v105 offset:96
	ds_read_b64 v[130:131], v105 offset:104
	ds_read_b64 v[132:133], v105 offset:112
	s_waitcnt lgkmcnt(3)
	v_mfma_f32_16x16x128_f8f6f4 v[134:137], v[122:127], v[2:7], 0 cbsz:2 blgp:2
	v_mfma_f32_16x16x128_f8f6f4 v[138:141], v[122:127], v[14:19], 0 cbsz:2 blgp:2
	v_mfma_f32_16x16x128_f8f6f4 v[142:145], v[122:127], v[26:31], v[188:191] cbsz:2 blgp:2
	v_mfma_f32_16x16x128_f8f6f4 v[204:207], v[122:127], v[38:43], 0 cbsz:2 blgp:2
	v_mfma_f32_16x16x128_f8f6f4 v[208:211], v[122:127], v[50:55], 0 cbsz:2 blgp:2
	v_mfma_f32_16x16x128_f8f6f4 v[212:215], v[122:127], v[62:67], v[188:191] cbsz:2 blgp:2
	s_waitcnt lgkmcnt(0)
	v_mfma_f32_16x16x128_f8f6f4 v[134:137], v[128:133], v[8:13], v[134:137] cbsz:2 blgp:2
	v_mfma_f32_16x16x128_f8f6f4 v[204:207], v[128:133], v[44:49], v[204:207] cbsz:2 blgp:2
	v_mfma_f32_16x16x128_f8f6f4 v[138:141], v[128:133], v[20:25], v[138:141] cbsz:2 blgp:2
	v_mfma_f32_16x16x128_f8f6f4 v[208:211], v[128:133], v[56:61], v[208:211] cbsz:2 blgp:2
	v_mfma_f32_16x16x128_f8f6f4 v[142:145], v[128:133], v[32:37], v[142:145] cbsz:2 blgp:2
	v_mfma_f32_16x16x128_f8f6f4 v[212:215], v[128:133], v[68:73], v[212:215] cbsz:2 blgp:2
	v_cndmask_b32_e64 v158, v134, v204, s[0:1]
	v_fma_mix_f32 v158, v158, v100, v147 op_sel_hi:[0,0,1]
	v_exp_f32_e32 v158, v158
	v_cndmask_b32_e64 v159, v138, v208, s[0:1]
	v_fma_mix_f32 v159, v159, v101, v151 op_sel_hi:[0,0,1]
	v_exp_f32_e32 v159, v159
	v_fma_f32 v158, v158, v186, v186
	v_rcp_f32_e32 v158, v158
	v_add_f32_e32 v159, 1.0, v159
	v_rcp_f32_e32 v159, v159
	v_cndmask_b32_e64 v160, v142, v212, s[0:1]
	v_fma_mix_f32 v161, v158, v160, v155 op_sel_hi:[0,0,1]
	v_exp_f32_e32 v161, v161
	s_add_u32 s48, s48, s40
	v_add_f32_e32 v161, 1.0, v161
	v_rcp_f32_e32 v161, v161
	s_addc_u32 s49, s49, s41
	v_fma_f32 v162, v161, -2.0, 1.0
	v_sub_f32_e32 v163, v176, v162
	v_fma_f32 v176, v159, v163, v162
	v_fma_f32 v164, |v176|, s17, v113
	v_fma_f32 v165, |v176|, s18, v114
	v_fma_f32 v166, |v176|, s19, v115
	v_lshrrev_b32_e32 v167, 26, v176
	v_min3_u32 v164, v164, v165, v166
	v_bfi_b32 v168, 31, v164, v167
	s_nop 1
	v_mul_u32_u24_dpp v170, v168, v180 quad_perm:[1,2,3,3] row_mask:0xf bank_mask:0xf bound_ctrl:1
	v_mad_u32_u24 v171, v168, v181, v170
	ds_write_b8_d16_hi v184, v171 offset:416
	global_store_short_d16_hi v185, v176, s[48:49]
	s_waitcnt lgkmcnt(0)
	s_barrier
	ds_read_b64 v[122:123], v105 offset:416
	ds_read_b64 v[124:125], v105 offset:424
	ds_read_b64 v[126:127], v105 offset:432
	s_barrier
	ds_read_b64 v[128:129], v105 offset:512
	ds_read_b64 v[130:131], v105 offset:520
	ds_read_b64 v[132:133], v105 offset:528
	s_waitcnt lgkmcnt(3)
	v_mfma_f32_16x16x128_f8f6f4 v[134:137], v[122:127], v[2:7], 0 cbsz:2 blgp:2
	v_mfma_f32_16x16x128_f8f6f4 v[138:141], v[122:127], v[14:19], 0 cbsz:2 blgp:2
	v_mfma_f32_16x16x128_f8f6f4 v[142:145], v[122:127], v[26:31], v[188:191] cbsz:2 blgp:2
	v_mfma_f32_16x16x128_f8f6f4 v[204:207], v[122:127], v[38:43], 0 cbsz:2 blgp:2
	v_mfma_f32_16x16x128_f8f6f4 v[208:211], v[122:127], v[50:55], 0 cbsz:2 blgp:2
	v_mfma_f32_16x16x128_f8f6f4 v[212:215], v[122:127], v[62:67], v[188:191] cbsz:2 blgp:2
	s_waitcnt lgkmcnt(0)
	v_mfma_f32_16x16x128_f8f6f4 v[134:137], v[128:133], v[8:13], v[134:137] cbsz:2 blgp:2
	v_mfma_f32_16x16x128_f8f6f4 v[204:207], v[128:133], v[44:49], v[204:207] cbsz:2 blgp:2
	v_mfma_f32_16x16x128_f8f6f4 v[138:141], v[128:133], v[20:25], v[138:141] cbsz:2 blgp:2
	v_mfma_f32_16x16x128_f8f6f4 v[208:211], v[128:133], v[56:61], v[208:211] cbsz:2 blgp:2
	v_mfma_f32_16x16x128_f8f6f4 v[142:145], v[128:133], v[32:37], v[142:145] cbsz:2 blgp:2
	v_mfma_f32_16x16x128_f8f6f4 v[212:215], v[128:133], v[68:73], v[212:215] cbsz:2 blgp:2
	v_cndmask_b32_e64 v158, v134, v204, s[0:1]
	v_fma_mix_f32 v158, v158, v100, v147 op_sel:[0,0,1] op_sel_hi:[0,0,1]
	v_exp_f32_e32 v158, v158
	v_cndmask_b32_e64 v159, v138, v208, s[0:1]
	v_fma_mix_f32 v159, v159, v101, v151 op_sel:[0,0,1] op_sel_hi:[0,0,1]
	v_exp_f32_e32 v159, v159
	v_fma_f32 v158, v158, v186, v186
	v_rcp_f32_e32 v158, v158
	v_add_f32_e32 v159, 1.0, v159
	v_rcp_f32_e32 v159, v159
	v_cndmask_b32_e64 v160, v142, v212, s[0:1]
	v_fma_mix_f32 v161, v158, v160, v155 op_sel:[0,0,1] op_sel_hi:[0,0,1]
	v_exp_f32_e32 v161, v161
	s_add_u32 s48, s48, s40
	v_add_f32_e32 v161, 1.0, v161
	v_rcp_f32_e32 v161, v161
	s_addc_u32 s49, s49, s41
	v_fma_f32 v162, v161, -2.0, 1.0
	v_sub_f32_e32 v163, v176, v162
	v_fma_f32 v176, v159, v163, v162
	v_fma_f32 v164, |v176|, s17, v113
	v_fma_f32 v165, |v176|, s18, v114
	v_fma_f32 v166, |v176|, s19, v115
	v_lshrrev_b32_e32 v167, 26, v176
	v_min3_u32 v164, v164, v165, v166
	v_bfi_b32 v168, 31, v164, v167
	s_nop 1
	v_mul_u32_u24_dpp v170, v168, v180 quad_perm:[1,2,3,3] row_mask:0xf bank_mask:0xf bound_ctrl:1
	v_mad_u32_u24 v171, v168, v181, v170
	ds_write_b8_d16_hi v184, v171
	global_store_short_d16_hi v185, v176, s[48:49]
	s_waitcnt lgkmcnt(0)
	s_barrier
	ds_read_b64 v[122:123], v105 offset:0
	ds_read_b64 v[124:125], v105 offset:8
	ds_read_b64 v[126:127], v105 offset:16
	s_barrier
	ds_read_b64 v[128:129], v105 offset:96
	ds_read_b64 v[130:131], v105 offset:104
	ds_read_b64 v[132:133], v105 offset:112
	s_waitcnt lgkmcnt(3)
	v_mfma_f32_16x16x128_f8f6f4 v[134:137], v[122:127], v[2:7], 0 cbsz:2 blgp:2
	v_mfma_f32_16x16x128_f8f6f4 v[138:141], v[122:127], v[14:19], 0 cbsz:2 blgp:2
	v_mfma_f32_16x16x128_f8f6f4 v[142:145], v[122:127], v[26:31], v[188:191] cbsz:2 blgp:2
	v_mfma_f32_16x16x128_f8f6f4 v[204:207], v[122:127], v[38:43], 0 cbsz:2 blgp:2
	v_mfma_f32_16x16x128_f8f6f4 v[208:211], v[122:127], v[50:55], 0 cbsz:2 blgp:2
	v_mfma_f32_16x16x128_f8f6f4 v[212:215], v[122:127], v[62:67], v[188:191] cbsz:2 blgp:2
	s_waitcnt lgkmcnt(0)
	v_mfma_f32_16x16x128_f8f6f4 v[134:137], v[128:133], v[8:13], v[134:137] cbsz:2 blgp:2
	v_mfma_f32_16x16x128_f8f6f4 v[204:207], v[128:133], v[44:49], v[204:207] cbsz:2 blgp:2
	v_mfma_f32_16x16x128_f8f6f4 v[138:141], v[128:133], v[20:25], v[138:141] cbsz:2 blgp:2
	v_mfma_f32_16x16x128_f8f6f4 v[208:211], v[128:133], v[56:61], v[208:211] cbsz:2 blgp:2
	v_mfma_f32_16x16x128_f8f6f4 v[142:145], v[128:133], v[32:37], v[142:145] cbsz:2 blgp:2
	v_mfma_f32_16x16x128_f8f6f4 v[212:215], v[128:133], v[68:73], v[212:215] cbsz:2 blgp:2
	v_cndmask_b32_e64 v158, v134, v204, s[0:1]
	v_fma_mix_f32 v158, v158, v100, v148 op_sel_hi:[0,0,1]
	v_exp_f32_e32 v158, v158
	v_cndmask_b32_e64 v159, v138, v208, s[0:1]
	v_fma_mix_f32 v159, v159, v101, v152 op_sel_hi:[0,0,1]
	v_exp_f32_e32 v159, v159
	v_fma_f32 v158, v158, v186, v186
	v_rcp_f32_e32 v158, v158
	v_add_f32_e32 v159, 1.0, v159
	v_rcp_f32_e32 v159, v159
	v_cndmask_b32_e64 v160, v142, v212, s[0:1]
	v_fma_mix_f32 v161, v158, v160, v156 op_sel_hi:[0,0,1]
	v_exp_f32_e32 v161, v161
	s_add_u32 s48, s48, s40
	v_add_f32_e32 v161, 1.0, v161
	v_rcp_f32_e32 v161, v161
	s_addc_u32 s49, s49, s41
	v_fma_f32 v162, v161, -2.0, 1.0
	v_sub_f32_e32 v163, v176, v162
	v_fma_f32 v176, v159, v163, v162
	v_fma_f32 v164, |v176|, s17, v113
	v_fma_f32 v165, |v176|, s18, v114
	v_fma_f32 v166, |v176|, s19, v115
	v_lshrrev_b32_e32 v167, 26, v176
	v_min3_u32 v164, v164, v165, v166
	v_bfi_b32 v168, 31, v164, v167
	s_nop 1
	v_mul_u32_u24_dpp v170, v168, v180 quad_perm:[1,2,3,3] row_mask:0xf bank_mask:0xf bound_ctrl:1
	v_mad_u32_u24 v171, v168, v181, v170
	ds_write_b8_d16_hi v184, v171 offset:416
	global_store_short_d16_hi v185, v176, s[48:49]
	s_waitcnt lgkmcnt(0)
	s_barrier
	ds_read_b64 v[122:123], v105 offset:416
	ds_read_b64 v[124:125], v105 offset:424
	ds_read_b64 v[126:127], v105 offset:432
	s_barrier
	ds_read_b64 v[128:129], v105 offset:512
	ds_read_b64 v[130:131], v105 offset:520
	ds_read_b64 v[132:133], v105 offset:528
	s_waitcnt lgkmcnt(3)
	v_mfma_f32_16x16x128_f8f6f4 v[134:137], v[122:127], v[2:7], 0 cbsz:2 blgp:2
	v_mfma_f32_16x16x128_f8f6f4 v[138:141], v[122:127], v[14:19], 0 cbsz:2 blgp:2
	v_mfma_f32_16x16x128_f8f6f4 v[142:145], v[122:127], v[26:31], v[188:191] cbsz:2 blgp:2
	v_mfma_f32_16x16x128_f8f6f4 v[204:207], v[122:127], v[38:43], 0 cbsz:2 blgp:2
	v_mfma_f32_16x16x128_f8f6f4 v[208:211], v[122:127], v[50:55], 0 cbsz:2 blgp:2
	v_mfma_f32_16x16x128_f8f6f4 v[212:215], v[122:127], v[62:67], v[188:191] cbsz:2 blgp:2
	s_waitcnt lgkmcnt(0)
	v_mfma_f32_16x16x128_f8f6f4 v[134:137], v[128:133], v[8:13], v[134:137] cbsz:2 blgp:2
	v_mfma_f32_16x16x128_f8f6f4 v[204:207], v[128:133], v[44:49], v[204:207] cbsz:2 blgp:2
	v_mfma_f32_16x16x128_f8f6f4 v[138:141], v[128:133], v[20:25], v[138:141] cbsz:2 blgp:2
	v_mfma_f32_16x16x128_f8f6f4 v[208:211], v[128:133], v[56:61], v[208:211] cbsz:2 blgp:2
	v_mfma_f32_16x16x128_f8f6f4 v[142:145], v[128:133], v[32:37], v[142:145] cbsz:2 blgp:2
	v_mfma_f32_16x16x128_f8f6f4 v[212:215], v[128:133], v[68:73], v[212:215] cbsz:2 blgp:2
	v_cndmask_b32_e64 v158, v134, v204, s[0:1]
	v_fma_mix_f32 v158, v158, v100, v148 op_sel:[0,0,1] op_sel_hi:[0,0,1]
	v_exp_f32_e32 v158, v158
	v_cndmask_b32_e64 v159, v138, v208, s[0:1]
	v_fma_mix_f32 v159, v159, v101, v152 op_sel:[0,0,1] op_sel_hi:[0,0,1]
	v_exp_f32_e32 v159, v159
	v_fma_f32 v158, v158, v186, v186
	v_rcp_f32_e32 v158, v158
	v_add_f32_e32 v159, 1.0, v159
	v_rcp_f32_e32 v159, v159
	v_cndmask_b32_e64 v160, v142, v212, s[0:1]
	v_fma_mix_f32 v161, v158, v160, v156 op_sel:[0,0,1] op_sel_hi:[0,0,1]
	v_exp_f32_e32 v161, v161
	s_add_u32 s48, s48, s40
	v_add_f32_e32 v161, 1.0, v161
	v_rcp_f32_e32 v161, v161
	s_addc_u32 s49, s49, s41
	v_fma_f32 v162, v161, -2.0, 1.0
	v_sub_f32_e32 v163, v176, v162
	v_fma_f32 v176, v159, v163, v162
	v_fma_f32 v164, |v176|, s17, v113
	v_fma_f32 v165, |v176|, s18, v114
	v_fma_f32 v166, |v176|, s19, v115
	v_lshrrev_b32_e32 v167, 26, v176
	v_min3_u32 v164, v164, v165, v166
	v_bfi_b32 v168, 31, v164, v167
	s_nop 1
	v_mul_u32_u24_dpp v170, v168, v180 quad_perm:[1,2,3,3] row_mask:0xf bank_mask:0xf bound_ctrl:1
	v_mad_u32_u24 v171, v168, v181, v170
	ds_write_b8_d16_hi v184, v171
	global_store_short_d16_hi v185, v176, s[48:49]
	s_waitcnt lgkmcnt(0)
	s_barrier
	ds_read_b64 v[122:123], v105 offset:0
	ds_read_b64 v[124:125], v105 offset:8
	ds_read_b64 v[126:127], v105 offset:16
	s_barrier
	ds_read_b64 v[128:129], v105 offset:96
	ds_read_b64 v[130:131], v105 offset:104
	ds_read_b64 v[132:133], v105 offset:112
	s_waitcnt lgkmcnt(3)
	v_mfma_f32_16x16x128_f8f6f4 v[134:137], v[122:127], v[2:7], 0 cbsz:2 blgp:2
	v_mfma_f32_16x16x128_f8f6f4 v[138:141], v[122:127], v[14:19], 0 cbsz:2 blgp:2
	v_mfma_f32_16x16x128_f8f6f4 v[142:145], v[122:127], v[26:31], v[188:191] cbsz:2 blgp:2
	v_mfma_f32_16x16x128_f8f6f4 v[204:207], v[122:127], v[38:43], 0 cbsz:2 blgp:2
	v_mfma_f32_16x16x128_f8f6f4 v[208:211], v[122:127], v[50:55], 0 cbsz:2 blgp:2
	v_mfma_f32_16x16x128_f8f6f4 v[212:215], v[122:127], v[62:67], v[188:191] cbsz:2 blgp:2
	s_waitcnt lgkmcnt(0)
	v_mfma_f32_16x16x128_f8f6f4 v[134:137], v[128:133], v[8:13], v[134:137] cbsz:2 blgp:2
	v_mfma_f32_16x16x128_f8f6f4 v[204:207], v[128:133], v[44:49], v[204:207] cbsz:2 blgp:2
	v_mfma_f32_16x16x128_f8f6f4 v[138:141], v[128:133], v[20:25], v[138:141] cbsz:2 blgp:2
	v_mfma_f32_16x16x128_f8f6f4 v[208:211], v[128:133], v[56:61], v[208:211] cbsz:2 blgp:2
	v_mfma_f32_16x16x128_f8f6f4 v[142:145], v[128:133], v[32:37], v[142:145] cbsz:2 blgp:2
	v_mfma_f32_16x16x128_f8f6f4 v[212:215], v[128:133], v[68:73], v[212:215] cbsz:2 blgp:2
	v_cndmask_b32_e64 v158, v134, v204, s[0:1]
	v_fma_mix_f32 v158, v158, v100, v149 op_sel_hi:[0,0,1]
	v_exp_f32_e32 v158, v158
	v_cndmask_b32_e64 v159, v138, v208, s[0:1]
	v_fma_mix_f32 v159, v159, v101, v153 op_sel_hi:[0,0,1]
	v_exp_f32_e32 v159, v159
	v_fma_f32 v158, v158, v186, v186
	v_rcp_f32_e32 v158, v158
	v_add_f32_e32 v159, 1.0, v159
	v_rcp_f32_e32 v159, v159
	v_cndmask_b32_e64 v160, v142, v212, s[0:1]
	v_fma_mix_f32 v161, v158, v160, v157 op_sel_hi:[0,0,1]
	v_exp_f32_e32 v161, v161
	s_add_u32 s48, s48, s40
	v_add_f32_e32 v161, 1.0, v161
	v_rcp_f32_e32 v161, v161
	s_addc_u32 s49, s49, s41
	v_fma_f32 v162, v161, -2.0, 1.0
	v_sub_f32_e32 v163, v176, v162
	v_fma_f32 v176, v159, v163, v162
	v_fma_f32 v164, |v176|, s17, v113
	v_fma_f32 v165, |v176|, s18, v114
	v_fma_f32 v166, |v176|, s19, v115
	v_lshrrev_b32_e32 v167, 26, v176
	v_min3_u32 v164, v164, v165, v166
	v_bfi_b32 v168, 31, v164, v167
	s_nop 1
	v_mul_u32_u24_dpp v170, v168, v180 quad_perm:[1,2,3,3] row_mask:0xf bank_mask:0xf bound_ctrl:1
	v_mad_u32_u24 v171, v168, v181, v170
	ds_write_b8_d16_hi v184, v171 offset:416
	global_store_short_d16_hi v185, v176, s[48:49]
	s_waitcnt lgkmcnt(0)
	s_barrier
	ds_read_b64 v[122:123], v105 offset:416
	ds_read_b64 v[124:125], v105 offset:424
	ds_read_b64 v[126:127], v105 offset:432
	s_barrier
	ds_read_b64 v[128:129], v105 offset:512
	ds_read_b64 v[130:131], v105 offset:520
	ds_read_b64 v[132:133], v105 offset:528
	s_add_i32 s44, s44, 16
	s_waitcnt lgkmcnt(3)
	v_mfma_f32_16x16x128_f8f6f4 v[134:137], v[122:127], v[2:7], 0 cbsz:2 blgp:2
	v_mfma_f32_16x16x128_f8f6f4 v[138:141], v[122:127], v[14:19], 0 cbsz:2 blgp:2
	v_mfma_f32_16x16x128_f8f6f4 v[142:145], v[122:127], v[26:31], v[188:191] cbsz:2 blgp:2
	v_mfma_f32_16x16x128_f8f6f4 v[204:207], v[122:127], v[38:43], 0 cbsz:2 blgp:2
	v_mfma_f32_16x16x128_f8f6f4 v[208:211], v[122:127], v[50:55], 0 cbsz:2 blgp:2
	v_mfma_f32_16x16x128_f8f6f4 v[212:215], v[122:127], v[62:67], v[188:191] cbsz:2 blgp:2
	s_waitcnt lgkmcnt(0)
	v_mfma_f32_16x16x128_f8f6f4 v[134:137], v[128:133], v[8:13], v[134:137] cbsz:2 blgp:2
	v_mfma_f32_16x16x128_f8f6f4 v[204:207], v[128:133], v[44:49], v[204:207] cbsz:2 blgp:2
	v_mfma_f32_16x16x128_f8f6f4 v[138:141], v[128:133], v[20:25], v[138:141] cbsz:2 blgp:2
	v_mfma_f32_16x16x128_f8f6f4 v[208:211], v[128:133], v[56:61], v[208:211] cbsz:2 blgp:2
	v_mfma_f32_16x16x128_f8f6f4 v[142:145], v[128:133], v[32:37], v[142:145] cbsz:2 blgp:2
	v_mfma_f32_16x16x128_f8f6f4 v[212:215], v[128:133], v[68:73], v[212:215] cbsz:2 blgp:2
	v_cndmask_b32_e64 v158, v134, v204, s[0:1]
	v_fma_mix_f32 v158, v158, v100, v149 op_sel:[0,0,1] op_sel_hi:[0,0,1]
	v_exp_f32_e32 v158, v158
	v_cndmask_b32_e64 v159, v138, v208, s[0:1]
	v_fma_mix_f32 v159, v159, v101, v153 op_sel:[0,0,1] op_sel_hi:[0,0,1]
	v_exp_f32_e32 v159, v159
	v_fma_f32 v158, v158, v186, v186
	v_rcp_f32_e32 v158, v158
	v_add_f32_e32 v159, 1.0, v159
	v_rcp_f32_e32 v159, v159
	v_cndmask_b32_e64 v160, v142, v212, s[0:1]
	v_fma_mix_f32 v161, v158, v160, v157 op_sel:[0,0,1] op_sel_hi:[0,0,1]
	v_exp_f32_e32 v161, v161
	s_add_u32 s48, s48, s40
	v_add_f32_e32 v161, 1.0, v161
	v_rcp_f32_e32 v161, v161
	s_addc_u32 s49, s49, s41
	v_fma_f32 v162, v161, -2.0, 1.0
	v_sub_f32_e32 v163, v176, v162
	v_fma_f32 v176, v159, v163, v162
	v_fma_f32 v164, |v176|, s17, v113
	v_fma_f32 v165, |v176|, s18, v114
	v_fma_f32 v166, |v176|, s19, v115
	v_lshrrev_b32_e32 v167, 26, v176
	v_min3_u32 v164, v164, v165, v166
	v_bfi_b32 v168, 31, v164, v167
	s_nop 1
	v_mul_u32_u24_dpp v170, v168, v180 quad_perm:[1,2,3,3] row_mask:0xf bank_mask:0xf bound_ctrl:1
	v_mad_u32_u24 v171, v168, v181, v170
	ds_write_b8_d16_hi v184, v171
	global_store_short_d16_hi v185, v176, s[48:49]
	s_waitcnt lgkmcnt(0)
	s_barrier
	ds_read_b64 v[122:123], v105 offset:0
	ds_read_b64 v[124:125], v105 offset:8
	ds_read_b64 v[126:127], v105 offset:16
	s_cmp_lt_i32 s44, s45
	s_barrier
	s_cbranch_scc1 .Lscan_loop_a_f2
	s_branch .Lscan_exit_f2
.Lscan_loop_b_f2:
	ds_read_b64 v[122:123], v105 offset:0
	ds_read_b64 v[124:125], v105 offset:8
	ds_read_b64 v[126:127], v105 offset:16
	ds_read_b64 v[128:129], v105 offset:96
	ds_read_b64 v[130:131], v105 offset:104
	ds_read_b64 v[132:133], v105 offset:112
	s_waitcnt vmcnt(8)
	global_load_dwordx4 v[146:149], v[196:197], off
	global_load_dwordx4 v[150:153], v[196:197], off offset:512
	global_load_dwordx4 v[154:157], v[196:197], off offset:1024
	v_lshl_add_u64 v[196:197], v[196:197], 0, s[42:43]
	s_waitcnt lgkmcnt(3)
	v_mfma_f32_16x16x128_f8f6f4 v[134:137], v[122:127], v[2:7], 0 cbsz:2 blgp:2
	v_mfma_f32_16x16x128_f8f6f4 v[138:141], v[122:127], v[14:19], 0 cbsz:2 blgp:2
	v_mfma_f32_16x16x128_f8f6f4 v[142:145], v[122:127], v[26:31], v[188:191] cbsz:2 blgp:2
	v_mfma_f32_16x16x128_f8f6f4 v[204:207], v[122:127], v[38:43], 0 cbsz:2 blgp:2
	v_mfma_f32_16x16x128_f8f6f4 v[208:211], v[122:127], v[50:55], 0 cbsz:2 blgp:2
	v_mfma_f32_16x16x128_f8f6f4 v[212:215], v[122:127], v[62:67], v[188:191] cbsz:2 blgp:2
	s_waitcnt lgkmcnt(0)
	v_mfma_f32_16x16x128_f8f6f4 v[134:137], v[128:133], v[8:13], v[134:137] cbsz:2 blgp:2
	v_mfma_f32_16x16x128_f8f6f4 v[204:207], v[128:133], v[44:49], v[204:207] cbsz:2 blgp:2
	v_mfma_f32_16x16x128_f8f6f4 v[138:141], v[128:133], v[20:25], v[138:141] cbsz:2 blgp:2
	v_mfma_f32_16x16x128_f8f6f4 v[208:211], v[128:133], v[56:61], v[208:211] cbsz:2 blgp:2
	v_mfma_f32_16x16x128_f8f6f4 v[142:145], v[128:133], v[32:37], v[142:145] cbsz:2 blgp:2
	v_mfma_f32_16x16x128_f8f6f4 v[212:215], v[128:133], v[68:73], v[212:215] cbsz:2 blgp:2
	v_cndmask_b32_e64 v158, v134, v204, s[0:1]
	v_fma_mix_f32 v158, v158, v100, v82 op_sel_hi:[0,0,1]
	v_exp_f32_e32 v158, v158
	v_cndmask_b32_e64 v159, v138, v208, s[0:1]
	v_fma_mix_f32 v159, v159, v101, v74 op_sel_hi:[0,0,1]
	v_exp_f32_e32 v159, v159
	v_fma_f32 v158, v158, v186, v186
	v_rcp_f32_e32 v158, v158
	v_add_f32_e32 v159, 1.0, v159
	v_rcp_f32_e32 v159, v159
	v_cndmask_b32_e64 v160, v142, v212, s[0:1]
	v_fma_mix_f32 v161, v158, v160, v78 op_sel_hi:[0,0,1]
	v_exp_f32_e32 v161, v161
	s_add_u32 s48, s48, s40
	v_add_f32_e32 v161, 1.0, v161
	v_rcp_f32_e32 v161, v161
	s_addc_u32 s49, s49, s41
	v_fma_f32 v162, v161, -2.0, 1.0
	v_sub_f32_e32 v163, v176, v162
	v_fma_f32 v176, v159, v163, v162
	v_fma_f32 v164, |v176|, s17, v113
	v_fma_f32 v165, |v176|, s18, v114
	v_fma_f32 v166, |v176|, s19, v115
	v_lshrrev_b32_e32 v167, 26, v176
	v_min3_u32 v164, v164, v165, v166
	v_bfi_b32 v168, 31, v164, v167
	s_nop 1
	v_mul_u32_u24_dpp v170, v168, v180 quad_perm:[1,2,3,3] row_mask:0xf bank_mask:0xf bound_ctrl:1
	v_mad_u32_u24 v171, v168, v181, v170
	ds_write_b8_d16_hi v184, v171 offset:416
	s_barrier
	global_store_short_d16_hi v185, v176, s[48:49]
	s_waitcnt lgkmcnt(0)
	s_barrier
	ds_read_b64 v[122:123], v105 offset:416
	ds_read_b64 v[124:125], v105 offset:424
	ds_read_b64 v[126:127], v105 offset:432
	ds_read_b64 v[128:129], v105 offset:512
	ds_read_b64 v[130:131], v105 offset:520
	ds_read_b64 v[132:133], v105 offset:528
	s_waitcnt lgkmcnt(3)
	v_mfma_f32_16x16x128_f8f6f4 v[134:137], v[122:127], v[2:7], 0 cbsz:2 blgp:2
	v_mfma_f32_16x16x128_f8f6f4 v[138:141], v[122:127], v[14:19], 0 cbsz:2 blgp:2
	v_mfma_f32_16x16x128_f8f6f4 v[142:145], v[122:127], v[26:31], v[188:191] cbsz:2 blgp:2
	v_mfma_f32_16x16x128_f8f6f4 v[204:207], v[122:127], v[38:43], 0 cbsz:2 blgp:2
	v_mfma_f32_16x16x128_f8f6f4 v[208:211], v[122:127], v[50:55], 0 cbsz:2 blgp:2
	v_mfma_f32_16x16x128_f8f6f4 v[212:215], v[122:127], v[62:67], v[188:191] cbsz:2 blgp:2
	s_waitcnt lgkmcnt(0)
	v_mfma_f32_16x16x128_f8f6f4 v[134:137], v[128:133], v[8:13], v[134:137] cbsz:2 blgp:2
	v_mfma_f32_16x16x128_f8f6f4 v[204:207], v[128:133], v[44:49], v[204:207] cbsz:2 blgp:2
	v_mfma_f32_16x16x128_f8f6f4 v[138:141], v[128:133], v[20:25], v[138:141] cbsz:2 blgp:2
	v_mfma_f32_16x16x128_f8f6f4 v[208:211], v[128:133], v[56:61], v[208:211] cbsz:2 blgp:2
	v_mfma_f32_16x16x128_f8f6f4 v[142:145], v[128:133], v[32:37], v[142:145] cbsz:2 blgp:2
	v_mfma_f32_16x16x128_f8f6f4 v[212:215], v[128:133], v[68:73], v[212:215] cbsz:2 blgp:2
	v_cndmask_b32_e64 v158, v134, v204, s[0:1]
	v_fma_mix_f32 v158, v158, v100, v82 op_sel:[0,0,1] op_sel_hi:[0,0,1]
	v_exp_f32_e32 v158, v158
	v_cndmask_b32_e64 v159, v138, v208, s[0:1]
	v_fma_mix_f32 v159, v159, v101, v74 op_sel:[0,0,1] op_sel_hi:[0,0,1]
	v_exp_f32_e32 v159, v159
	v_fma_f32 v158, v158, v186, v186
	v_rcp_f32_e32 v158, v158
	v_add_f32_e32 v159, 1.0, v159
	v_rcp_f32_e32 v159, v159
	v_cndmask_b32_e64 v160, v142, v212, s[0:1]
	v_fma_mix_f32 v161, v158, v160, v78 op_sel:[0,0,1] op_sel_hi:[0,0,1]
	v_exp_f32_e32 v161, v161
	s_add_u32 s48, s48, s40
	v_add_f32_e32 v161, 1.0, v161
	v_rcp_f32_e32 v161, v161
	s_addc_u32 s49, s49, s41
	v_fma_f32 v162, v161, -2.0, 1.0
	v_sub_f32_e32 v163, v176, v162
	v_fma_f32 v176, v159, v163, v162
	v_fma_f32 v164, |v176|, s17, v113
	v_fma_f32 v165, |v176|, s18, v114
	v_fma_f32 v166, |v176|, s19, v115
	v_lshrrev_b32_e32 v167, 26, v176
	v_min3_u32 v164, v164, v165, v166
	v_bfi_b32 v168, 31, v164, v167
	s_nop 1
	v_mul_u32_u24_dpp v170, v168, v180 quad_perm:[1,2,3,3] row_mask:0xf bank_mask:0xf bound_ctrl:1
	v_mad_u32_u24 v171, v168, v181, v170
	ds_write_b8_d16_hi v184, v171
	s_barrier
	global_store_short_d16_hi v185, v176, s[48:49]
	s_waitcnt lgkmcnt(0)
	s_barrier
	ds_read_b64 v[122:123], v105 offset:0
	ds_read_b64 v[124:125], v105 offset:8
	ds_read_b64 v[126:127], v105 offset:16
	ds_read_b64 v[128:129], v105 offset:96
	ds_read_b64 v[130:131], v105 offset:104
	ds_read_b64 v[132:133], v105 offset:112
	s_waitcnt lgkmcnt(3)
	v_mfma_f32_16x16x128_f8f6f4 v[134:137], v[122:127], v[2:7], 0 cbsz:2 blgp:2
	v_mfma_f32_16x16x128_f8f6f4 v[138:141], v[122:127], v[14:19], 0 cbsz:2 blgp:2
	v_mfma_f32_16x16x128_f8f6f4 v[142:145], v[122:127], v[26:31], v[188:191] cbsz:2 blgp:2
	v_mfma_f32_16x16x128_f8f6f4 v[204:207], v[122:127], v[38:43], 0 cbsz:2 blgp:2
	v_mfma_f32_16x16x128_f8f6f4 v[208:211], v[122:127], v[50:55], 0 cbsz:2 blgp:2
	v_mfma_f32_16x16x128_f8f6f4 v[212:215], v[122:127], v[62:67], v[188:191] cbsz:2 blgp:2
	s_waitcnt lgkmcnt(0)
	v_mfma_f32_16x16x128_f8f6f4 v[134:137], v[128:133], v[8:13], v[134:137] cbsz:2 blgp:2
	v_mfma_f32_16x16x128_f8f6f4 v[204:207], v[128:133], v[44:49], v[204:207] cbsz:2 blgp:2
	v_mfma_f32_16x16x128_f8f6f4 v[138:141], v[128:133], v[20:25], v[138:141] cbsz:2 blgp:2
	v_mfma_f32_16x16x128_f8f6f4 v[208:211], v[128:133], v[56:61], v[208:211] cbsz:2 blgp:2
	v_mfma_f32_16x16x128_f8f6f4 v[142:145], v[128:133], v[32:37], v[142:145] cbsz:2 blgp:2
	v_mfma_f32_16x16x128_f8f6f4 v[212:215], v[128:133], v[68:73], v[212:215] cbsz:2 blgp:2
	v_cndmask_b32_e64 v158, v134, v204, s[0:1]
	v_fma_mix_f32 v158, v158, v100, v83 op_sel_hi:[0,0,1]
	v_exp_f32_e32 v158, v158
	v_cndmask_b32_e64 v159, v138, v208, s[0:1]
	v_fma_mix_f32 v159, v159, v101, v75 op_sel_hi:[0,0,1]
	v_exp_f32_e32 v159, v159
	v_fma_f32 v158, v158, v186, v186
	v_rcp_f32_e32 v158, v158
	v_add_f32_e32 v159, 1.0, v159
	v_rcp_f32_e32 v159, v159
	v_cndmask_b32_e64 v160, v142, v212, s[0:1]
	v_fma_mix_f32 v161, v158, v160, v79 op_sel_hi:[0,0,1]
	v_exp_f32_e32 v161, v161
	s_add_u32 s48, s48, s40
	v_add_f32_e32 v161, 1.0, v161
	v_rcp_f32_e32 v161, v161
	s_addc_u32 s49, s49, s41
	v_fma_f32 v162, v161, -2.0, 1.0
	v_sub_f32_e32 v163, v176, v162
	v_fma_f32 v176, v159, v163, v162
	v_fma_f32 v164, |v176|, s17, v113
	v_fma_f32 v165, |v176|, s18, v114
	v_fma_f32 v166, |v176|, s19, v115
	v_lshrrev_b32_e32 v167, 26, v176
	v_min3_u32 v164, v164, v165, v166
	v_bfi_b32 v168, 31, v164, v167
	s_nop 1
	v_mul_u32_u24_dpp v170, v168, v180 quad_perm:[1,2,3,3] row_mask:0xf bank_mask:0xf bound_ctrl:1
	v_mad_u32_u24 v171, v168, v181, v170
	ds_write_b8_d16_hi v184, v171 offset:416
	s_barrier
	global_store_short_d16_hi v185, v176, s[48:49]
	s_waitcnt lgkmcnt(0)
	s_barrier
	ds_read_b64 v[122:123], v105 offset:416
	ds_read_b64 v[124:125], v105 offset:424
	ds_read_b64 v[126:127], v105 offset:432
	ds_read_b64 v[128:129], v105 offset:512
	ds_read_b64 v[130:131], v105 offset:520
	ds_read_b64 v[132:133], v105 offset:528
	s_waitcnt lgkmcnt(3)
	v_mfma_f32_16x16x128_f8f6f4 v[134:137], v[122:127], v[2:7], 0 cbsz:2 blgp:2
	v_mfma_f32_16x16x128_f8f6f4 v[138:141], v[122:127], v[14:19], 0 cbsz:2 blgp:2
	v_mfma_f32_16x16x128_f8f6f4 v[142:145], v[122:127], v[26:31], v[188:191] cbsz:2 blgp:2
	v_mfma_f32_16x16x128_f8f6f4 v[204:207], v[122:127], v[38:43], 0 cbsz:2 blgp:2
	v_mfma_f32_16x16x128_f8f6f4 v[208:211], v[122:127], v[50:55], 0 cbsz:2 blgp:2
	v_mfma_f32_16x16x128_f8f6f4 v[212:215], v[122:127], v[62:67], v[188:191] cbsz:2 blgp:2
	s_waitcnt lgkmcnt(0)
	v_mfma_f32_16x16x128_f8f6f4 v[134:137], v[128:133], v[8:13], v[134:137] cbsz:2 blgp:2
	v_mfma_f32_16x16x128_f8f6f4 v[204:207], v[128:133], v[44:49], v[204:207] cbsz:2 blgp:2
	v_mfma_f32_16x16x128_f8f6f4 v[138:141], v[128:133], v[20:25], v[138:141] cbsz:2 blgp:2
	v_mfma_f32_16x16x128_f8f6f4 v[208:211], v[128:133], v[56:61], v[208:211] cbsz:2 blgp:2
	v_mfma_f32_16x16x128_f8f6f4 v[142:145], v[128:133], v[32:37], v[142:145] cbsz:2 blgp:2
	v_mfma_f32_16x16x128_f8f6f4 v[212:215], v[128:133], v[68:73], v[212:215] cbsz:2 blgp:2
	v_cndmask_b32_e64 v158, v134, v204, s[0:1]
	v_fma_mix_f32 v158, v158, v100, v83 op_sel:[0,0,1] op_sel_hi:[0,0,1]
	v_exp_f32_e32 v158, v158
	v_cndmask_b32_e64 v159, v138, v208, s[0:1]
	v_fma_mix_f32 v159, v159, v101, v75 op_sel:[0,0,1] op_sel_hi:[0,0,1]
	v_exp_f32_e32 v159, v159
	v_fma_f32 v158, v158, v186, v186
	v_rcp_f32_e32 v158, v158
	v_add_f32_e32 v159, 1.0, v159
	v_rcp_f32_e32 v159, v159
	v_cndmask_b32_e64 v160, v142, v212, s[0:1]
	v_fma_mix_f32 v161, v158, v160, v79 op_sel:[0,0,1] op_sel_hi:[0,0,1]
	v_exp_f32_e32 v161, v161
	s_add_u32 s48, s48, s40
	v_add_f32_e32 v161, 1.0, v161
	v_rcp_f32_e32 v161, v161
	s_addc_u32 s49, s49, s41
	v_fma_f32 v162, v161, -2.0, 1.0
	v_sub_f32_e32 v163, v176, v162
	v_fma_f32 v176, v159, v163, v162
	v_fma_f32 v164, |v176|, s17, v113
	v_fma_f32 v165, |v176|, s18, v114
	v_fma_f32 v166, |v176|, s19, v115
	v_lshrrev_b32_e32 v167, 26, v176
	v_min3_u32 v164, v164, v165, v166
	v_bfi_b32 v168, 31, v164, v167
	s_nop 1
	v_mul_u32_u24_dpp v170, v168, v180 quad_perm:[1,2,3,3] row_mask:0xf bank_mask:0xf bound_ctrl:1
	v_mad_u32_u24 v171, v168, v181, v170
	ds_write_b8_d16_hi v184, v171
	s_barrier
	global_store_short_d16_hi v185, v176, s[48:49]
	s_waitcnt lgkmcnt(0)
	s_barrier
	ds_read_b64 v[122:123], v105 offset:0
	ds_read_b64 v[124:125], v105 offset:8
	ds_read_b64 v[126:127], v105 offset:16
	ds_read_b64 v[128:129], v105 offset:96
	ds_read_b64 v[130:131], v105 offset:104
	ds_read_b64 v[132:133], v105 offset:112
	s_waitcnt lgkmcnt(3)
	v_mfma_f32_16x16x128_f8f6f4 v[134:137], v[122:127], v[2:7], 0 cbsz:2 blgp:2
	v_mfma_f32_16x16x128_f8f6f4 v[138:141], v[122:127], v[14:19], 0 cbsz:2 blgp:2
	v_mfma_f32_16x16x128_f8f6f4 v[142:145], v[122:127], v[26:31], v[188:191] cbsz:2 blgp:2
	v_mfma_f32_16x16x128_f8f6f4 v[204:207], v[122:127], v[38:43], 0 cbsz:2 blgp:2
	v_mfma_f32_16x16x128_f8f6f4 v[208:211], v[122:127], v[50:55], 0 cbsz:2 blgp:2
	v_mfma_f32_16x16x128_f8f6f4 v[212:215], v[122:127], v[62:67], v[188:191] cbsz:2 blgp:2
	s_waitcnt lgkmcnt(0)
	v_mfma_f32_16x16x128_f8f6f4 v[134:137], v[128:133], v[8:13], v[134:137] cbsz:2 blgp:2
	v_mfma_f32_16x16x128_f8f6f4 v[204:207], v[128:133], v[44:49], v[204:207] cbsz:2 blgp:2
	v_mfma_f32_16x16x128_f8f6f4 v[138:141], v[128:133], v[20:25], v[138:141] cbsz:2 blgp:2
	v_mfma_f32_16x16x128_f8f6f4 v[208:211], v[128:133], v[56:61], v[208:211] cbsz:2 blgp:2
	v_mfma_f32_16x16x128_f8f6f4 v[142:145], v[128:133], v[32:37], v[142:145] cbsz:2 blgp:2
	v_mfma_f32_16x16x128_f8f6f4 v[212:215], v[128:133], v[68:73], v[212:215] cbsz:2 blgp:2
	v_cndmask_b32_e64 v158, v134, v204, s[0:1]
	v_fma_mix_f32 v158, v158, v100, v84 op_sel_hi:[0,0,1]
	v_exp_f32_e32 v158, v158
	v_cndmask_b32_e64 v159, v138, v208, s[0:1]
	v_fma_mix_f32 v159, v159, v101, v76 op_sel_hi:[0,0,1]
	v_exp_f32_e32 v159, v159
	v_fma_f32 v158, v158, v186, v186
	v_rcp_f32_e32 v158, v158
	v_add_f32_e32 v159, 1.0, v159
	v_rcp_f32_e32 v159, v159
	v_cndmask_b32_e64 v160, v142, v212, s[0:1]
	v_fma_mix_f32 v161, v158, v160, v80 op_sel_hi:[0,0,1]
	v_exp_f32_e32 v161, v161
	s_add_u32 s48, s48, s40
	v_add_f32_e32 v161, 1.0, v161
	v_rcp_f32_e32 v161, v161
	s_addc_u32 s49, s49, s41
	v_fma_f32 v162, v161, -2.0, 1.0
	v_sub_f32_e32 v163, v176, v162
	v_fma_f32 v176, v159, v163, v162
	v_fma_f32 v164, |v176|, s17, v113
	v_fma_f32 v165, |v176|, s18, v114
	v_fma_f32 v166, |v176|, s19, v115
	v_lshrrev_b32_e32 v167, 26, v176
	v_min3_u32 v164, v164, v165, v166
	v_bfi_b32 v168, 31, v164, v167
	s_nop 1
	v_mul_u32_u24_dpp v170, v168, v180 quad_perm:[1,2,3,3] row_mask:0xf bank_mask:0xf bound_ctrl:1
	v_mad_u32_u24 v171, v168, v181, v170
	ds_write_b8_d16_hi v184, v171 offset:416
	s_barrier
	global_store_short_d16_hi v185, v176, s[48:49]
	s_waitcnt lgkmcnt(0)
	s_barrier
	ds_read_b64 v[122:123], v105 offset:416
	ds_read_b64 v[124:125], v105 offset:424
	ds_read_b64 v[126:127], v105 offset:432
	ds_read_b64 v[128:129], v105 offset:512
	ds_read_b64 v[130:131], v105 offset:520
	ds_read_b64 v[132:133], v105 offset:528
	s_waitcnt lgkmcnt(3)
	v_mfma_f32_16x16x128_f8f6f4 v[134:137], v[122:127], v[2:7], 0 cbsz:2 blgp:2
	v_mfma_f32_16x16x128_f8f6f4 v[138:141], v[122:127], v[14:19], 0 cbsz:2 blgp:2
	v_mfma_f32_16x16x128_f8f6f4 v[142:145], v[122:127], v[26:31], v[188:191] cbsz:2 blgp:2
	v_mfma_f32_16x16x128_f8f6f4 v[204:207], v[122:127], v[38:43], 0 cbsz:2 blgp:2
	v_mfma_f32_16x16x128_f8f6f4 v[208:211], v[122:127], v[50:55], 0 cbsz:2 blgp:2
	v_mfma_f32_16x16x128_f8f6f4 v[212:215], v[122:127], v[62:67], v[188:191] cbsz:2 blgp:2
	s_waitcnt lgkmcnt(0)
	v_mfma_f32_16x16x128_f8f6f4 v[134:137], v[128:133], v[8:13], v[134:137] cbsz:2 blgp:2
	v_mfma_f32_16x16x128_f8f6f4 v[204:207], v[128:133], v[44:49], v[204:207] cbsz:2 blgp:2
	v_mfma_f32_16x16x128_f8f6f4 v[138:141], v[128:133], v[20:25], v[138:141] cbsz:2 blgp:2
	v_mfma_f32_16x16x128_f8f6f4 v[208:211], v[128:133], v[56:61], v[208:211] cbsz:2 blgp:2
	v_mfma_f32_16x16x128_f8f6f4 v[142:145], v[128:133], v[32:37], v[142:145] cbsz:2 blgp:2
	v_mfma_f32_16x16x128_f8f6f4 v[212:215], v[128:133], v[68:73], v[212:215] cbsz:2 blgp:2
	v_cndmask_b32_e64 v158, v134, v204, s[0:1]
	v_fma_mix_f32 v158, v158, v100, v84 op_sel:[0,0,1] op_sel_hi:[0,0,1]
	v_exp_f32_e32 v158, v158
	v_cndmask_b32_e64 v159, v138, v208, s[0:1]
	v_fma_mix_f32 v159, v159, v101, v76 op_sel:[0,0,1] op_sel_hi:[0,0,1]
	v_exp_f32_e32 v159, v159
	v_fma_f32 v158, v158, v186, v186
	v_rcp_f32_e32 v158, v158
	v_add_f32_e32 v159, 1.0, v159
	v_rcp_f32_e32 v159, v159
	v_cndmask_b32_e64 v160, v142, v212, s[0:1]
	v_fma_mix_f32 v161, v158, v160, v80 op_sel:[0,0,1] op_sel_hi:[0,0,1]
	v_exp_f32_e32 v161, v161
	s_add_u32 s48, s48, s40
	v_add_f32_e32 v161, 1.0, v161
	v_rcp_f32_e32 v161, v161
	s_addc_u32 s49, s49, s41
	v_fma_f32 v162, v161, -2.0, 1.0
	v_sub_f32_e32 v163, v176, v162
	v_fma_f32 v176, v159, v163, v162
	v_fma_f32 v164, |v176|, s17, v113
	v_fma_f32 v165, |v176|, s18, v114
	v_fma_f32 v166, |v176|, s19, v115
	v_lshrrev_b32_e32 v167, 26, v176
	v_min3_u32 v164, v164, v165, v166
	v_bfi_b32 v168, 31, v164, v167
	s_nop 1
	v_mul_u32_u24_dpp v170, v168, v180 quad_perm:[1,2,3,3] row_mask:0xf bank_mask:0xf bound_ctrl:1
	v_mad_u32_u24 v171, v168, v181, v170
	ds_write_b8_d16_hi v184, v171
	s_barrier
	global_store_short_d16_hi v185, v176, s[48:49]
	s_waitcnt lgkmcnt(0)
	s_barrier
	ds_read_b64 v[122:123], v105 offset:0
	ds_read_b64 v[124:125], v105 offset:8
	ds_read_b64 v[126:127], v105 offset:16
	ds_read_b64 v[128:129], v105 offset:96
	ds_read_b64 v[130:131], v105 offset:104
	ds_read_b64 v[132:133], v105 offset:112
	s_waitcnt lgkmcnt(3)
	v_mfma_f32_16x16x128_f8f6f4 v[134:137], v[122:127], v[2:7], 0 cbsz:2 blgp:2
	v_mfma_f32_16x16x128_f8f6f4 v[138:141], v[122:127], v[14:19], 0 cbsz:2 blgp:2
	v_mfma_f32_16x16x128_f8f6f4 v[142:145], v[122:127], v[26:31], v[188:191] cbsz:2 blgp:2
	v_mfma_f32_16x16x128_f8f6f4 v[204:207], v[122:127], v[38:43], 0 cbsz:2 blgp:2
	v_mfma_f32_16x16x128_f8f6f4 v[208:211], v[122:127], v[50:55], 0 cbsz:2 blgp:2
	v_mfma_f32_16x16x128_f8f6f4 v[212:215], v[122:127], v[62:67], v[188:191] cbsz:2 blgp:2
	s_waitcnt lgkmcnt(0)
	v_mfma_f32_16x16x128_f8f6f4 v[134:137], v[128:133], v[8:13], v[134:137] cbsz:2 blgp:2
	v_mfma_f32_16x16x128_f8f6f4 v[204:207], v[128:133], v[44:49], v[204:207] cbsz:2 blgp:2
	v_mfma_f32_16x16x128_f8f6f4 v[138:141], v[128:133], v[20:25], v[138:141] cbsz:2 blgp:2
	v_mfma_f32_16x16x128_f8f6f4 v[208:211], v[128:133], v[56:61], v[208:211] cbsz:2 blgp:2
	v_mfma_f32_16x16x128_f8f6f4 v[142:145], v[128:133], v[32:37], v[142:145] cbsz:2 blgp:2
	v_mfma_f32_16x16x128_f8f6f4 v[212:215], v[128:133], v[68:73], v[212:215] cbsz:2 blgp:2
	v_cndmask_b32_e64 v158, v134, v204, s[0:1]
	v_fma_mix_f32 v158, v158, v100, v85 op_sel_hi:[0,0,1]
	v_exp_f32_e32 v158, v158
	v_cndmask_b32_e64 v159, v138, v208, s[0:1]
	v_fma_mix_f32 v159, v159, v101, v77 op_sel_hi:[0,0,1]
	v_exp_f32_e32 v159, v159
	v_fma_f32 v158, v158, v186, v186
	v_rcp_f32_e32 v158, v158
	v_add_f32_e32 v159, 1.0, v159
	v_rcp_f32_e32 v159, v159
	v_cndmask_b32_e64 v160, v142, v212, s[0:1]
	v_fma_mix_f32 v161, v158, v160, v81 op_sel_hi:[0,0,1]
	v_exp_f32_e32 v161, v161
	s_add_u32 s48, s48, s40
	v_add_f32_e32 v161, 1.0, v161
	v_rcp_f32_e32 v161, v161
	s_addc_u32 s49, s49, s41
	v_fma_f32 v162, v161, -2.0, 1.0
	v_sub_f32_e32 v163, v176, v162
	v_fma_f32 v176, v159, v163, v162
	v_fma_f32 v164, |v176|, s17, v113
	v_fma_f32 v165, |v176|, s18, v114
	v_fma_f32 v166, |v176|, s19, v115
	v_lshrrev_b32_e32 v167, 26, v176
	v_min3_u32 v164, v164, v165, v166
	v_bfi_b32 v168, 31, v164, v167
	s_nop 1
	v_mul_u32_u24_dpp v170, v168, v180 quad_perm:[1,2,3,3] row_mask:0xf bank_mask:0xf bound_ctrl:1
	v_mad_u32_u24 v171, v168, v181, v170
	ds_write_b8_d16_hi v184, v171 offset:416
	s_barrier
	global_store_short_d16_hi v185, v176, s[48:49]
	s_waitcnt lgkmcnt(0)
	s_barrier
	ds_read_b64 v[122:123], v105 offset:416
	ds_read_b64 v[124:125], v105 offset:424
	ds_read_b64 v[126:127], v105 offset:432
	ds_read_b64 v[128:129], v105 offset:512
	ds_read_b64 v[130:131], v105 offset:520
	ds_read_b64 v[132:133], v105 offset:528
	s_waitcnt lgkmcnt(3)
	v_mfma_f32_16x16x128_f8f6f4 v[134:137], v[122:127], v[2:7], 0 cbsz:2 blgp:2
	v_mfma_f32_16x16x128_f8f6f4 v[138:141], v[122:127], v[14:19], 0 cbsz:2 blgp:2
	v_mfma_f32_16x16x128_f8f6f4 v[142:145], v[122:127], v[26:31], v[188:191] cbsz:2 blgp:2
	v_mfma_f32_16x16x128_f8f6f4 v[204:207], v[122:127], v[38:43], 0 cbsz:2 blgp:2
	v_mfma_f32_16x16x128_f8f6f4 v[208:211], v[122:127], v[50:55], 0 cbsz:2 blgp:2
	v_mfma_f32_16x16x128_f8f6f4 v[212:215], v[122:127], v[62:67], v[188:191] cbsz:2 blgp:2
	s_waitcnt lgkmcnt(0)
	v_mfma_f32_16x16x128_f8f6f4 v[134:137], v[128:133], v[8:13], v[134:137] cbsz:2 blgp:2
	v_mfma_f32_16x16x128_f8f6f4 v[204:207], v[128:133], v[44:49], v[204:207] cbsz:2 blgp:2
	v_mfma_f32_16x16x128_f8f6f4 v[138:141], v[128:133], v[20:25], v[138:141] cbsz:2 blgp:2
	v_mfma_f32_16x16x128_f8f6f4 v[208:211], v[128:133], v[56:61], v[208:211] cbsz:2 blgp:2
	v_mfma_f32_16x16x128_f8f6f4 v[142:145], v[128:133], v[32:37], v[142:145] cbsz:2 blgp:2
	v_mfma_f32_16x16x128_f8f6f4 v[212:215], v[128:133], v[68:73], v[212:215] cbsz:2 blgp:2
	v_cndmask_b32_e64 v158, v134, v204, s[0:1]
	v_fma_mix_f32 v158, v158, v100, v85 op_sel:[0,0,1] op_sel_hi:[0,0,1]
	v_exp_f32_e32 v158, v158
	v_cndmask_b32_e64 v159, v138, v208, s[0:1]
	v_fma_mix_f32 v159, v159, v101, v77 op_sel:[0,0,1] op_sel_hi:[0,0,1]
	v_exp_f32_e32 v159, v159
	v_fma_f32 v158, v158, v186, v186
	v_rcp_f32_e32 v158, v158
	v_add_f32_e32 v159, 1.0, v159
	v_rcp_f32_e32 v159, v159
	v_cndmask_b32_e64 v160, v142, v212, s[0:1]
	v_fma_mix_f32 v161, v158, v160, v81 op_sel:[0,0,1] op_sel_hi:[0,0,1]
	v_exp_f32_e32 v161, v161
	s_add_u32 s48, s48, s40
	v_add_f32_e32 v161, 1.0, v161
	v_rcp_f32_e32 v161, v161
	s_addc_u32 s49, s49, s41
	v_fma_f32 v162, v161, -2.0, 1.0
	v_sub_f32_e32 v163, v176, v162
	v_fma_f32 v176, v159, v163, v162
	v_fma_f32 v164, |v176|, s17, v113
	v_fma_f32 v165, |v176|, s18, v114
	v_fma_f32 v166, |v176|, s19, v115
	v_lshrrev_b32_e32 v167, 26, v176
	v_min3_u32 v164, v164, v165, v166
	v_bfi_b32 v168, 31, v164, v167
	s_nop 1
	v_mul_u32_u24_dpp v170, v168, v180 quad_perm:[1,2,3,3] row_mask:0xf bank_mask:0xf bound_ctrl:1
	v_mad_u32_u24 v171, v168, v181, v170
	ds_write_b8_d16_hi v184, v171
	s_barrier
	global_store_short_d16_hi v185, v176, s[48:49]
	s_waitcnt lgkmcnt(0)
	s_barrier
	ds_read_b64 v[122:123], v105 offset:0
	ds_read_b64 v[124:125], v105 offset:8
	ds_read_b64 v[126:127], v105 offset:16
	ds_read_b64 v[128:129], v105 offset:96
	ds_read_b64 v[130:131], v105 offset:104
	ds_read_b64 v[132:133], v105 offset:112
	s_waitcnt vmcnt(8)
	global_load_dwordx4 v[82:85], v[196:197], off
	global_load_dwordx4 v[74:77], v[196:197], off offset:512
	global_load_dwordx4 v[78:81], v[196:197], off offset:1024
	v_lshl_add_u64 v[196:197], v[196:197], 0, s[42:43]
	s_waitcnt lgkmcnt(3)
	v_mfma_f32_16x16x128_f8f6f4 v[134:137], v[122:127], v[2:7], 0 cbsz:2 blgp:2
	v_mfma_f32_16x16x128_f8f6f4 v[138:141], v[122:127], v[14:19], 0 cbsz:2 blgp:2
	v_mfma_f32_16x16x128_f8f6f4 v[142:145], v[122:127], v[26:31], v[188:191] cbsz:2 blgp:2
	v_mfma_f32_16x16x128_f8f6f4 v[204:207], v[122:127], v[38:43], 0 cbsz:2 blgp:2
	v_mfma_f32_16x16x128_f8f6f4 v[208:211], v[122:127], v[50:55], 0 cbsz:2 blgp:2
	v_mfma_f32_16x16x128_f8f6f4 v[212:215], v[122:127], v[62:67], v[188:191] cbsz:2 blgp:2
	s_waitcnt lgkmcnt(0)
	v_mfma_f32_16x16x128_f8f6f4 v[134:137], v[128:133], v[8:13], v[134:137] cbsz:2 blgp:2
	v_mfma_f32_16x16x128_f8f6f4 v[204:207], v[128:133], v[44:49], v[204:207] cbsz:2 blgp:2
	v_mfma_f32_16x16x128_f8f6f4 v[138:141], v[128:133], v[20:25], v[138:141] cbsz:2 blgp:2
	v_mfma_f32_16x16x128_f8f6f4 v[208:211], v[128:133], v[56:61], v[208:211] cbsz:2 blgp:2
	v_mfma_f32_16x16x128_f8f6f4 v[142:145], v[128:133], v[32:37], v[142:145] cbsz:2 blgp:2
	v_mfma_f32_16x16x128_f8f6f4 v[212:215], v[128:133], v[68:73], v[212:215] cbsz:2 blgp:2
	v_cndmask_b32_e64 v158, v134, v204, s[0:1]
	v_fma_mix_f32 v158, v158, v100, v146 op_sel_hi:[0,0,1]
	v_exp_f32_e32 v158, v158
	v_cndmask_b32_e64 v159, v138, v208, s[0:1]
	v_fma_mix_f32 v159, v159, v101, v150 op_sel_hi:[0,0,1]
	v_exp_f32_e32 v159, v159
	v_fma_f32 v158, v158, v186, v186
	v_rcp_f32_e32 v158, v158
	v_add_f32_e32 v159, 1.0, v159
	v_rcp_f32_e32 v159, v159
	v_cndmask_b32_e64 v160, v142, v212, s[0:1]
	v_fma_mix_f32 v161, v158, v160, v154 op_sel_hi:[0,0,1]
	v_exp_f32_e32 v161, v161
	s_add_u32 s48, s48, s40
	v_add_f32_e32 v161, 1.0, v161
	v_rcp_f32_e32 v161, v161
	s_addc_u32 s49, s49, s41
	v_fma_f32 v162, v161, -2.0, 1.0
	v_sub_f32_e32 v163, v176, v162
	v_fma_f32 v176, v159, v163, v162
	v_fma_f32 v164, |v176|, s17, v113
	v_fma_f32 v165, |v176|, s18, v114
	v_fma_f32 v166, |v176|, s19, v115
	v_lshrrev_b32_e32 v167, 26, v176
	v_min3_u32 v164, v164, v165, v166
	v_bfi_b32 v168, 31, v164, v167
	s_nop 1
	v_mul_u32_u24_dpp v170, v168, v180 quad_perm:[1,2,3,3] row_mask:0xf bank_mask:0xf bound_ctrl:1
	v_mad_u32_u24 v171, v168, v181, v170
	ds_write_b8_d16_hi v184, v171 offset:416
	s_barrier
	global_store_short_d16_hi v185, v176, s[48:49]
	s_waitcnt lgkmcnt(0)
	s_barrier
	ds_read_b64 v[122:123], v105 offset:416
	ds_read_b64 v[124:125], v105 offset:424
	ds_read_b64 v[126:127], v105 offset:432
	ds_read_b64 v[128:129], v105 offset:512
	ds_read_b64 v[130:131], v105 offset:520
	ds_read_b64 v[132:133], v105 offset:528
	s_waitcnt lgkmcnt(3)
	v_mfma_f32_16x16x128_f8f6f4 v[134:137], v[122:127], v[2:7], 0 cbsz:2 blgp:2
	v_mfma_f32_16x16x128_f8f6f4 v[138:141], v[122:127], v[14:19], 0 cbsz:2 blgp:2
	v_mfma_f32_16x16x128_f8f6f4 v[142:145], v[122:127], v[26:31], v[188:191] cbsz:2 blgp:2
	v_mfma_f32_16x16x128_f8f6f4 v[204:207], v[122:127], v[38:43], 0 cbsz:2 blgp:2
	v_mfma_f32_16x16x128_f8f6f4 v[208:211], v[122:127], v[50:55], 0 cbsz:2 blgp:2
	v_mfma_f32_16x16x128_f8f6f4 v[212:215], v[122:127], v[62:67], v[188:191] cbsz:2 blgp:2
	s_waitcnt lgkmcnt(0)
	v_mfma_f32_16x16x128_f8f6f4 v[134:137], v[128:133], v[8:13], v[134:137] cbsz:2 blgp:2
	v_mfma_f32_16x16x128_f8f6f4 v[204:207], v[128:133], v[44:49], v[204:207] cbsz:2 blgp:2
	v_mfma_f32_16x16x128_f8f6f4 v[138:141], v[128:133], v[20:25], v[138:141] cbsz:2 blgp:2
	v_mfma_f32_16x16x128_f8f6f4 v[208:211], v[128:133], v[56:61], v[208:211] cbsz:2 blgp:2
	v_mfma_f32_16x16x128_f8f6f4 v[142:145], v[128:133], v[32:37], v[142:145] cbsz:2 blgp:2
	v_mfma_f32_16x16x128_f8f6f4 v[212:215], v[128:133], v[68:73], v[212:215] cbsz:2 blgp:2
	v_cndmask_b32_e64 v158, v134, v204, s[0:1]
	v_fma_mix_f32 v158, v158, v100, v146 op_sel:[0,0,1] op_sel_hi:[0,0,1]
	v_exp_f32_e32 v158, v158
	v_cndmask_b32_e64 v159, v138, v208, s[0:1]
	v_fma_mix_f32 v159, v159, v101, v150 op_sel:[0,0,1] op_sel_hi:[0,0,1]
	v_exp_f32_e32 v159, v159
	v_fma_f32 v158, v158, v186, v186
	v_rcp_f32_e32 v158, v158
	v_add_f32_e32 v159, 1.0, v159
	v_rcp_f32_e32 v159, v159
	v_cndmask_b32_e64 v160, v142, v212, s[0:1]
	v_fma_mix_f32 v161, v158, v160, v154 op_sel:[0,0,1] op_sel_hi:[0,0,1]
	v_exp_f32_e32 v161, v161
	s_add_u32 s48, s48, s40
	v_add_f32_e32 v161, 1.0, v161
	v_rcp_f32_e32 v161, v161
	s_addc_u32 s49, s49, s41
	v_fma_f32 v162, v161, -2.0, 1.0
	v_sub_f32_e32 v163, v176, v162
	v_fma_f32 v176, v159, v163, v162
	v_fma_f32 v164, |v176|, s17, v113
	v_fma_f32 v165, |v176|, s18, v114
	v_fma_f32 v166, |v176|, s19, v115
	v_lshrrev_b32_e32 v167, 26, v176
	v_min3_u32 v164, v164, v165, v166
	v_bfi_b32 v168, 31, v164, v167
	s_nop 1
	v_mul_u32_u24_dpp v170, v168, v180 quad_perm:[1,2,3,3] row_mask:0xf bank_mask:0xf bound_ctrl:1
	v_mad_u32_u24 v171, v168, v181, v170
	ds_write_b8_d16_hi v184, v171
	s_barrier
	global_store_short_d16_hi v185, v176, s[48:49]
	s_waitcnt lgkmcnt(0)
	s_barrier
	ds_read_b64 v[122:123], v105 offset:0
	ds_read_b64 v[124:125], v105 offset:8
	ds_read_b64 v[126:127], v105 offset:16
	ds_read_b64 v[128:129], v105 offset:96
	ds_read_b64 v[130:131], v105 offset:104
	ds_read_b64 v[132:133], v105 offset:112
	s_waitcnt lgkmcnt(3)
	v_mfma_f32_16x16x128_f8f6f4 v[134:137], v[122:127], v[2:7], 0 cbsz:2 blgp:2
	v_mfma_f32_16x16x128_f8f6f4 v[138:141], v[122:127], v[14:19], 0 cbsz:2 blgp:2
	v_mfma_f32_16x16x128_f8f6f4 v[142:145], v[122:127], v[26:31], v[188:191] cbsz:2 blgp:2
	v_mfma_f32_16x16x128_f8f6f4 v[204:207], v[122:127], v[38:43], 0 cbsz:2 blgp:2
	v_mfma_f32_16x16x128_f8f6f4 v[208:211], v[122:127], v[50:55], 0 cbsz:2 blgp:2
	v_mfma_f32_16x16x128_f8f6f4 v[212:215], v[122:127], v[62:67], v[188:191] cbsz:2 blgp:2
	s_waitcnt lgkmcnt(0)
	v_mfma_f32_16x16x128_f8f6f4 v[134:137], v[128:133], v[8:13], v[134:137] cbsz:2 blgp:2
	v_mfma_f32_16x16x128_f8f6f4 v[204:207], v[128:133], v[44:49], v[204:207] cbsz:2 blgp:2
	v_mfma_f32_16x16x128_f8f6f4 v[138:141], v[128:133], v[20:25], v[138:141] cbsz:2 blgp:2
	v_mfma_f32_16x16x128_f8f6f4 v[208:211], v[128:133], v[56:61], v[208:211] cbsz:2 blgp:2
	v_mfma_f32_16x16x128_f8f6f4 v[142:145], v[128:133], v[32:37], v[142:145] cbsz:2 blgp:2
	v_mfma_f32_16x16x128_f8f6f4 v[212:215], v[128:133], v[68:73], v[212:215] cbsz:2 blgp:2
	v_cndmask_b32_e64 v158, v134, v204, s[0:1]
	v_fma_mix_f32 v158, v158, v100, v147 op_sel_hi:[0,0,1]
	v_exp_f32_e32 v158, v158
	v_cndmask_b32_e64 v159, v138, v208, s[0:1]
	v_fma_mix_f32 v159, v159, v101, v151 op_sel_hi:[0,0,1]
	v_exp_f32_e32 v159, v159
	v_fma_f32 v158, v158, v186, v186
	v_rcp_f32_e32 v158, v158
	v_add_f32_e32 v159, 1.0, v159
	v_rcp_f32_e32 v159, v159
	v_cndmask_b32_e64 v160, v142, v212, s[0:1]
	v_fma_mix_f32 v161, v158, v160, v155 op_sel_hi:[0,0,1]
	v_exp_f32_e32 v161, v161
	s_add_u32 s48, s48, s40
	v_add_f32_e32 v161, 1.0, v161
	v_rcp_f32_e32 v161, v161
	s_addc_u32 s49, s49, s41
	v_fma_f32 v162, v161, -2.0, 1.0
	v_sub_f32_e32 v163, v176, v162
	v_fma_f32 v176, v159, v163, v162
	v_fma_f32 v164, |v176|, s17, v113
	v_fma_f32 v165, |v176|, s18, v114
	v_fma_f32 v166, |v176|, s19, v115
	v_lshrrev_b32_e32 v167, 26, v176
	v_min3_u32 v164, v164, v165, v166
	v_bfi_b32 v168, 31, v164, v167
	s_nop 1
	v_mul_u32_u24_dpp v170, v168, v180 quad_perm:[1,2,3,3] row_mask:0xf bank_mask:0xf bound_ctrl:1
	v_mad_u32_u24 v171, v168, v181, v170
	ds_write_b8_d16_hi v184, v171 offset:416
	s_barrier
	global_store_short_d16_hi v185, v176, s[48:49]
	s_waitcnt lgkmcnt(0)
	s_barrier
	ds_read_b64 v[122:123], v105 offset:416
	ds_read_b64 v[124:125], v105 offset:424
	ds_read_b64 v[126:127], v105 offset:432
	ds_read_b64 v[128:129], v105 offset:512
	ds_read_b64 v[130:131], v105 offset:520
	ds_read_b64 v[132:133], v105 offset:528
	s_waitcnt lgkmcnt(3)
	v_mfma_f32_16x16x128_f8f6f4 v[134:137], v[122:127], v[2:7], 0 cbsz:2 blgp:2
	v_mfma_f32_16x16x128_f8f6f4 v[138:141], v[122:127], v[14:19], 0 cbsz:2 blgp:2
	v_mfma_f32_16x16x128_f8f6f4 v[142:145], v[122:127], v[26:31], v[188:191] cbsz:2 blgp:2
	v_mfma_f32_16x16x128_f8f6f4 v[204:207], v[122:127], v[38:43], 0 cbsz:2 blgp:2
	v_mfma_f32_16x16x128_f8f6f4 v[208:211], v[122:127], v[50:55], 0 cbsz:2 blgp:2
	v_mfma_f32_16x16x128_f8f6f4 v[212:215], v[122:127], v[62:67], v[188:191] cbsz:2 blgp:2
	s_waitcnt lgkmcnt(0)
	v_mfma_f32_16x16x128_f8f6f4 v[134:137], v[128:133], v[8:13], v[134:137] cbsz:2 blgp:2
	v_mfma_f32_16x16x128_f8f6f4 v[204:207], v[128:133], v[44:49], v[204:207] cbsz:2 blgp:2
	v_mfma_f32_16x16x128_f8f6f4 v[138:141], v[128:133], v[20:25], v[138:141] cbsz:2 blgp:2
	v_mfma_f32_16x16x128_f8f6f4 v[208:211], v[128:133], v[56:61], v[208:211] cbsz:2 blgp:2
	v_mfma_f32_16x16x128_f8f6f4 v[142:145], v[128:133], v[32:37], v[142:145] cbsz:2 blgp:2
	v_mfma_f32_16x16x128_f8f6f4 v[212:215], v[128:133], v[68:73], v[212:215] cbsz:2 blgp:2
	v_cndmask_b32_e64 v158, v134, v204, s[0:1]
	v_fma_mix_f32 v158, v158, v100, v147 op_sel:[0,0,1] op_sel_hi:[0,0,1]
	v_exp_f32_e32 v158, v158
	v_cndmask_b32_e64 v159, v138, v208, s[0:1]
	v_fma_mix_f32 v159, v159, v101, v151 op_sel:[0,0,1] op_sel_hi:[0,0,1]
	v_exp_f32_e32 v159, v159
	v_fma_f32 v158, v158, v186, v186
	v_rcp_f32_e32 v158, v158
	v_add_f32_e32 v159, 1.0, v159
	v_rcp_f32_e32 v159, v159
	v_cndmask_b32_e64 v160, v142, v212, s[0:1]
	v_fma_mix_f32 v161, v158, v160, v155 op_sel:[0,0,1] op_sel_hi:[0,0,1]
	v_exp_f32_e32 v161, v161
	s_add_u32 s48, s48, s40
	v_add_f32_e32 v161, 1.0, v161
	v_rcp_f32_e32 v161, v161
	s_addc_u32 s49, s49, s41
	v_fma_f32 v162, v161, -2.0, 1.0
	v_sub_f32_e32 v163, v176, v162
	v_fma_f32 v176, v159, v163, v162
	v_fma_f32 v164, |v176|, s17, v113
	v_fma_f32 v165, |v176|, s18, v114
	v_fma_f32 v166, |v176|, s19, v115
	v_lshrrev_b32_e32 v167, 26, v176
	v_min3_u32 v164, v164, v165, v166
	v_bfi_b32 v168, 31, v164, v167
	s_nop 1
	v_mul_u32_u24_dpp v170, v168, v180 quad_perm:[1,2,3,3] row_mask:0xf bank_mask:0xf bound_ctrl:1
	v_mad_u32_u24 v171, v168, v181, v170
	ds_write_b8_d16_hi v184, v171
	s_barrier
	global_store_short_d16_hi v185, v176, s[48:49]
	s_waitcnt lgkmcnt(0)
	s_barrier
	ds_read_b64 v[122:123], v105 offset:0
	ds_read_b64 v[124:125], v105 offset:8
	ds_read_b64 v[126:127], v105 offset:16
	ds_read_b64 v[128:129], v105 offset:96
	ds_read_b64 v[130:131], v105 offset:104
	ds_read_b64 v[132:133], v105 offset:112
	s_waitcnt lgkmcnt(3)
	v_mfma_f32_16x16x128_f8f6f4 v[134:137], v[122:127], v[2:7], 0 cbsz:2 blgp:2
	v_mfma_f32_16x16x128_f8f6f4 v[138:141], v[122:127], v[14:19], 0 cbsz:2 blgp:2
	v_mfma_f32_16x16x128_f8f6f4 v[142:145], v[122:127], v[26:31], v[188:191] cbsz:2 blgp:2
	v_mfma_f32_16x16x128_f8f6f4 v[204:207], v[122:127], v[38:43], 0 cbsz:2 blgp:2
	v_mfma_f32_16x16x128_f8f6f4 v[208:211], v[122:127], v[50:55], 0 cbsz:2 blgp:2
	v_mfma_f32_16x16x128_f8f6f4 v[212:215], v[122:127], v[62:67], v[188:191] cbsz:2 blgp:2
	s_waitcnt lgkmcnt(0)
	v_mfma_f32_16x16x128_f8f6f4 v[134:137], v[128:133], v[8:13], v[134:137] cbsz:2 blgp:2
	v_mfma_f32_16x16x128_f8f6f4 v[204:207], v[128:133], v[44:49], v[204:207] cbsz:2 blgp:2
	v_mfma_f32_16x16x128_f8f6f4 v[138:141], v[128:133], v[20:25], v[138:141] cbsz:2 blgp:2
	v_mfma_f32_16x16x128_f8f6f4 v[208:211], v[128:133], v[56:61], v[208:211] cbsz:2 blgp:2
	v_mfma_f32_16x16x128_f8f6f4 v[142:145], v[128:133], v[32:37], v[142:145] cbsz:2 blgp:2
	v_mfma_f32_16x16x128_f8f6f4 v[212:215], v[128:133], v[68:73], v[212:215] cbsz:2 blgp:2
	v_cndmask_b32_e64 v158, v134, v204, s[0:1]
	v_fma_mix_f32 v158, v158, v100, v148 op_sel_hi:[0,0,1]
	v_exp_f32_e32 v158, v158
	v_cndmask_b32_e64 v159, v138, v208, s[0:1]
	v_fma_mix_f32 v159, v159, v101, v152 op_sel_hi:[0,0,1]
	v_exp_f32_e32 v159, v159
	v_fma_f32 v158, v158, v186, v186
	v_rcp_f32_e32 v158, v158
	v_add_f32_e32 v159, 1.0, v159
	v_rcp_f32_e32 v159, v159
	v_cndmask_b32_e64 v160, v142, v212, s[0:1]
	v_fma_mix_f32 v161, v158, v160, v156 op_sel_hi:[0,0,1]
	v_exp_f32_e32 v161, v161
	s_add_u32 s48, s48, s40
	v_add_f32_e32 v161, 1.0, v161
	v_rcp_f32_e32 v161, v161
	s_addc_u32 s49, s49, s41
	v_fma_f32 v162, v161, -2.0, 1.0
	v_sub_f32_e32 v163, v176, v162
	v_fma_f32 v176, v159, v163, v162
	v_fma_f32 v164, |v176|, s17, v113
	v_fma_f32 v165, |v176|, s18, v114
	v_fma_f32 v166, |v176|, s19, v115
	v_lshrrev_b32_e32 v167, 26, v176
	v_min3_u32 v164, v164, v165, v166
	v_bfi_b32 v168, 31, v164, v167
	s_nop 1
	v_mul_u32_u24_dpp v170, v168, v180 quad_perm:[1,2,3,3] row_mask:0xf bank_mask:0xf bound_ctrl:1
	v_mad_u32_u24 v171, v168, v181, v170
	ds_write_b8_d16_hi v184, v171 offset:416
	s_barrier
	global_store_short_d16_hi v185, v176, s[48:49]
	s_waitcnt lgkmcnt(0)
	s_barrier
	ds_read_b64 v[122:123], v105 offset:416
	ds_read_b64 v[124:125], v105 offset:424
	ds_read_b64 v[126:127], v105 offset:432
	ds_read_b64 v[128:129], v105 offset:512
	ds_read_b64 v[130:131], v105 offset:520
	ds_read_b64 v[132:133], v105 offset:528
	s_waitcnt lgkmcnt(3)
	v_mfma_f32_16x16x128_f8f6f4 v[134:137], v[122:127], v[2:7], 0 cbsz:2 blgp:2
	v_mfma_f32_16x16x128_f8f6f4 v[138:141], v[122:127], v[14:19], 0 cbsz:2 blgp:2
	v_mfma_f32_16x16x128_f8f6f4 v[142:145], v[122:127], v[26:31], v[188:191] cbsz:2 blgp:2
	v_mfma_f32_16x16x128_f8f6f4 v[204:207], v[122:127], v[38:43], 0 cbsz:2 blgp:2
	v_mfma_f32_16x16x128_f8f6f4 v[208:211], v[122:127], v[50:55], 0 cbsz:2 blgp:2
	v_mfma_f32_16x16x128_f8f6f4 v[212:215], v[122:127], v[62:67], v[188:191] cbsz:2 blgp:2
	s_waitcnt lgkmcnt(0)
	v_mfma_f32_16x16x128_f8f6f4 v[134:137], v[128:133], v[8:13], v[134:137] cbsz:2 blgp:2
	v_mfma_f32_16x16x128_f8f6f4 v[204:207], v[128:133], v[44:49], v[204:207] cbsz:2 blgp:2
	v_mfma_f32_16x16x128_f8f6f4 v[138:141], v[128:133], v[20:25], v[138:141] cbsz:2 blgp:2
	v_mfma_f32_16x16x128_f8f6f4 v[208:211], v[128:133], v[56:61], v[208:211] cbsz:2 blgp:2
	v_mfma_f32_16x16x128_f8f6f4 v[142:145], v[128:133], v[32:37], v[142:145] cbsz:2 blgp:2
	v_mfma_f32_16x16x128_f8f6f4 v[212:215], v[128:133], v[68:73], v[212:215] cbsz:2 blgp:2
	v_cndmask_b32_e64 v158, v134, v204, s[0:1]
	v_fma_mix_f32 v158, v158, v100, v148 op_sel:[0,0,1] op_sel_hi:[0,0,1]
	v_exp_f32_e32 v158, v158
	v_cndmask_b32_e64 v159, v138, v208, s[0:1]
	v_fma_mix_f32 v159, v159, v101, v152 op_sel:[0,0,1] op_sel_hi:[0,0,1]
	v_exp_f32_e32 v159, v159
	v_fma_f32 v158, v158, v186, v186
	v_rcp_f32_e32 v158, v158
	v_add_f32_e32 v159, 1.0, v159
	v_rcp_f32_e32 v159, v159
	v_cndmask_b32_e64 v160, v142, v212, s[0:1]
	v_fma_mix_f32 v161, v158, v160, v156 op_sel:[0,0,1] op_sel_hi:[0,0,1]
	v_exp_f32_e32 v161, v161
	s_add_u32 s48, s48, s40
	v_add_f32_e32 v161, 1.0, v161
	v_rcp_f32_e32 v161, v161
	s_addc_u32 s49, s49, s41
	v_fma_f32 v162, v161, -2.0, 1.0
	v_sub_f32_e32 v163, v176, v162
	v_fma_f32 v176, v159, v163, v162
	v_fma_f32 v164, |v176|, s17, v113
	v_fma_f32 v165, |v176|, s18, v114
	v_fma_f32 v166, |v176|, s19, v115
	v_lshrrev_b32_e32 v167, 26, v176
	v_min3_u32 v164, v164, v165, v166
	v_bfi_b32 v168, 31, v164, v167
	s_nop 1
	v_mul_u32_u24_dpp v170, v168, v180 quad_perm:[1,2,3,3] row_mask:0xf bank_mask:0xf bound_ctrl:1
	v_mad_u32_u24 v171, v168, v181, v170
	ds_write_b8_d16_hi v184, v171
	s_barrier
	global_store_short_d16_hi v185, v176, s[48:49]
	s_waitcnt lgkmcnt(0)
	s_barrier
	ds_read_b64 v[122:123], v105 offset:0
	ds_read_b64 v[124:125], v105 offset:8
	ds_read_b64 v[126:127], v105 offset:16
	ds_read_b64 v[128:129], v105 offset:96
	ds_read_b64 v[130:131], v105 offset:104
	ds_read_b64 v[132:133], v105 offset:112
	s_waitcnt lgkmcnt(3)
	v_mfma_f32_16x16x128_f8f6f4 v[134:137], v[122:127], v[2:7], 0 cbsz:2 blgp:2
	v_mfma_f32_16x16x128_f8f6f4 v[138:141], v[122:127], v[14:19], 0 cbsz:2 blgp:2
	v_mfma_f32_16x16x128_f8f6f4 v[142:145], v[122:127], v[26:31], v[188:191] cbsz:2 blgp:2
	v_mfma_f32_16x16x128_f8f6f4 v[204:207], v[122:127], v[38:43], 0 cbsz:2 blgp:2
	v_mfma_f32_16x16x128_f8f6f4 v[208:211], v[122:127], v[50:55], 0 cbsz:2 blgp:2
	v_mfma_f32_16x16x128_f8f6f4 v[212:215], v[122:127], v[62:67], v[188:191] cbsz:2 blgp:2
	s_waitcnt lgkmcnt(0)
	v_mfma_f32_16x16x128_f8f6f4 v[134:137], v[128:133], v[8:13], v[134:137] cbsz:2 blgp:2
	v_mfma_f32_16x16x128_f8f6f4 v[204:207], v[128:133], v[44:49], v[204:207] cbsz:2 blgp:2
	v_mfma_f32_16x16x128_f8f6f4 v[138:141], v[128:133], v[20:25], v[138:141] cbsz:2 blgp:2
	v_mfma_f32_16x16x128_f8f6f4 v[208:211], v[128:133], v[56:61], v[208:211] cbsz:2 blgp:2
	v_mfma_f32_16x16x128_f8f6f4 v[142:145], v[128:133], v[32:37], v[142:145] cbsz:2 blgp:2
	v_mfma_f32_16x16x128_f8f6f4 v[212:215], v[128:133], v[68:73], v[212:215] cbsz:2 blgp:2
	v_cndmask_b32_e64 v158, v134, v204, s[0:1]
	v_fma_mix_f32 v158, v158, v100, v149 op_sel_hi:[0,0,1]
	v_exp_f32_e32 v158, v158
	v_cndmask_b32_e64 v159, v138, v208, s[0:1]
	v_fma_mix_f32 v159, v159, v101, v153 op_sel_hi:[0,0,1]
	v_exp_f32_e32 v159, v159
	v_fma_f32 v158, v158, v186, v186
	v_rcp_f32_e32 v158, v158
	v_add_f32_e32 v159, 1.0, v159
	v_rcp_f32_e32 v159, v159
	v_cndmask_b32_e64 v160, v142, v212, s[0:1]
	v_fma_mix_f32 v161, v158, v160, v157 op_sel_hi:[0,0,1]
	v_exp_f32_e32 v161, v161
	s_add_u32 s48, s48, s40
	v_add_f32_e32 v161, 1.0, v161
	v_rcp_f32_e32 v161, v161
	s_addc_u32 s49, s49, s41
	v_fma_f32 v162, v161, -2.0, 1.0
	v_sub_f32_e32 v163, v176, v162
	v_fma_f32 v176, v159, v163, v162
	v_fma_f32 v164, |v176|, s17, v113
	v_fma_f32 v165, |v176|, s18, v114
	v_fma_f32 v166, |v176|, s19, v115
	v_lshrrev_b32_e32 v167, 26, v176
	v_min3_u32 v164, v164, v165, v166
	v_bfi_b32 v168, 31, v164, v167
	s_nop 1
	v_mul_u32_u24_dpp v170, v168, v180 quad_perm:[1,2,3,3] row_mask:0xf bank_mask:0xf bound_ctrl:1
	v_mad_u32_u24 v171, v168, v181, v170
	ds_write_b8_d16_hi v184, v171 offset:416
	s_barrier
	global_store_short_d16_hi v185, v176, s[48:49]
	s_waitcnt lgkmcnt(0)
	s_barrier
	ds_read_b64 v[122:123], v105 offset:416
	ds_read_b64 v[124:125], v105 offset:424
	ds_read_b64 v[126:127], v105 offset:432
	ds_read_b64 v[128:129], v105 offset:512
	ds_read_b64 v[130:131], v105 offset:520
	ds_read_b64 v[132:133], v105 offset:528
	s_add_i32 s44, s44, 16
	s_waitcnt lgkmcnt(3)
	v_mfma_f32_16x16x128_f8f6f4 v[134:137], v[122:127], v[2:7], 0 cbsz:2 blgp:2
	v_mfma_f32_16x16x128_f8f6f4 v[138:141], v[122:127], v[14:19], 0 cbsz:2 blgp:2
	v_mfma_f32_16x16x128_f8f6f4 v[142:145], v[122:127], v[26:31], v[188:191] cbsz:2 blgp:2
	v_mfma_f32_16x16x128_f8f6f4 v[204:207], v[122:127], v[38:43], 0 cbsz:2 blgp:2
	v_mfma_f32_16x16x128_f8f6f4 v[208:211], v[122:127], v[50:55], 0 cbsz:2 blgp:2
	v_mfma_f32_16x16x128_f8f6f4 v[212:215], v[122:127], v[62:67], v[188:191] cbsz:2 blgp:2
	s_waitcnt lgkmcnt(0)
	v_mfma_f32_16x16x128_f8f6f4 v[134:137], v[128:133], v[8:13], v[134:137] cbsz:2 blgp:2
	v_mfma_f32_16x16x128_f8f6f4 v[204:207], v[128:133], v[44:49], v[204:207] cbsz:2 blgp:2
	v_mfma_f32_16x16x128_f8f6f4 v[138:141], v[128:133], v[20:25], v[138:141] cbsz:2 blgp:2
	v_mfma_f32_16x16x128_f8f6f4 v[208:211], v[128:133], v[56:61], v[208:211] cbsz:2 blgp:2
	v_mfma_f32_16x16x128_f8f6f4 v[142:145], v[128:133], v[32:37], v[142:145] cbsz:2 blgp:2
	v_mfma_f32_16x16x128_f8f6f4 v[212:215], v[128:133], v[68:73], v[212:215] cbsz:2 blgp:2
	v_cndmask_b32_e64 v158, v134, v204, s[0:1]
	v_fma_mix_f32 v158, v158, v100, v149 op_sel:[0,0,1] op_sel_hi:[0,0,1]
	v_exp_f32_e32 v158, v158
	v_cndmask_b32_e64 v159, v138, v208, s[0:1]
	v_fma_mix_f32 v159, v159, v101, v153 op_sel:[0,0,1] op_sel_hi:[0,0,1]
	v_exp_f32_e32 v159, v159
	v_fma_f32 v158, v158, v186, v186
	v_rcp_f32_e32 v158, v158
	v_add_f32_e32 v159, 1.0, v159
	v_rcp_f32_e32 v159, v159
	v_cndmask_b32_e64 v160, v142, v212, s[0:1]
	v_fma_mix_f32 v161, v158, v160, v157 op_sel:[0,0,1] op_sel_hi:[0,0,1]
	v_exp_f32_e32 v161, v161
	s_add_u32 s48, s48, s40
	v_add_f32_e32 v161, 1.0, v161
	v_rcp_f32_e32 v161, v161
	s_addc_u32 s49, s49, s41
	v_fma_f32 v162, v161, -2.0, 1.0
	v_sub_f32_e32 v163, v176, v162
	v_fma_f32 v176, v159, v163, v162
	v_fma_f32 v164, |v176|, s17, v113
	v_fma_f32 v165, |v176|, s18, v114
	v_fma_f32 v166, |v176|, s19, v115
	v_lshrrev_b32_e32 v167, 26, v176
	v_min3_u32 v164, v164, v165, v166
	v_bfi_b32 v168, 31, v164, v167
	s_nop 1
	v_mul_u32_u24_dpp v170, v168, v180 quad_perm:[1,2,3,3] row_mask:0xf bank_mask:0xf bound_ctrl:1
	v_mad_u32_u24 v171, v168, v181, v170
	ds_write_b8_d16_hi v184, v171
	s_barrier
	global_store_short_d16_hi v185, v176, s[48:49]
	s_cmp_lt_i32 s44, s45
	s_waitcnt lgkmcnt(0)
	s_barrier
	s_cbranch_scc1 .Lscan_loop_b_f2
